# speedup vs baseline: 1.0274x; 1.0117x over previous
.Lpf_common:
	s_mul_i32 s8, s11, 0x880
	s_mul_hi_u32 s24, s11, 0x880
	s_add_u32 s12, s12, s8
	s_addc_u32 s13, s13, s24
	s_lshl_b32 s8, s21, 10
	s_lshl_b32 s24, s5, 7
	s_add_u32 s8, s8, s24
	s_mul_i32 s8, s8, 0x880
	s_add_u32 s6, s30, s8
	s_addc_u32 s7, s31, 0
	s_mov_b32 s4, s12
	s_mov_b32 s5, s13
	s_and_b32 s24, s18, 1
	s_lshr_b32 s25, s18, 1
	s_lshr_b32 s26, s2, 3
	s_and_b32 s26, s26, 7
	s_lshl_b32 s26, s26, 1
	s_add_u32 s26, s26, s24
	s_lshl_b32 s27, s9, 4
	s_add_u32 s27, s27, s26
	s_lshl_b32 s28, s18, 10
	s_lshl_b32 s8, s26, 8
	s_add_u32 s14, s14, s8
	s_addc_u32 s15, s15, 0
	v_lshrrev_b32_e32 v5, 3, v1
	v_lshl_add_u32 v5, v2, 3, v5
	v_mul_u32_u24_e32 v5, 0x880, v5
	v_and_b32_e32 v6, 7, v1
	v_lshrrev_b32_e32 v7, 4, v1
	v_and_b32_e32 v8, 1, v2
	v_lshl_or_b32 v7, v8, 2, v7
	v_xor_b32_e32 v6, v6, v7
	v_lshl_add_u32 v10, v6, 4, v5
	v_add_u32_e32 v11, 0x22000, v10
	v_add_u32_e32 v12, 0x44000, v10
	v_add_u32_e32 v13, 0x66000, v10
	v_lshrrev_b32_e32 v5, 1, v3
	v_xor_b32_e32 v6, v4, v5
	v_lshlrev_b32_e32 v6, 4, v6
	v_or_b32_e32 v7, 4, v4
	v_xor_b32_e32 v7, v7, v5
	v_lshlrev_b32_e32 v7, 4, v7
	v_lshrrev_b32_e32 v9, 1, v2
	v_lshl_add_u32 v9, v9, 6, v3
	v_lshlrev_b32_e32 v9, 7, v9
	v_add_u32_e32 v14, v9, v6
	v_add_u32_e32 v15, v9, v7
	v_lshl_add_u32 v9, v8, 6, v3
	v_lshlrev_b32_e32 v9, 7, v9
	v_add_u32_e32 v9, 0x8000, v9
	v_add_u32_e32 v16, v9, v6
	v_add_u32_e32 v17, v9, v7
	v_add_u32_e32 v18, 0x18000, v14
	v_add_u32_e32 v19, 0x18000, v15
	v_add_u32_e32 v20, 0x18000, v16
	v_add_u32_e32 v21, 0x18000, v17
	v_and_b32_e32 v5, 1, v4
	v_lshl_add_u32 v5, v5, 5, v3
	v_lshlrev_b32_e32 v5, 4, v5
	v_lshrrev_b32_e32 v6, 1, v4
	v_lshl_add_u32 v22, v6, 3, v5
	v_add_u32_e32 v23, 0x1000, v22
	s_cmp_eq_u32 s21, 2
	s_cbranch_scc1 .Lpf_v
	v_lshlrev_b32_e32 v5, 4, v4
	global_load_dwordx4 v[24:27], v5, s[14:15] offset:0
	global_load_dwordx4 v[28:31], v5, s[14:15] offset:64
	global_load_dwordx4 v[32:35], v5, s[14:15] offset:128
	global_load_dwordx4 v[36:39], v5, s[14:15] offset:192
	global_load_dwordx4 v[40:43], v5, s[16:17] offset:0
	global_load_dwordx4 v[44:47], v5, s[16:17] offset:64
	global_load_dwordx4 v[48:51], v5, s[16:17] offset:128
	global_load_dwordx4 v[52:55], v5, s[16:17] offset:192
	s_lshl_b32 s8, s27, 6
	s_lshr_b32 s24, s10, 5
	s_add_u32 s8, s8, s24
	s_lshl_b32 s24, s25, 1
	s_add_u32 s8, s8, s24
	s_lshl_b32 s8, s8, 12
	s_add_u32 s22, s22, s8
	s_addc_u32 s23, s23, 0
	s_add_u32 m0, s28, 0x0
	s_nop 0
	global_load_lds_dwordx4 v10, s[4:5]
	s_add_u32 m0, s28, 0x2000
	s_nop 0
	global_load_lds_dwordx4 v11, s[4:5]
	s_add_u32 m0, s28, 0x4000
	s_nop 0
	global_load_lds_dwordx4 v12, s[4:5]
	s_add_u32 m0, s28, 0x6000
	s_nop 0
	global_load_lds_dwordx4 v13, s[4:5]
	s_add_u32 s4, s4, s20
	s_addc_u32 s5, s5, 0
	s_add_u32 m0, s28, 0x8000
	s_nop 0
	global_load_lds_dwordx4 v10, s[6:7]
	s_add_u32 m0, s28, 0xa000
	s_nop 0
	global_load_lds_dwordx4 v11, s[6:7]
	s_add_u32 s6, s6, s20
	s_addc_u32 s7, s7, 0
	s_add_u32 m0, s28, 0xc000
	s_nop 0
	global_load_lds_dwordx4 v10, s[4:5]
	s_add_u32 m0, s28, 0xe000
	s_nop 0
	global_load_lds_dwordx4 v11, s[4:5]
	s_add_u32 m0, s28, 0x10000
	s_nop 0
	global_load_lds_dwordx4 v12, s[4:5]
	s_add_u32 m0, s28, 0x12000
	s_nop 0
	global_load_lds_dwordx4 v13, s[4:5]
	s_add_u32 s4, s4, s20
	s_addc_u32 s5, s5, 0
	s_add_u32 m0, s28, 0x14000
	s_nop 0
	global_load_lds_dwordx4 v10, s[6:7]
	s_add_u32 m0, s28, 0x16000
	s_nop 0
	global_load_lds_dwordx4 v11, s[6:7]
	s_add_u32 s6, s6, s20
	s_addc_u32 s7, s7, 0
	s_add_u32 m0, s28, 0x18000
	s_nop 0
	global_load_lds_dwordx4 v10, s[4:5]
	s_add_u32 m0, s28, 0x1a000
	s_nop 0
	global_load_lds_dwordx4 v11, s[4:5]
	s_add_u32 m0, s28, 0x1c000
	s_nop 0
	global_load_lds_dwordx4 v12, s[4:5]
	s_add_u32 m0, s28, 0x1e000
	s_nop 0
	global_load_lds_dwordx4 v13, s[4:5]
	s_add_u32 s4, s4, s20
	s_addc_u32 s5, s5, 0
	s_add_u32 m0, s28, 0x20000
	s_nop 0
	global_load_lds_dwordx4 v10, s[6:7]
	s_add_u32 m0, s28, 0x22000
	s_nop 0
	global_load_lds_dwordx4 v11, s[6:7]
	s_add_u32 s6, s6, s20
	s_addc_u32 s7, s7, 0
	s_waitcnt vmcnt(12)
	s_barrier
	s_waitcnt lgkmcnt(7)
	ds_read_b128 v[120:123], v14
	ds_read_b128 v[136:139], v16
	ds_read_b128 v[140:143], v16 offset:2048
	ds_read_b128 v[144:147], v16 offset:4096
	ds_read_b128 v[148:151], v16 offset:6144
	ds_read_b128 v[124:127], v14 offset:2048
	ds_read_b128 v[128:131], v14 offset:4096
	ds_read_b128 v[132:135], v14 offset:6144
	s_waitcnt lgkmcnt(7)
	ds_read_b128 v[152:155], v15
	ds_read_b128 v[168:171], v17
	ds_read_b128 v[172:175], v17 offset:2048
	ds_read_b128 v[176:179], v17 offset:4096
	ds_read_b128 v[180:183], v17 offset:6144
	ds_read_b128 v[156:159], v15 offset:2048
	ds_read_b128 v[160:163], v15 offset:4096
	ds_read_b128 v[164:167], v15 offset:6144
	s_waitcnt lgkmcnt(14)
	v_mfma_f32_16x16x32_f16 v[56:59], v[136:139], v[120:123], 0
	s_waitcnt lgkmcnt(13)
	v_mfma_f32_16x16x32_f16 v[60:63], v[140:143], v[120:123], 0
	s_waitcnt lgkmcnt(12)
	v_mfma_f32_16x16x32_f16 v[64:67], v[144:147], v[120:123], 0
	s_waitcnt lgkmcnt(11)
	v_mfma_f32_16x16x32_f16 v[68:71], v[148:151], v[120:123], 0
	s_waitcnt lgkmcnt(10)
	v_mfma_f32_16x16x32_f16 v[72:75], v[136:139], v[124:127], 0
	v_mfma_f32_16x16x32_f16 v[76:79], v[140:143], v[124:127], 0
	v_mfma_f32_16x16x32_f16 v[80:83], v[144:147], v[124:127], 0
	v_mfma_f32_16x16x32_f16 v[84:87], v[148:151], v[124:127], 0
	s_waitcnt lgkmcnt(9)
	v_mfma_f32_16x16x32_f16 v[88:91], v[136:139], v[128:131], 0
	v_mfma_f32_16x16x32_f16 v[92:95], v[140:143], v[128:131], 0
	v_mfma_f32_16x16x32_f16 v[96:99], v[144:147], v[128:131], 0
	v_mfma_f32_16x16x32_f16 v[100:103], v[148:151], v[128:131], 0
	s_waitcnt lgkmcnt(8)
	v_mfma_f32_16x16x32_f16 v[104:107], v[136:139], v[132:135], 0
	v_mfma_f32_16x16x32_f16 v[108:111], v[140:143], v[132:135], 0
	v_mfma_f32_16x16x32_f16 v[112:115], v[144:147], v[132:135], 0
	v_mfma_f32_16x16x32_f16 v[116:119], v[148:151], v[132:135], 0
	s_waitcnt vmcnt(6) lgkmcnt(0)
	s_barrier
	s_waitcnt lgkmcnt(7)
	ds_read_b128 v[120:123], v14 offset:49152
	ds_read_b128 v[136:139], v16 offset:49152
	ds_read_b128 v[140:143], v16 offset:51200
	ds_read_b128 v[144:147], v16 offset:53248
	ds_read_b128 v[148:151], v16 offset:55296
	ds_read_b128 v[124:127], v14 offset:51200
	ds_read_b128 v[128:131], v14 offset:53248
	ds_read_b128 v[132:135], v14 offset:55296
	s_waitcnt lgkmcnt(14)
	v_mfma_f32_16x16x32_f16 v[56:59], v[168:171], v[152:155], v[56:59]
	s_waitcnt lgkmcnt(13)
	v_mfma_f32_16x16x32_f16 v[60:63], v[172:175], v[152:155], v[60:63]
	s_add_u32 m0, s28, 0x0
	s_nop 0
	global_load_lds_dwordx4 v10, s[4:5]
	s_waitcnt lgkmcnt(12)
	v_mfma_f32_16x16x32_f16 v[64:67], v[176:179], v[152:155], v[64:67]
	s_waitcnt lgkmcnt(11)
	v_mfma_f32_16x16x32_f16 v[68:71], v[180:183], v[152:155], v[68:71]
	s_waitcnt lgkmcnt(10)
	v_mfma_f32_16x16x32_f16 v[72:75], v[168:171], v[156:159], v[72:75]
	v_mfma_f32_16x16x32_f16 v[76:79], v[172:175], v[156:159], v[76:79]
	v_mfma_f32_16x16x32_f16 v[80:83], v[176:179], v[156:159], v[80:83]
	s_add_u32 m0, s28, 0x2000
	s_nop 0
	global_load_lds_dwordx4 v11, s[4:5]
	v_mfma_f32_16x16x32_f16 v[84:87], v[180:183], v[156:159], v[84:87]
	s_waitcnt lgkmcnt(9)
	v_mfma_f32_16x16x32_f16 v[88:91], v[168:171], v[160:163], v[88:91]
	v_mfma_f32_16x16x32_f16 v[92:95], v[172:175], v[160:163], v[92:95]
	v_mfma_f32_16x16x32_f16 v[96:99], v[176:179], v[160:163], v[96:99]
	v_mfma_f32_16x16x32_f16 v[100:103], v[180:183], v[160:163], v[100:103]
	s_add_u32 m0, s28, 0x4000
	s_nop 0
	global_load_lds_dwordx4 v12, s[4:5]
	s_waitcnt lgkmcnt(8)
	v_mfma_f32_16x16x32_f16 v[104:107], v[168:171], v[164:167], v[104:107]
	v_mfma_f32_16x16x32_f16 v[108:111], v[172:175], v[164:167], v[108:111]
	v_mfma_f32_16x16x32_f16 v[112:115], v[176:179], v[164:167], v[112:115]
	v_mfma_f32_16x16x32_f16 v[116:119], v[180:183], v[164:167], v[116:119]
	s_waitcnt lgkmcnt(7)
	ds_read_b128 v[152:155], v15 offset:49152
	ds_read_b128 v[168:171], v17 offset:49152
	ds_read_b128 v[172:175], v17 offset:51200
	ds_read_b128 v[176:179], v17 offset:53248
	ds_read_b128 v[180:183], v17 offset:55296
	ds_read_b128 v[156:159], v15 offset:51200
	ds_read_b128 v[160:163], v15 offset:53248
	ds_read_b128 v[164:167], v15 offset:55296
	s_waitcnt lgkmcnt(14)
	v_mfma_f32_16x16x32_f16 v[56:59], v[136:139], v[120:123], v[56:59]
	s_waitcnt lgkmcnt(13)
	v_mfma_f32_16x16x32_f16 v[60:63], v[140:143], v[120:123], v[60:63]
	s_add_u32 m0, s28, 0x6000
	s_nop 0
	global_load_lds_dwordx4 v13, s[4:5]
	s_add_u32 s4, s4, s20
	s_addc_u32 s5, s5, 0
	s_waitcnt lgkmcnt(12)
	v_mfma_f32_16x16x32_f16 v[64:67], v[144:147], v[120:123], v[64:67]
	s_waitcnt lgkmcnt(11)
	v_mfma_f32_16x16x32_f16 v[68:71], v[148:151], v[120:123], v[68:71]
	s_waitcnt lgkmcnt(10)
	v_mfma_f32_16x16x32_f16 v[72:75], v[136:139], v[124:127], v[72:75]
	v_mfma_f32_16x16x32_f16 v[76:79], v[140:143], v[124:127], v[76:79]
	v_mfma_f32_16x16x32_f16 v[80:83], v[144:147], v[124:127], v[80:83]
	s_add_u32 m0, s28, 0x8000
	s_nop 0
	global_load_lds_dwordx4 v10, s[6:7]
	v_mfma_f32_16x16x32_f16 v[84:87], v[148:151], v[124:127], v[84:87]
	s_waitcnt lgkmcnt(9)
	v_mfma_f32_16x16x32_f16 v[88:91], v[136:139], v[128:131], v[88:91]
	v_mfma_f32_16x16x32_f16 v[92:95], v[140:143], v[128:131], v[92:95]
	v_mfma_f32_16x16x32_f16 v[96:99], v[144:147], v[128:131], v[96:99]
	v_mfma_f32_16x16x32_f16 v[100:103], v[148:151], v[128:131], v[100:103]
	s_add_u32 m0, s28, 0xa000
	s_nop 0
	global_load_lds_dwordx4 v11, s[6:7]
	s_add_u32 s6, s6, s20
	s_addc_u32 s7, s7, 0
	s_waitcnt lgkmcnt(8)
	v_mfma_f32_16x16x32_f16 v[104:107], v[136:139], v[132:135], v[104:107]
	v_mfma_f32_16x16x32_f16 v[108:111], v[140:143], v[132:135], v[108:111]
	v_mfma_f32_16x16x32_f16 v[112:115], v[144:147], v[132:135], v[112:115]
	v_mfma_f32_16x16x32_f16 v[116:119], v[148:151], v[132:135], v[116:119]
	s_waitcnt vmcnt(6) lgkmcnt(0)
	s_barrier
	s_waitcnt lgkmcnt(7)
	ds_read_b128 v[120:123], v18
	ds_read_b128 v[136:139], v20
	ds_read_b128 v[140:143], v20 offset:2048
	ds_read_b128 v[144:147], v20 offset:4096
	ds_read_b128 v[148:151], v20 offset:6144
	ds_read_b128 v[124:127], v18 offset:2048
	ds_read_b128 v[128:131], v18 offset:4096
	ds_read_b128 v[132:135], v18 offset:6144
	s_waitcnt lgkmcnt(14)
	v_mfma_f32_16x16x32_f16 v[56:59], v[168:171], v[152:155], v[56:59]
	s_waitcnt lgkmcnt(13)
	v_mfma_f32_16x16x32_f16 v[60:63], v[172:175], v[152:155], v[60:63]
	s_add_u32 m0, s28, 0xc000
	s_nop 0
	global_load_lds_dwordx4 v10, s[4:5]
	s_waitcnt lgkmcnt(12)
	v_mfma_f32_16x16x32_f16 v[64:67], v[176:179], v[152:155], v[64:67]
	s_waitcnt lgkmcnt(11)
	v_mfma_f32_16x16x32_f16 v[68:71], v[180:183], v[152:155], v[68:71]
	s_waitcnt lgkmcnt(10)
	v_mfma_f32_16x16x32_f16 v[72:75], v[168:171], v[156:159], v[72:75]
	v_mfma_f32_16x16x32_f16 v[76:79], v[172:175], v[156:159], v[76:79]
	v_mfma_f32_16x16x32_f16 v[80:83], v[176:179], v[156:159], v[80:83]
	s_add_u32 m0, s28, 0xe000
	s_nop 0
	global_load_lds_dwordx4 v11, s[4:5]
	v_mfma_f32_16x16x32_f16 v[84:87], v[180:183], v[156:159], v[84:87]
	s_waitcnt lgkmcnt(9)
	v_mfma_f32_16x16x32_f16 v[88:91], v[168:171], v[160:163], v[88:91]
	v_mfma_f32_16x16x32_f16 v[92:95], v[172:175], v[160:163], v[92:95]
	v_mfma_f32_16x16x32_f16 v[96:99], v[176:179], v[160:163], v[96:99]
	v_mfma_f32_16x16x32_f16 v[100:103], v[180:183], v[160:163], v[100:103]
	s_add_u32 m0, s28, 0x10000
	s_nop 0
	global_load_lds_dwordx4 v12, s[4:5]
	s_waitcnt lgkmcnt(8)
	v_mfma_f32_16x16x32_f16 v[104:107], v[168:171], v[164:167], v[104:107]
	v_mfma_f32_16x16x32_f16 v[108:111], v[172:175], v[164:167], v[108:111]
	v_mfma_f32_16x16x32_f16 v[112:115], v[176:179], v[164:167], v[112:115]
	v_mfma_f32_16x16x32_f16 v[116:119], v[180:183], v[164:167], v[116:119]
	s_waitcnt lgkmcnt(7)
	ds_read_b128 v[152:155], v19
	ds_read_b128 v[168:171], v21
	ds_read_b128 v[172:175], v21 offset:2048
	ds_read_b128 v[176:179], v21 offset:4096
	ds_read_b128 v[180:183], v21 offset:6144
	ds_read_b128 v[156:159], v19 offset:2048
	ds_read_b128 v[160:163], v19 offset:4096
	ds_read_b128 v[164:167], v19 offset:6144
	s_waitcnt lgkmcnt(14)
	v_mfma_f32_16x16x32_f16 v[56:59], v[136:139], v[120:123], v[56:59]
	s_waitcnt lgkmcnt(13)
	v_mfma_f32_16x16x32_f16 v[60:63], v[140:143], v[120:123], v[60:63]
	s_add_u32 m0, s28, 0x12000
	s_nop 0
	global_load_lds_dwordx4 v13, s[4:5]
	s_add_u32 s4, s4, s20
	s_addc_u32 s5, s5, 0
	s_waitcnt lgkmcnt(12)
	v_mfma_f32_16x16x32_f16 v[64:67], v[144:147], v[120:123], v[64:67]
	s_waitcnt lgkmcnt(11)
	v_mfma_f32_16x16x32_f16 v[68:71], v[148:151], v[120:123], v[68:71]
	s_waitcnt lgkmcnt(10)
	v_mfma_f32_16x16x32_f16 v[72:75], v[136:139], v[124:127], v[72:75]
	v_mfma_f32_16x16x32_f16 v[76:79], v[140:143], v[124:127], v[76:79]
	v_mfma_f32_16x16x32_f16 v[80:83], v[144:147], v[124:127], v[80:83]
	s_add_u32 m0, s28, 0x14000
	s_nop 0
	global_load_lds_dwordx4 v10, s[6:7]
	v_mfma_f32_16x16x32_f16 v[84:87], v[148:151], v[124:127], v[84:87]
	s_waitcnt lgkmcnt(9)
	v_mfma_f32_16x16x32_f16 v[88:91], v[136:139], v[128:131], v[88:91]
	v_mfma_f32_16x16x32_f16 v[92:95], v[140:143], v[128:131], v[92:95]
	v_mfma_f32_16x16x32_f16 v[96:99], v[144:147], v[128:131], v[96:99]
	v_mfma_f32_16x16x32_f16 v[100:103], v[148:151], v[128:131], v[100:103]
	s_add_u32 m0, s28, 0x16000
	s_nop 0
	global_load_lds_dwordx4 v11, s[6:7]
	s_add_u32 s6, s6, s20
	s_addc_u32 s7, s7, 0
	s_waitcnt lgkmcnt(8)
	v_mfma_f32_16x16x32_f16 v[104:107], v[136:139], v[132:135], v[104:107]
	v_mfma_f32_16x16x32_f16 v[108:111], v[140:143], v[132:135], v[108:111]
	v_mfma_f32_16x16x32_f16 v[112:115], v[144:147], v[132:135], v[112:115]
	v_mfma_f32_16x16x32_f16 v[116:119], v[148:151], v[132:135], v[116:119]
	s_waitcnt vmcnt(6) lgkmcnt(0)
	s_barrier
	s_waitcnt lgkmcnt(7)
	ds_read_b128 v[120:123], v14
	ds_read_b128 v[136:139], v16
	ds_read_b128 v[140:143], v16 offset:2048
	ds_read_b128 v[144:147], v16 offset:4096
	ds_read_b128 v[148:151], v16 offset:6144
	ds_read_b128 v[124:127], v14 offset:2048
	ds_read_b128 v[128:131], v14 offset:4096
	ds_read_b128 v[132:135], v14 offset:6144
	s_waitcnt lgkmcnt(14)
	v_mfma_f32_16x16x32_f16 v[56:59], v[168:171], v[152:155], v[56:59]
	s_waitcnt lgkmcnt(13)
	v_mfma_f32_16x16x32_f16 v[60:63], v[172:175], v[152:155], v[60:63]
	s_add_u32 m0, s28, 0x18000
	s_nop 0
	global_load_lds_dwordx4 v10, s[4:5]
	s_waitcnt lgkmcnt(12)
	v_mfma_f32_16x16x32_f16 v[64:67], v[176:179], v[152:155], v[64:67]
	s_waitcnt lgkmcnt(11)
	v_mfma_f32_16x16x32_f16 v[68:71], v[180:183], v[152:155], v[68:71]
	s_waitcnt lgkmcnt(10)
	v_mfma_f32_16x16x32_f16 v[72:75], v[168:171], v[156:159], v[72:75]
	v_mfma_f32_16x16x32_f16 v[76:79], v[172:175], v[156:159], v[76:79]
	v_mfma_f32_16x16x32_f16 v[80:83], v[176:179], v[156:159], v[80:83]
	s_add_u32 m0, s28, 0x1a000
	s_nop 0
	global_load_lds_dwordx4 v11, s[4:5]
	v_mfma_f32_16x16x32_f16 v[84:87], v[180:183], v[156:159], v[84:87]
	s_waitcnt lgkmcnt(9)
	v_mfma_f32_16x16x32_f16 v[88:91], v[168:171], v[160:163], v[88:91]
	v_mfma_f32_16x16x32_f16 v[92:95], v[172:175], v[160:163], v[92:95]
	v_mfma_f32_16x16x32_f16 v[96:99], v[176:179], v[160:163], v[96:99]
	v_mfma_f32_16x16x32_f16 v[100:103], v[180:183], v[160:163], v[100:103]
	s_add_u32 m0, s28, 0x1c000
	s_nop 0
	global_load_lds_dwordx4 v12, s[4:5]
	s_waitcnt lgkmcnt(8)
	v_mfma_f32_16x16x32_f16 v[104:107], v[168:171], v[164:167], v[104:107]
	v_mfma_f32_16x16x32_f16 v[108:111], v[172:175], v[164:167], v[108:111]
	v_mfma_f32_16x16x32_f16 v[112:115], v[176:179], v[164:167], v[112:115]
	v_mfma_f32_16x16x32_f16 v[116:119], v[180:183], v[164:167], v[116:119]
	s_waitcnt lgkmcnt(7)
	ds_read_b128 v[152:155], v15
	ds_read_b128 v[168:171], v17
	ds_read_b128 v[172:175], v17 offset:2048
	ds_read_b128 v[176:179], v17 offset:4096
	ds_read_b128 v[180:183], v17 offset:6144
	ds_read_b128 v[156:159], v15 offset:2048
	ds_read_b128 v[160:163], v15 offset:4096
	ds_read_b128 v[164:167], v15 offset:6144
	s_waitcnt lgkmcnt(14)
	v_mfma_f32_16x16x32_f16 v[56:59], v[136:139], v[120:123], v[56:59]
	s_waitcnt lgkmcnt(13)
	v_mfma_f32_16x16x32_f16 v[60:63], v[140:143], v[120:123], v[60:63]
	s_add_u32 m0, s28, 0x1e000
	s_nop 0
	global_load_lds_dwordx4 v13, s[4:5]
	s_add_u32 s4, s4, s20
	s_addc_u32 s5, s5, 0
	s_waitcnt lgkmcnt(12)
	v_mfma_f32_16x16x32_f16 v[64:67], v[144:147], v[120:123], v[64:67]
	s_waitcnt lgkmcnt(11)
	v_mfma_f32_16x16x32_f16 v[68:71], v[148:151], v[120:123], v[68:71]
	s_waitcnt lgkmcnt(10)
	v_mfma_f32_16x16x32_f16 v[72:75], v[136:139], v[124:127], v[72:75]
	v_mfma_f32_16x16x32_f16 v[76:79], v[140:143], v[124:127], v[76:79]
	v_mfma_f32_16x16x32_f16 v[80:83], v[144:147], v[124:127], v[80:83]
	s_add_u32 m0, s28, 0x20000
	s_nop 0
	global_load_lds_dwordx4 v10, s[6:7]
	v_mfma_f32_16x16x32_f16 v[84:87], v[148:151], v[124:127], v[84:87]
	s_waitcnt lgkmcnt(9)
	v_mfma_f32_16x16x32_f16 v[88:91], v[136:139], v[128:131], v[88:91]
	v_mfma_f32_16x16x32_f16 v[92:95], v[140:143], v[128:131], v[92:95]
	v_mfma_f32_16x16x32_f16 v[96:99], v[144:147], v[128:131], v[96:99]
	v_mfma_f32_16x16x32_f16 v[100:103], v[148:151], v[128:131], v[100:103]
	s_add_u32 m0, s28, 0x22000
	s_nop 0
	global_load_lds_dwordx4 v11, s[6:7]
	s_add_u32 s6, s6, s20
	s_addc_u32 s7, s7, 0
	s_waitcnt lgkmcnt(8)
	v_mfma_f32_16x16x32_f16 v[104:107], v[136:139], v[132:135], v[104:107]
	v_mfma_f32_16x16x32_f16 v[108:111], v[140:143], v[132:135], v[108:111]
	v_mfma_f32_16x16x32_f16 v[112:115], v[144:147], v[132:135], v[112:115]
	v_mfma_f32_16x16x32_f16 v[116:119], v[148:151], v[132:135], v[116:119]
	s_waitcnt vmcnt(6) lgkmcnt(0)
	s_barrier
	s_waitcnt lgkmcnt(7)
	ds_read_b128 v[120:123], v14 offset:49152
	ds_read_b128 v[136:139], v16 offset:49152
	ds_read_b128 v[140:143], v16 offset:51200
	ds_read_b128 v[144:147], v16 offset:53248
	ds_read_b128 v[148:151], v16 offset:55296
	ds_read_b128 v[124:127], v14 offset:51200
	ds_read_b128 v[128:131], v14 offset:53248
	ds_read_b128 v[132:135], v14 offset:55296
	s_waitcnt lgkmcnt(14)
	v_mfma_f32_16x16x32_f16 v[56:59], v[168:171], v[152:155], v[56:59]
	s_waitcnt lgkmcnt(13)
	v_mfma_f32_16x16x32_f16 v[60:63], v[172:175], v[152:155], v[60:63]
	s_add_u32 m0, s28, 0x0
	s_nop 0
	global_load_lds_dwordx4 v10, s[4:5]
	s_waitcnt lgkmcnt(12)
	v_mfma_f32_16x16x32_f16 v[64:67], v[176:179], v[152:155], v[64:67]
	s_waitcnt lgkmcnt(11)
	v_mfma_f32_16x16x32_f16 v[68:71], v[180:183], v[152:155], v[68:71]
	s_waitcnt lgkmcnt(10)
	v_mfma_f32_16x16x32_f16 v[72:75], v[168:171], v[156:159], v[72:75]
	v_mfma_f32_16x16x32_f16 v[76:79], v[172:175], v[156:159], v[76:79]
	v_mfma_f32_16x16x32_f16 v[80:83], v[176:179], v[156:159], v[80:83]
	s_add_u32 m0, s28, 0x2000
	s_nop 0
	global_load_lds_dwordx4 v11, s[4:5]
	v_mfma_f32_16x16x32_f16 v[84:87], v[180:183], v[156:159], v[84:87]
	s_waitcnt lgkmcnt(9)
	v_mfma_f32_16x16x32_f16 v[88:91], v[168:171], v[160:163], v[88:91]
	v_mfma_f32_16x16x32_f16 v[92:95], v[172:175], v[160:163], v[92:95]
	v_mfma_f32_16x16x32_f16 v[96:99], v[176:179], v[160:163], v[96:99]
	v_mfma_f32_16x16x32_f16 v[100:103], v[180:183], v[160:163], v[100:103]
	s_add_u32 m0, s28, 0x4000
	s_nop 0
	global_load_lds_dwordx4 v12, s[4:5]
	s_waitcnt lgkmcnt(8)
	v_mfma_f32_16x16x32_f16 v[104:107], v[168:171], v[164:167], v[104:107]
	v_mfma_f32_16x16x32_f16 v[108:111], v[172:175], v[164:167], v[108:111]
	v_mfma_f32_16x16x32_f16 v[112:115], v[176:179], v[164:167], v[112:115]
	v_mfma_f32_16x16x32_f16 v[116:119], v[180:183], v[164:167], v[116:119]
	s_waitcnt lgkmcnt(7)
	ds_read_b128 v[152:155], v15 offset:49152
	ds_read_b128 v[168:171], v17 offset:49152
	ds_read_b128 v[172:175], v17 offset:51200
	ds_read_b128 v[176:179], v17 offset:53248
	ds_read_b128 v[180:183], v17 offset:55296
	ds_read_b128 v[156:159], v15 offset:51200
	ds_read_b128 v[160:163], v15 offset:53248
	ds_read_b128 v[164:167], v15 offset:55296
	s_waitcnt lgkmcnt(14)
	v_mfma_f32_16x16x32_f16 v[56:59], v[136:139], v[120:123], v[56:59]
	s_waitcnt lgkmcnt(13)
	v_mfma_f32_16x16x32_f16 v[60:63], v[140:143], v[120:123], v[60:63]
	s_add_u32 m0, s28, 0x6000
	s_nop 0
	global_load_lds_dwordx4 v13, s[4:5]
	s_add_u32 s4, s4, s20
	s_addc_u32 s5, s5, 0
	s_waitcnt lgkmcnt(12)
	v_mfma_f32_16x16x32_f16 v[64:67], v[144:147], v[120:123], v[64:67]
	s_waitcnt lgkmcnt(11)
	v_mfma_f32_16x16x32_f16 v[68:71], v[148:151], v[120:123], v[68:71]
	s_waitcnt lgkmcnt(10)
	v_mfma_f32_16x16x32_f16 v[72:75], v[136:139], v[124:127], v[72:75]
	v_mfma_f32_16x16x32_f16 v[76:79], v[140:143], v[124:127], v[76:79]
	v_mfma_f32_16x16x32_f16 v[80:83], v[144:147], v[124:127], v[80:83]
	s_add_u32 m0, s28, 0x8000
	s_nop 0
	global_load_lds_dwordx4 v10, s[6:7]
	v_mfma_f32_16x16x32_f16 v[84:87], v[148:151], v[124:127], v[84:87]
	s_waitcnt lgkmcnt(9)
	v_mfma_f32_16x16x32_f16 v[88:91], v[136:139], v[128:131], v[88:91]
	v_mfma_f32_16x16x32_f16 v[92:95], v[140:143], v[128:131], v[92:95]
	v_mfma_f32_16x16x32_f16 v[96:99], v[144:147], v[128:131], v[96:99]
	v_mfma_f32_16x16x32_f16 v[100:103], v[148:151], v[128:131], v[100:103]
	s_add_u32 m0, s28, 0xa000
	s_nop 0
	global_load_lds_dwordx4 v11, s[6:7]
	s_add_u32 s6, s6, s20
	s_addc_u32 s7, s7, 0
	s_waitcnt lgkmcnt(8)
	v_mfma_f32_16x16x32_f16 v[104:107], v[136:139], v[132:135], v[104:107]
	v_mfma_f32_16x16x32_f16 v[108:111], v[140:143], v[132:135], v[108:111]
	v_mfma_f32_16x16x32_f16 v[112:115], v[144:147], v[132:135], v[112:115]
	v_mfma_f32_16x16x32_f16 v[116:119], v[148:151], v[132:135], v[116:119]
	s_waitcnt vmcnt(6) lgkmcnt(0)
	s_barrier
	s_waitcnt lgkmcnt(7)
	ds_read_b128 v[120:123], v18
	ds_read_b128 v[136:139], v20
	ds_read_b128 v[140:143], v20 offset:2048
	ds_read_b128 v[144:147], v20 offset:4096
	ds_read_b128 v[148:151], v20 offset:6144
	ds_read_b128 v[124:127], v18 offset:2048
	ds_read_b128 v[128:131], v18 offset:4096
	ds_read_b128 v[132:135], v18 offset:6144
	s_waitcnt lgkmcnt(14)
	v_mfma_f32_16x16x32_f16 v[56:59], v[168:171], v[152:155], v[56:59]
	s_waitcnt lgkmcnt(13)
	v_mfma_f32_16x16x32_f16 v[60:63], v[172:175], v[152:155], v[60:63]
	s_add_u32 m0, s28, 0xc000
	s_nop 0
	global_load_lds_dwordx4 v10, s[4:5]
	s_waitcnt lgkmcnt(12)
	v_mfma_f32_16x16x32_f16 v[64:67], v[176:179], v[152:155], v[64:67]
	s_waitcnt lgkmcnt(11)
	v_mfma_f32_16x16x32_f16 v[68:71], v[180:183], v[152:155], v[68:71]
	s_waitcnt lgkmcnt(10)
	v_mfma_f32_16x16x32_f16 v[72:75], v[168:171], v[156:159], v[72:75]
	v_mfma_f32_16x16x32_f16 v[76:79], v[172:175], v[156:159], v[76:79]
	v_mfma_f32_16x16x32_f16 v[80:83], v[176:179], v[156:159], v[80:83]
	s_add_u32 m0, s28, 0xe000
	s_nop 0
	global_load_lds_dwordx4 v11, s[4:5]
	v_mfma_f32_16x16x32_f16 v[84:87], v[180:183], v[156:159], v[84:87]
	s_waitcnt lgkmcnt(9)
	v_mfma_f32_16x16x32_f16 v[88:91], v[168:171], v[160:163], v[88:91]
	v_mfma_f32_16x16x32_f16 v[92:95], v[172:175], v[160:163], v[92:95]
	v_mfma_f32_16x16x32_f16 v[96:99], v[176:179], v[160:163], v[96:99]
	v_mfma_f32_16x16x32_f16 v[100:103], v[180:183], v[160:163], v[100:103]
	s_add_u32 m0, s28, 0x10000
	s_nop 0
	global_load_lds_dwordx4 v12, s[4:5]
	s_waitcnt lgkmcnt(8)
	v_mfma_f32_16x16x32_f16 v[104:107], v[168:171], v[164:167], v[104:107]
	v_mfma_f32_16x16x32_f16 v[108:111], v[172:175], v[164:167], v[108:111]
	v_mfma_f32_16x16x32_f16 v[112:115], v[176:179], v[164:167], v[112:115]
	v_mfma_f32_16x16x32_f16 v[116:119], v[180:183], v[164:167], v[116:119]
	s_waitcnt lgkmcnt(7)
	ds_read_b128 v[152:155], v19
	ds_read_b128 v[168:171], v21
	ds_read_b128 v[172:175], v21 offset:2048
	ds_read_b128 v[176:179], v21 offset:4096
	ds_read_b128 v[180:183], v21 offset:6144
	ds_read_b128 v[156:159], v19 offset:2048
	ds_read_b128 v[160:163], v19 offset:4096
	ds_read_b128 v[164:167], v19 offset:6144
	s_waitcnt lgkmcnt(14)
	v_mfma_f32_16x16x32_f16 v[56:59], v[136:139], v[120:123], v[56:59]
	s_waitcnt lgkmcnt(13)
	v_mfma_f32_16x16x32_f16 v[60:63], v[140:143], v[120:123], v[60:63]
	s_add_u32 m0, s28, 0x12000
	s_nop 0
	global_load_lds_dwordx4 v13, s[4:5]
	s_add_u32 s4, s4, s20
	s_addc_u32 s5, s5, 0
	s_waitcnt lgkmcnt(12)
	v_mfma_f32_16x16x32_f16 v[64:67], v[144:147], v[120:123], v[64:67]
	s_waitcnt lgkmcnt(11)
	v_mfma_f32_16x16x32_f16 v[68:71], v[148:151], v[120:123], v[68:71]
	s_waitcnt lgkmcnt(10)
	v_mfma_f32_16x16x32_f16 v[72:75], v[136:139], v[124:127], v[72:75]
	v_mfma_f32_16x16x32_f16 v[76:79], v[140:143], v[124:127], v[76:79]
	v_mfma_f32_16x16x32_f16 v[80:83], v[144:147], v[124:127], v[80:83]
	s_add_u32 m0, s28, 0x14000
	s_nop 0
	global_load_lds_dwordx4 v10, s[6:7]
	v_mfma_f32_16x16x32_f16 v[84:87], v[148:151], v[124:127], v[84:87]
	s_waitcnt lgkmcnt(9)
	v_mfma_f32_16x16x32_f16 v[88:91], v[136:139], v[128:131], v[88:91]
	v_mfma_f32_16x16x32_f16 v[92:95], v[140:143], v[128:131], v[92:95]
	v_mfma_f32_16x16x32_f16 v[96:99], v[144:147], v[128:131], v[96:99]
	v_mfma_f32_16x16x32_f16 v[100:103], v[148:151], v[128:131], v[100:103]
	s_add_u32 m0, s28, 0x16000
	s_nop 0
	global_load_lds_dwordx4 v11, s[6:7]
	s_add_u32 s6, s6, s20
	s_addc_u32 s7, s7, 0
	s_waitcnt lgkmcnt(8)
	v_mfma_f32_16x16x32_f16 v[104:107], v[136:139], v[132:135], v[104:107]
	v_mfma_f32_16x16x32_f16 v[108:111], v[140:143], v[132:135], v[108:111]
	v_mfma_f32_16x16x32_f16 v[112:115], v[144:147], v[132:135], v[112:115]
	v_mfma_f32_16x16x32_f16 v[116:119], v[148:151], v[132:135], v[116:119]
	s_waitcnt vmcnt(6) lgkmcnt(0)
	s_barrier
	s_waitcnt lgkmcnt(7)
	ds_read_b128 v[120:123], v14
	ds_read_b128 v[136:139], v16
	ds_read_b128 v[140:143], v16 offset:2048
	ds_read_b128 v[144:147], v16 offset:4096
	ds_read_b128 v[148:151], v16 offset:6144
	ds_read_b128 v[124:127], v14 offset:2048
	ds_read_b128 v[128:131], v14 offset:4096
	ds_read_b128 v[132:135], v14 offset:6144
	s_waitcnt lgkmcnt(14)
	v_mfma_f32_16x16x32_f16 v[56:59], v[168:171], v[152:155], v[56:59]
	s_waitcnt lgkmcnt(13)
	v_mfma_f32_16x16x32_f16 v[60:63], v[172:175], v[152:155], v[60:63]
	s_add_u32 m0, s28, 0x18000
	s_nop 0
	global_load_lds_dwordx4 v10, s[4:5]
	s_waitcnt lgkmcnt(12)
	v_mfma_f32_16x16x32_f16 v[64:67], v[176:179], v[152:155], v[64:67]
	s_waitcnt lgkmcnt(11)
	v_mfma_f32_16x16x32_f16 v[68:71], v[180:183], v[152:155], v[68:71]
	s_waitcnt lgkmcnt(10)
	v_mfma_f32_16x16x32_f16 v[72:75], v[168:171], v[156:159], v[72:75]
	v_mfma_f32_16x16x32_f16 v[76:79], v[172:175], v[156:159], v[76:79]
	v_mfma_f32_16x16x32_f16 v[80:83], v[176:179], v[156:159], v[80:83]
	s_add_u32 m0, s28, 0x1a000
	s_nop 0
	global_load_lds_dwordx4 v11, s[4:5]
	v_mfma_f32_16x16x32_f16 v[84:87], v[180:183], v[156:159], v[84:87]
	s_waitcnt lgkmcnt(9)
	v_mfma_f32_16x16x32_f16 v[88:91], v[168:171], v[160:163], v[88:91]
	v_mfma_f32_16x16x32_f16 v[92:95], v[172:175], v[160:163], v[92:95]
	v_mfma_f32_16x16x32_f16 v[96:99], v[176:179], v[160:163], v[96:99]
	v_mfma_f32_16x16x32_f16 v[100:103], v[180:183], v[160:163], v[100:103]
	s_add_u32 m0, s28, 0x1c000
	s_nop 0
	global_load_lds_dwordx4 v12, s[4:5]
	s_waitcnt lgkmcnt(8)
	v_mfma_f32_16x16x32_f16 v[104:107], v[168:171], v[164:167], v[104:107]
	v_mfma_f32_16x16x32_f16 v[108:111], v[172:175], v[164:167], v[108:111]
	v_mfma_f32_16x16x32_f16 v[112:115], v[176:179], v[164:167], v[112:115]
	v_mfma_f32_16x16x32_f16 v[116:119], v[180:183], v[164:167], v[116:119]
	s_waitcnt lgkmcnt(7)
	ds_read_b128 v[152:155], v15
	ds_read_b128 v[168:171], v17
	ds_read_b128 v[172:175], v17 offset:2048
	ds_read_b128 v[176:179], v17 offset:4096
	ds_read_b128 v[180:183], v17 offset:6144
	ds_read_b128 v[156:159], v15 offset:2048
	ds_read_b128 v[160:163], v15 offset:4096
	ds_read_b128 v[164:167], v15 offset:6144
	s_waitcnt lgkmcnt(14)
	v_mfma_f32_16x16x32_f16 v[56:59], v[136:139], v[120:123], v[56:59]
	s_waitcnt lgkmcnt(13)
	v_mfma_f32_16x16x32_f16 v[60:63], v[140:143], v[120:123], v[60:63]
	s_add_u32 m0, s28, 0x1e000
	s_nop 0
	global_load_lds_dwordx4 v13, s[4:5]
	s_add_u32 s4, s4, s20
	s_addc_u32 s5, s5, 0
	s_waitcnt lgkmcnt(12)
	v_mfma_f32_16x16x32_f16 v[64:67], v[144:147], v[120:123], v[64:67]
	s_waitcnt lgkmcnt(11)
	v_mfma_f32_16x16x32_f16 v[68:71], v[148:151], v[120:123], v[68:71]
	s_waitcnt lgkmcnt(10)
	v_mfma_f32_16x16x32_f16 v[72:75], v[136:139], v[124:127], v[72:75]
	v_mfma_f32_16x16x32_f16 v[76:79], v[140:143], v[124:127], v[76:79]
	v_mfma_f32_16x16x32_f16 v[80:83], v[144:147], v[124:127], v[80:83]
	s_add_u32 m0, s28, 0x20000
	s_nop 0
	global_load_lds_dwordx4 v10, s[6:7]
	v_mfma_f32_16x16x32_f16 v[84:87], v[148:151], v[124:127], v[84:87]
	s_waitcnt lgkmcnt(9)
	v_mfma_f32_16x16x32_f16 v[88:91], v[136:139], v[128:131], v[88:91]
	v_mfma_f32_16x16x32_f16 v[92:95], v[140:143], v[128:131], v[92:95]
	v_mfma_f32_16x16x32_f16 v[96:99], v[144:147], v[128:131], v[96:99]
	v_mfma_f32_16x16x32_f16 v[100:103], v[148:151], v[128:131], v[100:103]
	s_add_u32 m0, s28, 0x22000
	s_nop 0
	global_load_lds_dwordx4 v11, s[6:7]
	s_add_u32 s6, s6, s20
	s_addc_u32 s7, s7, 0
	s_waitcnt lgkmcnt(8)
	v_mfma_f32_16x16x32_f16 v[104:107], v[136:139], v[132:135], v[104:107]
	v_mfma_f32_16x16x32_f16 v[108:111], v[140:143], v[132:135], v[108:111]
	v_mfma_f32_16x16x32_f16 v[112:115], v[144:147], v[132:135], v[112:115]
	v_mfma_f32_16x16x32_f16 v[116:119], v[148:151], v[132:135], v[116:119]
	s_waitcnt vmcnt(6) lgkmcnt(0)
	s_barrier
	s_waitcnt lgkmcnt(7)
	ds_read_b128 v[120:123], v14 offset:49152
	ds_read_b128 v[136:139], v16 offset:49152
	ds_read_b128 v[140:143], v16 offset:51200
	ds_read_b128 v[144:147], v16 offset:53248
	ds_read_b128 v[148:151], v16 offset:55296
	ds_read_b128 v[124:127], v14 offset:51200
	ds_read_b128 v[128:131], v14 offset:53248
	ds_read_b128 v[132:135], v14 offset:55296
	s_waitcnt lgkmcnt(14)
	v_mfma_f32_16x16x32_f16 v[56:59], v[168:171], v[152:155], v[56:59]
	s_waitcnt lgkmcnt(13)
	v_mfma_f32_16x16x32_f16 v[60:63], v[172:175], v[152:155], v[60:63]
	s_add_u32 m0, s28, 0x0
	s_nop 0
	global_load_lds_dwordx4 v10, s[4:5]
	s_waitcnt lgkmcnt(12)
	v_mfma_f32_16x16x32_f16 v[64:67], v[176:179], v[152:155], v[64:67]
	s_waitcnt lgkmcnt(11)
	v_mfma_f32_16x16x32_f16 v[68:71], v[180:183], v[152:155], v[68:71]
	s_waitcnt lgkmcnt(10)
	v_mfma_f32_16x16x32_f16 v[72:75], v[168:171], v[156:159], v[72:75]
	v_mfma_f32_16x16x32_f16 v[76:79], v[172:175], v[156:159], v[76:79]
	v_mfma_f32_16x16x32_f16 v[80:83], v[176:179], v[156:159], v[80:83]
	s_add_u32 m0, s28, 0x2000
	s_nop 0
	global_load_lds_dwordx4 v11, s[4:5]
	v_mfma_f32_16x16x32_f16 v[84:87], v[180:183], v[156:159], v[84:87]
	s_waitcnt lgkmcnt(9)
	v_mfma_f32_16x16x32_f16 v[88:91], v[168:171], v[160:163], v[88:91]
	v_mfma_f32_16x16x32_f16 v[92:95], v[172:175], v[160:163], v[92:95]
	v_mfma_f32_16x16x32_f16 v[96:99], v[176:179], v[160:163], v[96:99]
	v_mfma_f32_16x16x32_f16 v[100:103], v[180:183], v[160:163], v[100:103]
	s_add_u32 m0, s28, 0x4000
	s_nop 0
	global_load_lds_dwordx4 v12, s[4:5]
	s_waitcnt lgkmcnt(8)
	v_mfma_f32_16x16x32_f16 v[104:107], v[168:171], v[164:167], v[104:107]
	v_mfma_f32_16x16x32_f16 v[108:111], v[172:175], v[164:167], v[108:111]
	v_mfma_f32_16x16x32_f16 v[112:115], v[176:179], v[164:167], v[112:115]
	v_mfma_f32_16x16x32_f16 v[116:119], v[180:183], v[164:167], v[116:119]
	s_waitcnt lgkmcnt(7)
	ds_read_b128 v[152:155], v15 offset:49152
	ds_read_b128 v[168:171], v17 offset:49152
	ds_read_b128 v[172:175], v17 offset:51200
	ds_read_b128 v[176:179], v17 offset:53248
	ds_read_b128 v[180:183], v17 offset:55296
	ds_read_b128 v[156:159], v15 offset:51200
	ds_read_b128 v[160:163], v15 offset:53248
	ds_read_b128 v[164:167], v15 offset:55296
	s_waitcnt lgkmcnt(14)
	v_mfma_f32_16x16x32_f16 v[56:59], v[136:139], v[120:123], v[56:59]
	s_waitcnt lgkmcnt(13)
	v_mfma_f32_16x16x32_f16 v[60:63], v[140:143], v[120:123], v[60:63]
	s_add_u32 m0, s28, 0x6000
	s_nop 0
	global_load_lds_dwordx4 v13, s[4:5]
	s_add_u32 s4, s4, s20
	s_addc_u32 s5, s5, 0
	s_waitcnt lgkmcnt(12)
	v_mfma_f32_16x16x32_f16 v[64:67], v[144:147], v[120:123], v[64:67]
	s_waitcnt lgkmcnt(11)
	v_mfma_f32_16x16x32_f16 v[68:71], v[148:151], v[120:123], v[68:71]
	s_waitcnt lgkmcnt(10)
	v_mfma_f32_16x16x32_f16 v[72:75], v[136:139], v[124:127], v[72:75]
	v_mfma_f32_16x16x32_f16 v[76:79], v[140:143], v[124:127], v[76:79]
	v_mfma_f32_16x16x32_f16 v[80:83], v[144:147], v[124:127], v[80:83]
	s_add_u32 m0, s28, 0x8000
	s_nop 0
	global_load_lds_dwordx4 v10, s[6:7]
	v_mfma_f32_16x16x32_f16 v[84:87], v[148:151], v[124:127], v[84:87]
	s_waitcnt lgkmcnt(9)
	v_mfma_f32_16x16x32_f16 v[88:91], v[136:139], v[128:131], v[88:91]
	v_mfma_f32_16x16x32_f16 v[92:95], v[140:143], v[128:131], v[92:95]
	v_mfma_f32_16x16x32_f16 v[96:99], v[144:147], v[128:131], v[96:99]
	v_mfma_f32_16x16x32_f16 v[100:103], v[148:151], v[128:131], v[100:103]
	s_add_u32 m0, s28, 0xa000
	s_nop 0
	global_load_lds_dwordx4 v11, s[6:7]
	s_add_u32 s6, s6, s20
	s_addc_u32 s7, s7, 0
	s_waitcnt lgkmcnt(8)
	v_mfma_f32_16x16x32_f16 v[104:107], v[136:139], v[132:135], v[104:107]
	v_mfma_f32_16x16x32_f16 v[108:111], v[140:143], v[132:135], v[108:111]
	v_mfma_f32_16x16x32_f16 v[112:115], v[144:147], v[132:135], v[112:115]
	v_mfma_f32_16x16x32_f16 v[116:119], v[148:151], v[132:135], v[116:119]
	s_waitcnt vmcnt(6) lgkmcnt(0)
	s_barrier
	s_waitcnt lgkmcnt(7)
	ds_read_b128 v[120:123], v18
	ds_read_b128 v[136:139], v20
	ds_read_b128 v[140:143], v20 offset:2048
	ds_read_b128 v[144:147], v20 offset:4096
	ds_read_b128 v[148:151], v20 offset:6144
	ds_read_b128 v[124:127], v18 offset:2048
	ds_read_b128 v[128:131], v18 offset:4096
	ds_read_b128 v[132:135], v18 offset:6144
	s_waitcnt lgkmcnt(14)
	v_mfma_f32_16x16x32_f16 v[56:59], v[168:171], v[152:155], v[56:59]
	s_waitcnt lgkmcnt(13)
	v_mfma_f32_16x16x32_f16 v[60:63], v[172:175], v[152:155], v[60:63]
	s_add_u32 m0, s28, 0xc000
	s_nop 0
	global_load_lds_dwordx4 v10, s[4:5]
	s_waitcnt lgkmcnt(12)
	v_mfma_f32_16x16x32_f16 v[64:67], v[176:179], v[152:155], v[64:67]
	s_waitcnt lgkmcnt(11)
	v_mfma_f32_16x16x32_f16 v[68:71], v[180:183], v[152:155], v[68:71]
	s_waitcnt lgkmcnt(10)
	v_mfma_f32_16x16x32_f16 v[72:75], v[168:171], v[156:159], v[72:75]
	v_mfma_f32_16x16x32_f16 v[76:79], v[172:175], v[156:159], v[76:79]
	v_mfma_f32_16x16x32_f16 v[80:83], v[176:179], v[156:159], v[80:83]
	s_add_u32 m0, s28, 0xe000
	s_nop 0
	global_load_lds_dwordx4 v11, s[4:5]
	v_mfma_f32_16x16x32_f16 v[84:87], v[180:183], v[156:159], v[84:87]
	s_waitcnt lgkmcnt(9)
	v_mfma_f32_16x16x32_f16 v[88:91], v[168:171], v[160:163], v[88:91]
	v_mfma_f32_16x16x32_f16 v[92:95], v[172:175], v[160:163], v[92:95]
	v_mfma_f32_16x16x32_f16 v[96:99], v[176:179], v[160:163], v[96:99]
	v_mfma_f32_16x16x32_f16 v[100:103], v[180:183], v[160:163], v[100:103]
	s_add_u32 m0, s28, 0x10000
	s_nop 0
	global_load_lds_dwordx4 v12, s[4:5]
	s_waitcnt lgkmcnt(8)
	v_mfma_f32_16x16x32_f16 v[104:107], v[168:171], v[164:167], v[104:107]
	v_mfma_f32_16x16x32_f16 v[108:111], v[172:175], v[164:167], v[108:111]
	v_mfma_f32_16x16x32_f16 v[112:115], v[176:179], v[164:167], v[112:115]
	v_mfma_f32_16x16x32_f16 v[116:119], v[180:183], v[164:167], v[116:119]
	s_waitcnt lgkmcnt(7)
	ds_read_b128 v[152:155], v19
	ds_read_b128 v[168:171], v21
	ds_read_b128 v[172:175], v21 offset:2048
	ds_read_b128 v[176:179], v21 offset:4096
	ds_read_b128 v[180:183], v21 offset:6144
	ds_read_b128 v[156:159], v19 offset:2048
	ds_read_b128 v[160:163], v19 offset:4096
	ds_read_b128 v[164:167], v19 offset:6144
	s_waitcnt lgkmcnt(14)
	v_mfma_f32_16x16x32_f16 v[56:59], v[136:139], v[120:123], v[56:59]
	s_waitcnt lgkmcnt(13)
	v_mfma_f32_16x16x32_f16 v[60:63], v[140:143], v[120:123], v[60:63]
	s_add_u32 m0, s28, 0x12000
	s_nop 0
	global_load_lds_dwordx4 v13, s[4:5]
	s_add_u32 s4, s4, s20
	s_addc_u32 s5, s5, 0
	s_waitcnt lgkmcnt(12)
	v_mfma_f32_16x16x32_f16 v[64:67], v[144:147], v[120:123], v[64:67]
	s_waitcnt lgkmcnt(11)
	v_mfma_f32_16x16x32_f16 v[68:71], v[148:151], v[120:123], v[68:71]
	s_waitcnt lgkmcnt(10)
	v_mfma_f32_16x16x32_f16 v[72:75], v[136:139], v[124:127], v[72:75]
	v_mfma_f32_16x16x32_f16 v[76:79], v[140:143], v[124:127], v[76:79]
	v_mfma_f32_16x16x32_f16 v[80:83], v[144:147], v[124:127], v[80:83]
	s_add_u32 m0, s28, 0x14000
	s_nop 0
	global_load_lds_dwordx4 v10, s[6:7]
	v_mfma_f32_16x16x32_f16 v[84:87], v[148:151], v[124:127], v[84:87]
	s_waitcnt lgkmcnt(9)
	v_mfma_f32_16x16x32_f16 v[88:91], v[136:139], v[128:131], v[88:91]
	v_mfma_f32_16x16x32_f16 v[92:95], v[140:143], v[128:131], v[92:95]
	v_mfma_f32_16x16x32_f16 v[96:99], v[144:147], v[128:131], v[96:99]
	v_mfma_f32_16x16x32_f16 v[100:103], v[148:151], v[128:131], v[100:103]
	s_add_u32 m0, s28, 0x16000
	s_nop 0
	global_load_lds_dwordx4 v11, s[6:7]
	s_add_u32 s6, s6, s20
	s_addc_u32 s7, s7, 0
	s_waitcnt lgkmcnt(8)
	v_mfma_f32_16x16x32_f16 v[104:107], v[136:139], v[132:135], v[104:107]
	v_mfma_f32_16x16x32_f16 v[108:111], v[140:143], v[132:135], v[108:111]
	v_mfma_f32_16x16x32_f16 v[112:115], v[144:147], v[132:135], v[112:115]
	v_mfma_f32_16x16x32_f16 v[116:119], v[148:151], v[132:135], v[116:119]
	s_waitcnt vmcnt(6) lgkmcnt(0)
	s_barrier
	s_waitcnt lgkmcnt(7)
	ds_read_b128 v[120:123], v14
	ds_read_b128 v[136:139], v16
	ds_read_b128 v[140:143], v16 offset:2048
	ds_read_b128 v[144:147], v16 offset:4096
	ds_read_b128 v[148:151], v16 offset:6144
	ds_read_b128 v[124:127], v14 offset:2048
	ds_read_b128 v[128:131], v14 offset:4096
	ds_read_b128 v[132:135], v14 offset:6144
	s_waitcnt lgkmcnt(14)
	v_mfma_f32_16x16x32_f16 v[56:59], v[168:171], v[152:155], v[56:59]
	s_waitcnt lgkmcnt(13)
	v_mfma_f32_16x16x32_f16 v[60:63], v[172:175], v[152:155], v[60:63]
	s_add_u32 m0, s28, 0x18000
	s_nop 0
	global_load_lds_dwordx4 v10, s[4:5]
	s_waitcnt lgkmcnt(12)
	v_mfma_f32_16x16x32_f16 v[64:67], v[176:179], v[152:155], v[64:67]
	s_waitcnt lgkmcnt(11)
	v_mfma_f32_16x16x32_f16 v[68:71], v[180:183], v[152:155], v[68:71]
	s_waitcnt lgkmcnt(10)
	v_mfma_f32_16x16x32_f16 v[72:75], v[168:171], v[156:159], v[72:75]
	v_mfma_f32_16x16x32_f16 v[76:79], v[172:175], v[156:159], v[76:79]
	v_mfma_f32_16x16x32_f16 v[80:83], v[176:179], v[156:159], v[80:83]
	s_add_u32 m0, s28, 0x1a000
	s_nop 0
	global_load_lds_dwordx4 v11, s[4:5]
	v_mfma_f32_16x16x32_f16 v[84:87], v[180:183], v[156:159], v[84:87]
	s_waitcnt lgkmcnt(9)
	v_mfma_f32_16x16x32_f16 v[88:91], v[168:171], v[160:163], v[88:91]
	v_mfma_f32_16x16x32_f16 v[92:95], v[172:175], v[160:163], v[92:95]
	v_mfma_f32_16x16x32_f16 v[96:99], v[176:179], v[160:163], v[96:99]
	v_mfma_f32_16x16x32_f16 v[100:103], v[180:183], v[160:163], v[100:103]
	s_add_u32 m0, s28, 0x1c000
	s_nop 0
	global_load_lds_dwordx4 v12, s[4:5]
	s_waitcnt lgkmcnt(8)
	v_mfma_f32_16x16x32_f16 v[104:107], v[168:171], v[164:167], v[104:107]
	v_mfma_f32_16x16x32_f16 v[108:111], v[172:175], v[164:167], v[108:111]
	v_mfma_f32_16x16x32_f16 v[112:115], v[176:179], v[164:167], v[112:115]
	v_mfma_f32_16x16x32_f16 v[116:119], v[180:183], v[164:167], v[116:119]
	s_waitcnt lgkmcnt(7)
	ds_read_b128 v[152:155], v15
	ds_read_b128 v[168:171], v17
	ds_read_b128 v[172:175], v17 offset:2048
	ds_read_b128 v[176:179], v17 offset:4096
	ds_read_b128 v[180:183], v17 offset:6144
	ds_read_b128 v[156:159], v15 offset:2048
	ds_read_b128 v[160:163], v15 offset:4096
	ds_read_b128 v[164:167], v15 offset:6144
	s_waitcnt lgkmcnt(14)
	v_mfma_f32_16x16x32_f16 v[56:59], v[136:139], v[120:123], v[56:59]
	s_waitcnt lgkmcnt(13)
	v_mfma_f32_16x16x32_f16 v[60:63], v[140:143], v[120:123], v[60:63]
	s_add_u32 m0, s28, 0x1e000
	s_nop 0
	global_load_lds_dwordx4 v13, s[4:5]
	s_add_u32 s4, s4, s20
	s_addc_u32 s5, s5, 0
	s_waitcnt lgkmcnt(12)
	v_mfma_f32_16x16x32_f16 v[64:67], v[144:147], v[120:123], v[64:67]
	s_waitcnt lgkmcnt(11)
	v_mfma_f32_16x16x32_f16 v[68:71], v[148:151], v[120:123], v[68:71]
	s_waitcnt lgkmcnt(10)
	v_mfma_f32_16x16x32_f16 v[72:75], v[136:139], v[124:127], v[72:75]
	v_mfma_f32_16x16x32_f16 v[76:79], v[140:143], v[124:127], v[76:79]
	v_mfma_f32_16x16x32_f16 v[80:83], v[144:147], v[124:127], v[80:83]
	s_add_u32 m0, s28, 0x20000
	s_nop 0
	global_load_lds_dwordx4 v10, s[6:7]
	v_mfma_f32_16x16x32_f16 v[84:87], v[148:151], v[124:127], v[84:87]
	s_waitcnt lgkmcnt(9)
	v_mfma_f32_16x16x32_f16 v[88:91], v[136:139], v[128:131], v[88:91]
	v_mfma_f32_16x16x32_f16 v[92:95], v[140:143], v[128:131], v[92:95]
	v_mfma_f32_16x16x32_f16 v[96:99], v[144:147], v[128:131], v[96:99]
	v_mfma_f32_16x16x32_f16 v[100:103], v[148:151], v[128:131], v[100:103]
	s_add_u32 m0, s28, 0x22000
	s_nop 0
	global_load_lds_dwordx4 v11, s[6:7]
	s_add_u32 s6, s6, s20
	s_addc_u32 s7, s7, 0
	s_waitcnt lgkmcnt(8)
	v_mfma_f32_16x16x32_f16 v[104:107], v[136:139], v[132:135], v[104:107]
	v_mfma_f32_16x16x32_f16 v[108:111], v[140:143], v[132:135], v[108:111]
	v_mfma_f32_16x16x32_f16 v[112:115], v[144:147], v[132:135], v[112:115]
	v_mfma_f32_16x16x32_f16 v[116:119], v[148:151], v[132:135], v[116:119]
	s_waitcnt vmcnt(6) lgkmcnt(0)
	s_barrier
	s_waitcnt lgkmcnt(7)
	ds_read_b128 v[120:123], v14 offset:49152
	ds_read_b128 v[136:139], v16 offset:49152
	ds_read_b128 v[140:143], v16 offset:51200
	ds_read_b128 v[144:147], v16 offset:53248
	ds_read_b128 v[148:151], v16 offset:55296
	ds_read_b128 v[124:127], v14 offset:51200
	ds_read_b128 v[128:131], v14 offset:53248
	ds_read_b128 v[132:135], v14 offset:55296
	s_waitcnt lgkmcnt(14)
	v_mfma_f32_16x16x32_f16 v[56:59], v[168:171], v[152:155], v[56:59]
	s_waitcnt lgkmcnt(13)
	v_mfma_f32_16x16x32_f16 v[60:63], v[172:175], v[152:155], v[60:63]
	s_add_u32 m0, s28, 0x0
	s_nop 0
	global_load_lds_dwordx4 v10, s[4:5]
	s_waitcnt lgkmcnt(12)
	v_mfma_f32_16x16x32_f16 v[64:67], v[176:179], v[152:155], v[64:67]
	s_waitcnt lgkmcnt(11)
	v_mfma_f32_16x16x32_f16 v[68:71], v[180:183], v[152:155], v[68:71]
	s_waitcnt lgkmcnt(10)
	v_mfma_f32_16x16x32_f16 v[72:75], v[168:171], v[156:159], v[72:75]
	v_mfma_f32_16x16x32_f16 v[76:79], v[172:175], v[156:159], v[76:79]
	v_mfma_f32_16x16x32_f16 v[80:83], v[176:179], v[156:159], v[80:83]
	s_add_u32 m0, s28, 0x2000
	s_nop 0
	global_load_lds_dwordx4 v11, s[4:5]
	v_mfma_f32_16x16x32_f16 v[84:87], v[180:183], v[156:159], v[84:87]
	s_waitcnt lgkmcnt(9)
	v_mfma_f32_16x16x32_f16 v[88:91], v[168:171], v[160:163], v[88:91]
	v_mfma_f32_16x16x32_f16 v[92:95], v[172:175], v[160:163], v[92:95]
	v_mfma_f32_16x16x32_f16 v[96:99], v[176:179], v[160:163], v[96:99]
	v_mfma_f32_16x16x32_f16 v[100:103], v[180:183], v[160:163], v[100:103]
	s_add_u32 m0, s28, 0x4000
	s_nop 0
	global_load_lds_dwordx4 v12, s[4:5]
	s_waitcnt lgkmcnt(8)
	v_mfma_f32_16x16x32_f16 v[104:107], v[168:171], v[164:167], v[104:107]
	v_mfma_f32_16x16x32_f16 v[108:111], v[172:175], v[164:167], v[108:111]
	v_mfma_f32_16x16x32_f16 v[112:115], v[176:179], v[164:167], v[112:115]
	v_mfma_f32_16x16x32_f16 v[116:119], v[180:183], v[164:167], v[116:119]
	s_waitcnt lgkmcnt(7)
	ds_read_b128 v[152:155], v15 offset:49152
	ds_read_b128 v[168:171], v17 offset:49152
	ds_read_b128 v[172:175], v17 offset:51200
	ds_read_b128 v[176:179], v17 offset:53248
	ds_read_b128 v[180:183], v17 offset:55296
	ds_read_b128 v[156:159], v15 offset:51200
	ds_read_b128 v[160:163], v15 offset:53248
	ds_read_b128 v[164:167], v15 offset:55296
	s_waitcnt lgkmcnt(14)
	v_mfma_f32_16x16x32_f16 v[56:59], v[136:139], v[120:123], v[56:59]
	s_waitcnt lgkmcnt(13)
	v_mfma_f32_16x16x32_f16 v[60:63], v[140:143], v[120:123], v[60:63]
	s_add_u32 m0, s28, 0x6000
	s_nop 0
	global_load_lds_dwordx4 v13, s[4:5]
	s_add_u32 s4, s4, s20
	s_addc_u32 s5, s5, 0
	s_waitcnt lgkmcnt(12)
	v_mfma_f32_16x16x32_f16 v[64:67], v[144:147], v[120:123], v[64:67]
	s_waitcnt lgkmcnt(11)
	v_mfma_f32_16x16x32_f16 v[68:71], v[148:151], v[120:123], v[68:71]
	s_waitcnt lgkmcnt(10)
	v_mfma_f32_16x16x32_f16 v[72:75], v[136:139], v[124:127], v[72:75]
	v_mfma_f32_16x16x32_f16 v[76:79], v[140:143], v[124:127], v[76:79]
	v_mfma_f32_16x16x32_f16 v[80:83], v[144:147], v[124:127], v[80:83]
	s_add_u32 m0, s28, 0x8000
	s_nop 0
	global_load_lds_dwordx4 v10, s[6:7]
	v_mfma_f32_16x16x32_f16 v[84:87], v[148:151], v[124:127], v[84:87]
	s_waitcnt lgkmcnt(9)
	v_mfma_f32_16x16x32_f16 v[88:91], v[136:139], v[128:131], v[88:91]
	v_mfma_f32_16x16x32_f16 v[92:95], v[140:143], v[128:131], v[92:95]
	v_mfma_f32_16x16x32_f16 v[96:99], v[144:147], v[128:131], v[96:99]
	v_mfma_f32_16x16x32_f16 v[100:103], v[148:151], v[128:131], v[100:103]
	s_add_u32 m0, s28, 0xa000
	s_nop 0
	global_load_lds_dwordx4 v11, s[6:7]
	s_add_u32 s6, s6, s20
	s_addc_u32 s7, s7, 0
	s_waitcnt lgkmcnt(8)
	v_mfma_f32_16x16x32_f16 v[104:107], v[136:139], v[132:135], v[104:107]
	v_mfma_f32_16x16x32_f16 v[108:111], v[140:143], v[132:135], v[108:111]
	v_mfma_f32_16x16x32_f16 v[112:115], v[144:147], v[132:135], v[112:115]
	v_mfma_f32_16x16x32_f16 v[116:119], v[148:151], v[132:135], v[116:119]
	s_waitcnt vmcnt(6) lgkmcnt(0)
	s_barrier
	s_waitcnt lgkmcnt(7)
	ds_read_b128 v[120:123], v18
	ds_read_b128 v[136:139], v20
	ds_read_b128 v[140:143], v20 offset:2048
	ds_read_b128 v[144:147], v20 offset:4096
	ds_read_b128 v[148:151], v20 offset:6144
	ds_read_b128 v[124:127], v18 offset:2048
	ds_read_b128 v[128:131], v18 offset:4096
	ds_read_b128 v[132:135], v18 offset:6144
	s_waitcnt lgkmcnt(14)
	v_mfma_f32_16x16x32_f16 v[56:59], v[168:171], v[152:155], v[56:59]
	s_waitcnt lgkmcnt(13)
	v_mfma_f32_16x16x32_f16 v[60:63], v[172:175], v[152:155], v[60:63]
	s_add_u32 m0, s28, 0xc000
	s_nop 0
	global_load_lds_dwordx4 v10, s[4:5]
	s_waitcnt lgkmcnt(12)
	v_mfma_f32_16x16x32_f16 v[64:67], v[176:179], v[152:155], v[64:67]
	s_waitcnt lgkmcnt(11)
	v_mfma_f32_16x16x32_f16 v[68:71], v[180:183], v[152:155], v[68:71]
	s_waitcnt lgkmcnt(10)
	v_mfma_f32_16x16x32_f16 v[72:75], v[168:171], v[156:159], v[72:75]
	v_mfma_f32_16x16x32_f16 v[76:79], v[172:175], v[156:159], v[76:79]
	v_mfma_f32_16x16x32_f16 v[80:83], v[176:179], v[156:159], v[80:83]
	s_add_u32 m0, s28, 0xe000
	s_nop 0
	global_load_lds_dwordx4 v11, s[4:5]
	v_mfma_f32_16x16x32_f16 v[84:87], v[180:183], v[156:159], v[84:87]
	s_waitcnt lgkmcnt(9)
	v_mfma_f32_16x16x32_f16 v[88:91], v[168:171], v[160:163], v[88:91]
	v_mfma_f32_16x16x32_f16 v[92:95], v[172:175], v[160:163], v[92:95]
	v_mfma_f32_16x16x32_f16 v[96:99], v[176:179], v[160:163], v[96:99]
	v_mfma_f32_16x16x32_f16 v[100:103], v[180:183], v[160:163], v[100:103]
	s_add_u32 m0, s28, 0x10000
	s_nop 0
	global_load_lds_dwordx4 v12, s[4:5]
	s_waitcnt lgkmcnt(8)
	v_mfma_f32_16x16x32_f16 v[104:107], v[168:171], v[164:167], v[104:107]
	v_mfma_f32_16x16x32_f16 v[108:111], v[172:175], v[164:167], v[108:111]
	v_mfma_f32_16x16x32_f16 v[112:115], v[176:179], v[164:167], v[112:115]
	v_mfma_f32_16x16x32_f16 v[116:119], v[180:183], v[164:167], v[116:119]
	s_waitcnt lgkmcnt(7)
	ds_read_b128 v[152:155], v19
	ds_read_b128 v[168:171], v21
	ds_read_b128 v[172:175], v21 offset:2048
	ds_read_b128 v[176:179], v21 offset:4096
	ds_read_b128 v[180:183], v21 offset:6144
	ds_read_b128 v[156:159], v19 offset:2048
	ds_read_b128 v[160:163], v19 offset:4096
	ds_read_b128 v[164:167], v19 offset:6144
	s_waitcnt lgkmcnt(14)
	v_mfma_f32_16x16x32_f16 v[56:59], v[136:139], v[120:123], v[56:59]
	s_waitcnt lgkmcnt(13)
	v_mfma_f32_16x16x32_f16 v[60:63], v[140:143], v[120:123], v[60:63]
	s_add_u32 m0, s28, 0x12000
	s_nop 0
	global_load_lds_dwordx4 v13, s[4:5]
	s_add_u32 s4, s4, s20
	s_addc_u32 s5, s5, 0
	s_waitcnt lgkmcnt(12)
	v_mfma_f32_16x16x32_f16 v[64:67], v[144:147], v[120:123], v[64:67]
	s_waitcnt lgkmcnt(11)
	v_mfma_f32_16x16x32_f16 v[68:71], v[148:151], v[120:123], v[68:71]
	s_waitcnt lgkmcnt(10)
	v_mfma_f32_16x16x32_f16 v[72:75], v[136:139], v[124:127], v[72:75]
	v_mfma_f32_16x16x32_f16 v[76:79], v[140:143], v[124:127], v[76:79]
	v_mfma_f32_16x16x32_f16 v[80:83], v[144:147], v[124:127], v[80:83]
	s_add_u32 m0, s28, 0x14000
	s_nop 0
	global_load_lds_dwordx4 v10, s[6:7]
	v_mfma_f32_16x16x32_f16 v[84:87], v[148:151], v[124:127], v[84:87]
	s_waitcnt lgkmcnt(9)
	v_mfma_f32_16x16x32_f16 v[88:91], v[136:139], v[128:131], v[88:91]
	v_mfma_f32_16x16x32_f16 v[92:95], v[140:143], v[128:131], v[92:95]
	v_mfma_f32_16x16x32_f16 v[96:99], v[144:147], v[128:131], v[96:99]
	v_mfma_f32_16x16x32_f16 v[100:103], v[148:151], v[128:131], v[100:103]
	s_add_u32 m0, s28, 0x16000
	s_nop 0
	global_load_lds_dwordx4 v11, s[6:7]
	s_add_u32 s6, s6, s20
	s_addc_u32 s7, s7, 0
	s_waitcnt lgkmcnt(8)
	v_mfma_f32_16x16x32_f16 v[104:107], v[136:139], v[132:135], v[104:107]
	v_mfma_f32_16x16x32_f16 v[108:111], v[140:143], v[132:135], v[108:111]
	v_mfma_f32_16x16x32_f16 v[112:115], v[144:147], v[132:135], v[112:115]
	v_mfma_f32_16x16x32_f16 v[116:119], v[148:151], v[132:135], v[116:119]
	s_waitcnt vmcnt(6) lgkmcnt(0)
	s_barrier
	s_waitcnt lgkmcnt(7)
	ds_read_b128 v[120:123], v14
	ds_read_b128 v[136:139], v16
	ds_read_b128 v[140:143], v16 offset:2048
	ds_read_b128 v[144:147], v16 offset:4096
	ds_read_b128 v[148:151], v16 offset:6144
	ds_read_b128 v[124:127], v14 offset:2048
	ds_read_b128 v[128:131], v14 offset:4096
	ds_read_b128 v[132:135], v14 offset:6144
	s_waitcnt lgkmcnt(14)
	v_mfma_f32_16x16x32_f16 v[56:59], v[168:171], v[152:155], v[56:59]
	s_waitcnt lgkmcnt(13)
	v_mfma_f32_16x16x32_f16 v[60:63], v[172:175], v[152:155], v[60:63]
	s_add_u32 m0, s28, 0x18000
	s_nop 0
	global_load_lds_dwordx4 v10, s[4:5]
	s_waitcnt lgkmcnt(12)
	v_mfma_f32_16x16x32_f16 v[64:67], v[176:179], v[152:155], v[64:67]
	s_waitcnt lgkmcnt(11)
	v_mfma_f32_16x16x32_f16 v[68:71], v[180:183], v[152:155], v[68:71]
	s_waitcnt lgkmcnt(10)
	v_mfma_f32_16x16x32_f16 v[72:75], v[168:171], v[156:159], v[72:75]
	v_mfma_f32_16x16x32_f16 v[76:79], v[172:175], v[156:159], v[76:79]
	v_mfma_f32_16x16x32_f16 v[80:83], v[176:179], v[156:159], v[80:83]
	s_add_u32 m0, s28, 0x1a000
	s_nop 0
	global_load_lds_dwordx4 v11, s[4:5]
	v_mfma_f32_16x16x32_f16 v[84:87], v[180:183], v[156:159], v[84:87]
	s_waitcnt lgkmcnt(9)
	v_mfma_f32_16x16x32_f16 v[88:91], v[168:171], v[160:163], v[88:91]
	v_mfma_f32_16x16x32_f16 v[92:95], v[172:175], v[160:163], v[92:95]
	v_mfma_f32_16x16x32_f16 v[96:99], v[176:179], v[160:163], v[96:99]
	v_mfma_f32_16x16x32_f16 v[100:103], v[180:183], v[160:163], v[100:103]
	s_add_u32 m0, s28, 0x1c000
	s_nop 0
	global_load_lds_dwordx4 v12, s[4:5]
	s_waitcnt lgkmcnt(8)
	v_mfma_f32_16x16x32_f16 v[104:107], v[168:171], v[164:167], v[104:107]
	v_mfma_f32_16x16x32_f16 v[108:111], v[172:175], v[164:167], v[108:111]
	v_mfma_f32_16x16x32_f16 v[112:115], v[176:179], v[164:167], v[112:115]
	v_mfma_f32_16x16x32_f16 v[116:119], v[180:183], v[164:167], v[116:119]
	s_waitcnt lgkmcnt(7)
	ds_read_b128 v[152:155], v15
	ds_read_b128 v[168:171], v17
	ds_read_b128 v[172:175], v17 offset:2048
	ds_read_b128 v[176:179], v17 offset:4096
	ds_read_b128 v[180:183], v17 offset:6144
	ds_read_b128 v[156:159], v15 offset:2048
	ds_read_b128 v[160:163], v15 offset:4096
	ds_read_b128 v[164:167], v15 offset:6144
	s_waitcnt lgkmcnt(14)
	v_mfma_f32_16x16x32_f16 v[56:59], v[136:139], v[120:123], v[56:59]
	s_waitcnt lgkmcnt(13)
	v_mfma_f32_16x16x32_f16 v[60:63], v[140:143], v[120:123], v[60:63]
	s_add_u32 m0, s28, 0x1e000
	s_nop 0
	global_load_lds_dwordx4 v13, s[4:5]
	s_add_u32 s4, s4, s20
	s_addc_u32 s5, s5, 0
	s_waitcnt lgkmcnt(12)
	v_mfma_f32_16x16x32_f16 v[64:67], v[144:147], v[120:123], v[64:67]
	s_waitcnt lgkmcnt(11)
	v_mfma_f32_16x16x32_f16 v[68:71], v[148:151], v[120:123], v[68:71]
	s_waitcnt lgkmcnt(10)
	v_mfma_f32_16x16x32_f16 v[72:75], v[136:139], v[124:127], v[72:75]
	v_mfma_f32_16x16x32_f16 v[76:79], v[140:143], v[124:127], v[76:79]
	v_mfma_f32_16x16x32_f16 v[80:83], v[144:147], v[124:127], v[80:83]
	s_add_u32 m0, s28, 0x20000
	s_nop 0
	global_load_lds_dwordx4 v10, s[6:7]
	v_mfma_f32_16x16x32_f16 v[84:87], v[148:151], v[124:127], v[84:87]
	s_waitcnt lgkmcnt(9)
	v_mfma_f32_16x16x32_f16 v[88:91], v[136:139], v[128:131], v[88:91]
	v_mfma_f32_16x16x32_f16 v[92:95], v[140:143], v[128:131], v[92:95]
	v_mfma_f32_16x16x32_f16 v[96:99], v[144:147], v[128:131], v[96:99]
	v_mfma_f32_16x16x32_f16 v[100:103], v[148:151], v[128:131], v[100:103]
	s_add_u32 m0, s28, 0x22000
	s_nop 0
	global_load_lds_dwordx4 v11, s[6:7]
	s_add_u32 s6, s6, s20
	s_addc_u32 s7, s7, 0
	s_waitcnt lgkmcnt(8)
	v_mfma_f32_16x16x32_f16 v[104:107], v[136:139], v[132:135], v[104:107]
	v_mfma_f32_16x16x32_f16 v[108:111], v[140:143], v[132:135], v[108:111]
	v_mfma_f32_16x16x32_f16 v[112:115], v[144:147], v[132:135], v[112:115]
	v_mfma_f32_16x16x32_f16 v[116:119], v[148:151], v[132:135], v[116:119]
	s_waitcnt vmcnt(6) lgkmcnt(0)
	s_barrier
	s_waitcnt lgkmcnt(7)
	ds_read_b128 v[120:123], v14 offset:49152
	ds_read_b128 v[136:139], v16 offset:49152
	ds_read_b128 v[140:143], v16 offset:51200
	ds_read_b128 v[144:147], v16 offset:53248
	ds_read_b128 v[148:151], v16 offset:55296
	ds_read_b128 v[124:127], v14 offset:51200
	ds_read_b128 v[128:131], v14 offset:53248
	ds_read_b128 v[132:135], v14 offset:55296
	s_waitcnt lgkmcnt(14)
	v_mfma_f32_16x16x32_f16 v[56:59], v[168:171], v[152:155], v[56:59]
	s_waitcnt lgkmcnt(13)
	v_mfma_f32_16x16x32_f16 v[60:63], v[172:175], v[152:155], v[60:63]
	s_add_u32 m0, s28, 0x0
	s_nop 0
	global_load_lds_dwordx4 v10, s[4:5]
	s_waitcnt lgkmcnt(12)
	v_mfma_f32_16x16x32_f16 v[64:67], v[176:179], v[152:155], v[64:67]
	s_waitcnt lgkmcnt(11)
	v_mfma_f32_16x16x32_f16 v[68:71], v[180:183], v[152:155], v[68:71]
	s_waitcnt lgkmcnt(10)
	v_mfma_f32_16x16x32_f16 v[72:75], v[168:171], v[156:159], v[72:75]
	v_mfma_f32_16x16x32_f16 v[76:79], v[172:175], v[156:159], v[76:79]
	v_mfma_f32_16x16x32_f16 v[80:83], v[176:179], v[156:159], v[80:83]
	s_add_u32 m0, s28, 0x2000
	s_nop 0
	global_load_lds_dwordx4 v11, s[4:5]
	v_mfma_f32_16x16x32_f16 v[84:87], v[180:183], v[156:159], v[84:87]
	s_waitcnt lgkmcnt(9)
	v_mfma_f32_16x16x32_f16 v[88:91], v[168:171], v[160:163], v[88:91]
	v_mfma_f32_16x16x32_f16 v[92:95], v[172:175], v[160:163], v[92:95]
	v_mfma_f32_16x16x32_f16 v[96:99], v[176:179], v[160:163], v[96:99]
	v_mfma_f32_16x16x32_f16 v[100:103], v[180:183], v[160:163], v[100:103]
	s_add_u32 m0, s28, 0x4000
	s_nop 0
	global_load_lds_dwordx4 v12, s[4:5]
	s_waitcnt lgkmcnt(8)
	v_mfma_f32_16x16x32_f16 v[104:107], v[168:171], v[164:167], v[104:107]
	v_mfma_f32_16x16x32_f16 v[108:111], v[172:175], v[164:167], v[108:111]
	v_mfma_f32_16x16x32_f16 v[112:115], v[176:179], v[164:167], v[112:115]
	v_mfma_f32_16x16x32_f16 v[116:119], v[180:183], v[164:167], v[116:119]
	s_waitcnt lgkmcnt(7)
	ds_read_b128 v[152:155], v15 offset:49152
	ds_read_b128 v[168:171], v17 offset:49152
	ds_read_b128 v[172:175], v17 offset:51200
	ds_read_b128 v[176:179], v17 offset:53248
	ds_read_b128 v[180:183], v17 offset:55296
	ds_read_b128 v[156:159], v15 offset:51200
	ds_read_b128 v[160:163], v15 offset:53248
	ds_read_b128 v[164:167], v15 offset:55296
	s_waitcnt lgkmcnt(14)
	v_mfma_f32_16x16x32_f16 v[56:59], v[136:139], v[120:123], v[56:59]
	s_waitcnt lgkmcnt(13)
	v_mfma_f32_16x16x32_f16 v[60:63], v[140:143], v[120:123], v[60:63]
	s_add_u32 m0, s28, 0x6000
	s_nop 0
	global_load_lds_dwordx4 v13, s[4:5]
	s_add_u32 s4, s4, s20
	s_addc_u32 s5, s5, 0
	s_waitcnt lgkmcnt(12)
	v_mfma_f32_16x16x32_f16 v[64:67], v[144:147], v[120:123], v[64:67]
	s_waitcnt lgkmcnt(11)
	v_mfma_f32_16x16x32_f16 v[68:71], v[148:151], v[120:123], v[68:71]
	s_waitcnt lgkmcnt(10)
	v_mfma_f32_16x16x32_f16 v[72:75], v[136:139], v[124:127], v[72:75]
	v_mfma_f32_16x16x32_f16 v[76:79], v[140:143], v[124:127], v[76:79]
	v_mfma_f32_16x16x32_f16 v[80:83], v[144:147], v[124:127], v[80:83]
	s_add_u32 m0, s28, 0x8000
	s_nop 0
	global_load_lds_dwordx4 v10, s[6:7]
	v_mfma_f32_16x16x32_f16 v[84:87], v[148:151], v[124:127], v[84:87]
	s_waitcnt lgkmcnt(9)
	v_mfma_f32_16x16x32_f16 v[88:91], v[136:139], v[128:131], v[88:91]
	v_mfma_f32_16x16x32_f16 v[92:95], v[140:143], v[128:131], v[92:95]
	v_mfma_f32_16x16x32_f16 v[96:99], v[144:147], v[128:131], v[96:99]
	v_mfma_f32_16x16x32_f16 v[100:103], v[148:151], v[128:131], v[100:103]
	s_add_u32 m0, s28, 0xa000
	s_nop 0
	global_load_lds_dwordx4 v11, s[6:7]
	s_add_u32 s6, s6, s20
	s_addc_u32 s7, s7, 0
	s_waitcnt lgkmcnt(8)
	v_mfma_f32_16x16x32_f16 v[104:107], v[136:139], v[132:135], v[104:107]
	v_mfma_f32_16x16x32_f16 v[108:111], v[140:143], v[132:135], v[108:111]
	v_mfma_f32_16x16x32_f16 v[112:115], v[144:147], v[132:135], v[112:115]
	v_mfma_f32_16x16x32_f16 v[116:119], v[148:151], v[132:135], v[116:119]
	s_waitcnt vmcnt(6) lgkmcnt(0)
	s_barrier
	s_waitcnt lgkmcnt(7)
	ds_read_b128 v[120:123], v18
	ds_read_b128 v[136:139], v20
	ds_read_b128 v[140:143], v20 offset:2048
	ds_read_b128 v[144:147], v20 offset:4096
	ds_read_b128 v[148:151], v20 offset:6144
	ds_read_b128 v[124:127], v18 offset:2048
	ds_read_b128 v[128:131], v18 offset:4096
	ds_read_b128 v[132:135], v18 offset:6144
	s_waitcnt lgkmcnt(14)
	v_mfma_f32_16x16x32_f16 v[56:59], v[168:171], v[152:155], v[56:59]
	s_waitcnt lgkmcnt(13)
	v_mfma_f32_16x16x32_f16 v[60:63], v[172:175], v[152:155], v[60:63]
	s_waitcnt lgkmcnt(12)
	v_mfma_f32_16x16x32_f16 v[64:67], v[176:179], v[152:155], v[64:67]
	s_waitcnt lgkmcnt(11)
	v_mfma_f32_16x16x32_f16 v[68:71], v[180:183], v[152:155], v[68:71]
	s_waitcnt lgkmcnt(10)
	v_mfma_f32_16x16x32_f16 v[72:75], v[168:171], v[156:159], v[72:75]
	v_mfma_f32_16x16x32_f16 v[76:79], v[172:175], v[156:159], v[76:79]
	v_mfma_f32_16x16x32_f16 v[80:83], v[176:179], v[156:159], v[80:83]
	v_mfma_f32_16x16x32_f16 v[84:87], v[180:183], v[156:159], v[84:87]
	s_waitcnt lgkmcnt(9)
	v_mfma_f32_16x16x32_f16 v[88:91], v[168:171], v[160:163], v[88:91]
	v_mfma_f32_16x16x32_f16 v[92:95], v[172:175], v[160:163], v[92:95]
	v_mfma_f32_16x16x32_f16 v[96:99], v[176:179], v[160:163], v[96:99]
	v_mfma_f32_16x16x32_f16 v[100:103], v[180:183], v[160:163], v[100:103]
	s_waitcnt lgkmcnt(8)
	v_mfma_f32_16x16x32_f16 v[104:107], v[168:171], v[164:167], v[104:107]
	v_mfma_f32_16x16x32_f16 v[108:111], v[172:175], v[164:167], v[108:111]
	v_mfma_f32_16x16x32_f16 v[112:115], v[176:179], v[164:167], v[112:115]
	v_mfma_f32_16x16x32_f16 v[116:119], v[180:183], v[164:167], v[116:119]
	s_waitcnt lgkmcnt(7)
	ds_read_b128 v[152:155], v19
	ds_read_b128 v[168:171], v21
	ds_read_b128 v[172:175], v21 offset:2048
	ds_read_b128 v[176:179], v21 offset:4096
	ds_read_b128 v[180:183], v21 offset:6144
	ds_read_b128 v[156:159], v19 offset:2048
	ds_read_b128 v[160:163], v19 offset:4096
	ds_read_b128 v[164:167], v19 offset:6144
	s_waitcnt lgkmcnt(14)
	v_mfma_f32_16x16x32_f16 v[56:59], v[136:139], v[120:123], v[56:59]
	s_waitcnt lgkmcnt(13)
	v_mfma_f32_16x16x32_f16 v[60:63], v[140:143], v[120:123], v[60:63]
	s_waitcnt lgkmcnt(12)
	v_mfma_f32_16x16x32_f16 v[64:67], v[144:147], v[120:123], v[64:67]
	s_waitcnt lgkmcnt(11)
	v_mfma_f32_16x16x32_f16 v[68:71], v[148:151], v[120:123], v[68:71]
	s_waitcnt lgkmcnt(10)
	v_mfma_f32_16x16x32_f16 v[72:75], v[136:139], v[124:127], v[72:75]
	v_mfma_f32_16x16x32_f16 v[76:79], v[140:143], v[124:127], v[76:79]
	v_mfma_f32_16x16x32_f16 v[80:83], v[144:147], v[124:127], v[80:83]
	v_mfma_f32_16x16x32_f16 v[84:87], v[148:151], v[124:127], v[84:87]
	s_waitcnt lgkmcnt(9)
	v_mfma_f32_16x16x32_f16 v[88:91], v[136:139], v[128:131], v[88:91]
	v_mfma_f32_16x16x32_f16 v[92:95], v[140:143], v[128:131], v[92:95]
	v_mfma_f32_16x16x32_f16 v[96:99], v[144:147], v[128:131], v[96:99]
	v_mfma_f32_16x16x32_f16 v[100:103], v[148:151], v[128:131], v[100:103]
	s_waitcnt lgkmcnt(8)
	v_mfma_f32_16x16x32_f16 v[104:107], v[136:139], v[132:135], v[104:107]
	v_mfma_f32_16x16x32_f16 v[108:111], v[140:143], v[132:135], v[108:111]
	v_mfma_f32_16x16x32_f16 v[112:115], v[144:147], v[132:135], v[112:115]
	v_mfma_f32_16x16x32_f16 v[116:119], v[148:151], v[132:135], v[116:119]
	s_waitcnt vmcnt(0) lgkmcnt(0)
	s_barrier
	s_waitcnt lgkmcnt(7)
	ds_read_b128 v[120:123], v14
	ds_read_b128 v[136:139], v16
	ds_read_b128 v[140:143], v16 offset:2048
	ds_read_b128 v[144:147], v16 offset:4096
	ds_read_b128 v[148:151], v16 offset:6144
	ds_read_b128 v[124:127], v14 offset:2048
	ds_read_b128 v[128:131], v14 offset:4096
	ds_read_b128 v[132:135], v14 offset:6144
	s_waitcnt lgkmcnt(14)
	v_mfma_f32_16x16x32_f16 v[56:59], v[168:171], v[152:155], v[56:59]
	s_waitcnt lgkmcnt(13)
	v_mfma_f32_16x16x32_f16 v[60:63], v[172:175], v[152:155], v[60:63]
	s_waitcnt lgkmcnt(12)
	v_mfma_f32_16x16x32_f16 v[64:67], v[176:179], v[152:155], v[64:67]
	s_waitcnt lgkmcnt(11)
	v_mfma_f32_16x16x32_f16 v[68:71], v[180:183], v[152:155], v[68:71]
	s_waitcnt lgkmcnt(10)
	v_mfma_f32_16x16x32_f16 v[72:75], v[168:171], v[156:159], v[72:75]
	v_mfma_f32_16x16x32_f16 v[76:79], v[172:175], v[156:159], v[76:79]
	v_mfma_f32_16x16x32_f16 v[80:83], v[176:179], v[156:159], v[80:83]
	v_mfma_f32_16x16x32_f16 v[84:87], v[180:183], v[156:159], v[84:87]
	s_waitcnt lgkmcnt(9)
	v_mfma_f32_16x16x32_f16 v[88:91], v[168:171], v[160:163], v[88:91]
	v_mfma_f32_16x16x32_f16 v[92:95], v[172:175], v[160:163], v[92:95]
	v_mfma_f32_16x16x32_f16 v[96:99], v[176:179], v[160:163], v[96:99]
	v_mfma_f32_16x16x32_f16 v[100:103], v[180:183], v[160:163], v[100:103]
	s_waitcnt lgkmcnt(8)
	v_mfma_f32_16x16x32_f16 v[104:107], v[168:171], v[164:167], v[104:107]
	v_mfma_f32_16x16x32_f16 v[108:111], v[172:175], v[164:167], v[108:111]
	v_mfma_f32_16x16x32_f16 v[112:115], v[176:179], v[164:167], v[112:115]
	v_mfma_f32_16x16x32_f16 v[116:119], v[180:183], v[164:167], v[116:119]
	s_waitcnt lgkmcnt(7)
	ds_read_b128 v[152:155], v15
	ds_read_b128 v[168:171], v17
	ds_read_b128 v[172:175], v17 offset:2048
	ds_read_b128 v[176:179], v17 offset:4096
	ds_read_b128 v[180:183], v17 offset:6144
	ds_read_b128 v[156:159], v15 offset:2048
	ds_read_b128 v[160:163], v15 offset:4096
	ds_read_b128 v[164:167], v15 offset:6144
	s_waitcnt lgkmcnt(14)
	v_mfma_f32_16x16x32_f16 v[56:59], v[136:139], v[120:123], v[56:59]
	s_waitcnt lgkmcnt(13)
	v_mfma_f32_16x16x32_f16 v[60:63], v[140:143], v[120:123], v[60:63]
	s_waitcnt lgkmcnt(12)
	v_mfma_f32_16x16x32_f16 v[64:67], v[144:147], v[120:123], v[64:67]
	s_waitcnt lgkmcnt(11)
	v_mfma_f32_16x16x32_f16 v[68:71], v[148:151], v[120:123], v[68:71]
	s_waitcnt lgkmcnt(10)
	v_mfma_f32_16x16x32_f16 v[72:75], v[136:139], v[124:127], v[72:75]
	v_mfma_f32_16x16x32_f16 v[76:79], v[140:143], v[124:127], v[76:79]
	v_mfma_f32_16x16x32_f16 v[80:83], v[144:147], v[124:127], v[80:83]
	v_mfma_f32_16x16x32_f16 v[84:87], v[148:151], v[124:127], v[84:87]
	s_waitcnt lgkmcnt(9)
	v_mfma_f32_16x16x32_f16 v[88:91], v[136:139], v[128:131], v[88:91]
	v_mfma_f32_16x16x32_f16 v[92:95], v[140:143], v[128:131], v[92:95]
	v_mfma_f32_16x16x32_f16 v[96:99], v[144:147], v[128:131], v[96:99]
	v_mfma_f32_16x16x32_f16 v[100:103], v[148:151], v[128:131], v[100:103]
	s_waitcnt lgkmcnt(8)
	v_mfma_f32_16x16x32_f16 v[104:107], v[136:139], v[132:135], v[104:107]
	v_mfma_f32_16x16x32_f16 v[108:111], v[140:143], v[132:135], v[108:111]
	v_mfma_f32_16x16x32_f16 v[112:115], v[144:147], v[132:135], v[112:115]
	v_mfma_f32_16x16x32_f16 v[116:119], v[148:151], v[132:135], v[116:119]
	s_waitcnt lgkmcnt(6)
	v_mfma_f32_16x16x32_f16 v[56:59], v[168:171], v[152:155], v[56:59]
	s_waitcnt lgkmcnt(5)
	v_mfma_f32_16x16x32_f16 v[60:63], v[172:175], v[152:155], v[60:63]
	s_waitcnt lgkmcnt(4)
	v_mfma_f32_16x16x32_f16 v[64:67], v[176:179], v[152:155], v[64:67]
	s_waitcnt lgkmcnt(3)
	v_mfma_f32_16x16x32_f16 v[68:71], v[180:183], v[152:155], v[68:71]
	s_waitcnt lgkmcnt(2)
	v_mfma_f32_16x16x32_f16 v[72:75], v[168:171], v[156:159], v[72:75]
	v_mfma_f32_16x16x32_f16 v[76:79], v[172:175], v[156:159], v[76:79]
	v_mfma_f32_16x16x32_f16 v[80:83], v[176:179], v[156:159], v[80:83]
	v_mfma_f32_16x16x32_f16 v[84:87], v[180:183], v[156:159], v[84:87]
	s_waitcnt lgkmcnt(1)
	v_mfma_f32_16x16x32_f16 v[88:91], v[168:171], v[160:163], v[88:91]
	v_mfma_f32_16x16x32_f16 v[92:95], v[172:175], v[160:163], v[92:95]
	v_mfma_f32_16x16x32_f16 v[96:99], v[176:179], v[160:163], v[96:99]
	v_mfma_f32_16x16x32_f16 v[100:103], v[180:183], v[160:163], v[100:103]
	s_waitcnt lgkmcnt(0)
	v_mfma_f32_16x16x32_f16 v[104:107], v[168:171], v[164:167], v[104:107]
	v_mfma_f32_16x16x32_f16 v[108:111], v[172:175], v[164:167], v[108:111]
	v_mfma_f32_16x16x32_f16 v[112:115], v[176:179], v[164:167], v[112:115]
	v_mfma_f32_16x16x32_f16 v[116:119], v[180:183], v[164:167], v[116:119]
	s_nop 7
	s_nop 1
	v_mov_b32_e32 v187, s19
	v_add_f32_e32 v56, v56, v24
	v_add_f32_e32 v57, v57, v25
	v_add_f32_e32 v58, v58, v26
	v_add_f32_e32 v59, v59, v27
	v_add_f32_e32 v60, v60, v28
	v_add_f32_e32 v61, v61, v29
	v_add_f32_e32 v62, v62, v30
	v_add_f32_e32 v63, v63, v31
	v_add_f32_e32 v64, v64, v32
	v_add_f32_e32 v65, v65, v33
	v_add_f32_e32 v66, v66, v34
	v_add_f32_e32 v67, v67, v35
	v_add_f32_e32 v68, v68, v36
	v_add_f32_e32 v69, v69, v37
	v_add_f32_e32 v70, v70, v38
	v_add_f32_e32 v71, v71, v39
	v_mul_f32_e32 v184, v56, v56
	v_fmac_f32_e32 v184, v57, v57
	v_fmac_f32_e32 v184, v58, v58
	v_fmac_f32_e32 v184, v59, v59
	v_fmac_f32_e32 v184, v60, v60
	v_fmac_f32_e32 v184, v61, v61
	v_fmac_f32_e32 v184, v62, v62
	v_fmac_f32_e32 v184, v63, v63
	v_fmac_f32_e32 v184, v64, v64
	v_fmac_f32_e32 v184, v65, v65
	v_fmac_f32_e32 v184, v66, v66
	v_fmac_f32_e32 v184, v67, v67
	v_fmac_f32_e32 v184, v68, v68
	v_fmac_f32_e32 v184, v69, v69
	v_fmac_f32_e32 v184, v70, v70
	v_fmac_f32_e32 v184, v71, v71
	v_mov_b32_e32 v185, v184
	s_nop 1
	v_permlane16_swap_b32_e32 v184, v185
	v_add_f32_e32 v184, v184, v185
	v_mov_b32_e32 v185, v184
	s_nop 1
	v_permlane32_swap_b32_e32 v184, v185
	v_add_f32_e32 v184, v184, v185
	v_mov_b32_e32 v186, 0x358637bd
	v_fmac_f32_e32 v186, 0x3c800000, v184
	v_rsq_f32_e32 v186, v186
	s_nop 0
	v_mul_f32_e32 v186, v187, v186
	v_mul_f32_e32 v56, v56, v186
	v_mul_f32_e32 v57, v57, v186
	v_mul_f32_e32 v58, v58, v186
	v_mul_f32_e32 v59, v59, v186
	v_mul_f32_e32 v56, v56, v40
	v_mul_f32_e32 v57, v57, v41
	v_mul_f32_e32 v58, v58, v42
	v_mul_f32_e32 v59, v59, v43
	v_cvt_pk_f16_f32 v56, v56, v57
	v_cvt_pk_f16_f32 v57, v58, v59
	global_store_dwordx2 v22, v[56:57], s[22:23] offset:0
	v_mul_f32_e32 v60, v60, v186
	v_mul_f32_e32 v61, v61, v186
	v_mul_f32_e32 v62, v62, v186
	v_mul_f32_e32 v63, v63, v186
	v_mul_f32_e32 v60, v60, v44
	v_mul_f32_e32 v61, v61, v45
	v_mul_f32_e32 v62, v62, v46
	v_mul_f32_e32 v63, v63, v47
	v_cvt_pk_f16_f32 v60, v60, v61
	v_cvt_pk_f16_f32 v61, v62, v63
	global_store_dwordx2 v22, v[60:61], s[22:23] offset:1024
	v_mul_f32_e32 v64, v64, v186
	v_mul_f32_e32 v65, v65, v186
	v_mul_f32_e32 v66, v66, v186
	v_mul_f32_e32 v67, v67, v186
	v_mul_f32_e32 v64, v64, v48
	v_mul_f32_e32 v65, v65, v49
	v_mul_f32_e32 v66, v66, v50
	v_mul_f32_e32 v67, v67, v51
	v_cvt_pk_f16_f32 v64, v64, v65
	v_cvt_pk_f16_f32 v65, v66, v67
	global_store_dwordx2 v22, v[64:65], s[22:23] offset:2048
	v_mul_f32_e32 v68, v68, v186
	v_mul_f32_e32 v69, v69, v186
	v_mul_f32_e32 v70, v70, v186
	v_mul_f32_e32 v71, v71, v186
	v_mul_f32_e32 v68, v68, v52
	v_mul_f32_e32 v69, v69, v53
	v_mul_f32_e32 v70, v70, v54
	v_mul_f32_e32 v71, v71, v55
	v_cvt_pk_f16_f32 v68, v68, v69
	v_cvt_pk_f16_f32 v69, v70, v71
	global_store_dwordx2 v22, v[68:69], s[22:23] offset:3072
	v_add_f32_e32 v72, v72, v24
	v_add_f32_e32 v73, v73, v25
	v_add_f32_e32 v74, v74, v26
	v_add_f32_e32 v75, v75, v27
	v_add_f32_e32 v76, v76, v28
	v_add_f32_e32 v77, v77, v29
	v_add_f32_e32 v78, v78, v30
	v_add_f32_e32 v79, v79, v31
	v_add_f32_e32 v80, v80, v32
	v_add_f32_e32 v81, v81, v33
	v_add_f32_e32 v82, v82, v34
	v_add_f32_e32 v83, v83, v35
	v_add_f32_e32 v84, v84, v36
	v_add_f32_e32 v85, v85, v37
	v_add_f32_e32 v86, v86, v38
	v_add_f32_e32 v87, v87, v39
	v_mul_f32_e32 v184, v72, v72
	v_fmac_f32_e32 v184, v73, v73
	v_fmac_f32_e32 v184, v74, v74
	v_fmac_f32_e32 v184, v75, v75
	v_fmac_f32_e32 v184, v76, v76
	v_fmac_f32_e32 v184, v77, v77
	v_fmac_f32_e32 v184, v78, v78
	v_fmac_f32_e32 v184, v79, v79
	v_fmac_f32_e32 v184, v80, v80
	v_fmac_f32_e32 v184, v81, v81
	v_fmac_f32_e32 v184, v82, v82
	v_fmac_f32_e32 v184, v83, v83
	v_fmac_f32_e32 v184, v84, v84
	v_fmac_f32_e32 v184, v85, v85
	v_fmac_f32_e32 v184, v86, v86
	v_fmac_f32_e32 v184, v87, v87
	v_mov_b32_e32 v185, v184
	s_nop 1
	v_permlane16_swap_b32_e32 v184, v185
	v_add_f32_e32 v184, v184, v185
	v_mov_b32_e32 v185, v184
	s_nop 1
	v_permlane32_swap_b32_e32 v184, v185
	v_add_f32_e32 v184, v184, v185
	v_mov_b32_e32 v186, 0x358637bd
	v_fmac_f32_e32 v186, 0x3c800000, v184
	v_rsq_f32_e32 v186, v186
	s_nop 0
	v_mul_f32_e32 v186, v187, v186
	v_mul_f32_e32 v72, v72, v186
	v_mul_f32_e32 v73, v73, v186
	v_mul_f32_e32 v74, v74, v186
	v_mul_f32_e32 v75, v75, v186
	v_mul_f32_e32 v72, v72, v40
	v_mul_f32_e32 v73, v73, v41
	v_mul_f32_e32 v74, v74, v42
	v_mul_f32_e32 v75, v75, v43
	v_cvt_pk_f16_f32 v72, v72, v73
	v_cvt_pk_f16_f32 v73, v74, v75
	global_store_dwordx2 v22, v[72:73], s[22:23] offset:256
	v_mul_f32_e32 v76, v76, v186
	v_mul_f32_e32 v77, v77, v186
	v_mul_f32_e32 v78, v78, v186
	v_mul_f32_e32 v79, v79, v186
	v_mul_f32_e32 v76, v76, v44
	v_mul_f32_e32 v77, v77, v45
	v_mul_f32_e32 v78, v78, v46
	v_mul_f32_e32 v79, v79, v47
	v_cvt_pk_f16_f32 v76, v76, v77
	v_cvt_pk_f16_f32 v77, v78, v79
	global_store_dwordx2 v22, v[76:77], s[22:23] offset:1280
	v_mul_f32_e32 v80, v80, v186
	v_mul_f32_e32 v81, v81, v186
	v_mul_f32_e32 v82, v82, v186
	v_mul_f32_e32 v83, v83, v186
	v_mul_f32_e32 v80, v80, v48
	v_mul_f32_e32 v81, v81, v49
	v_mul_f32_e32 v82, v82, v50
	v_mul_f32_e32 v83, v83, v51
	v_cvt_pk_f16_f32 v80, v80, v81
	v_cvt_pk_f16_f32 v81, v82, v83
	global_store_dwordx2 v22, v[80:81], s[22:23] offset:2304
	v_mul_f32_e32 v84, v84, v186
	v_mul_f32_e32 v85, v85, v186
	v_mul_f32_e32 v86, v86, v186
	v_mul_f32_e32 v87, v87, v186
	v_mul_f32_e32 v84, v84, v52
	v_mul_f32_e32 v85, v85, v53
	v_mul_f32_e32 v86, v86, v54
	v_mul_f32_e32 v87, v87, v55
	v_cvt_pk_f16_f32 v84, v84, v85
	v_cvt_pk_f16_f32 v85, v86, v87
	global_store_dwordx2 v22, v[84:85], s[22:23] offset:3328
	v_add_f32_e32 v88, v88, v24
	v_add_f32_e32 v89, v89, v25
	v_add_f32_e32 v90, v90, v26
	v_add_f32_e32 v91, v91, v27
	v_add_f32_e32 v92, v92, v28
	v_add_f32_e32 v93, v93, v29
	v_add_f32_e32 v94, v94, v30
	v_add_f32_e32 v95, v95, v31
	v_add_f32_e32 v96, v96, v32
	v_add_f32_e32 v97, v97, v33
	v_add_f32_e32 v98, v98, v34
	v_add_f32_e32 v99, v99, v35
	v_add_f32_e32 v100, v100, v36
	v_add_f32_e32 v101, v101, v37
	v_add_f32_e32 v102, v102, v38
	v_add_f32_e32 v103, v103, v39
	v_mul_f32_e32 v184, v88, v88
	v_fmac_f32_e32 v184, v89, v89
	v_fmac_f32_e32 v184, v90, v90
	v_fmac_f32_e32 v184, v91, v91
	v_fmac_f32_e32 v184, v92, v92
	v_fmac_f32_e32 v184, v93, v93
	v_fmac_f32_e32 v184, v94, v94
	v_fmac_f32_e32 v184, v95, v95
	v_fmac_f32_e32 v184, v96, v96
	v_fmac_f32_e32 v184, v97, v97
	v_fmac_f32_e32 v184, v98, v98
	v_fmac_f32_e32 v184, v99, v99
	v_fmac_f32_e32 v184, v100, v100
	v_fmac_f32_e32 v184, v101, v101
	v_fmac_f32_e32 v184, v102, v102
	v_fmac_f32_e32 v184, v103, v103
	v_mov_b32_e32 v185, v184
	s_nop 1
	v_permlane16_swap_b32_e32 v184, v185
	v_add_f32_e32 v184, v184, v185
	v_mov_b32_e32 v185, v184
	s_nop 1
	v_permlane32_swap_b32_e32 v184, v185
	v_add_f32_e32 v184, v184, v185
	v_mov_b32_e32 v186, 0x358637bd
	v_fmac_f32_e32 v186, 0x3c800000, v184
	v_rsq_f32_e32 v186, v186
	s_nop 0
	v_mul_f32_e32 v186, v187, v186
	v_mul_f32_e32 v88, v88, v186
	v_mul_f32_e32 v89, v89, v186
	v_mul_f32_e32 v90, v90, v186
	v_mul_f32_e32 v91, v91, v186
	v_mul_f32_e32 v88, v88, v40
	v_mul_f32_e32 v89, v89, v41
	v_mul_f32_e32 v90, v90, v42
	v_mul_f32_e32 v91, v91, v43
	v_cvt_pk_f16_f32 v88, v88, v89
	v_cvt_pk_f16_f32 v89, v90, v91
	global_store_dwordx2 v23, v[88:89], s[22:23] offset:0
	v_mul_f32_e32 v92, v92, v186
	v_mul_f32_e32 v93, v93, v186
	v_mul_f32_e32 v94, v94, v186
	v_mul_f32_e32 v95, v95, v186
	v_mul_f32_e32 v92, v92, v44
	v_mul_f32_e32 v93, v93, v45
	v_mul_f32_e32 v94, v94, v46
	v_mul_f32_e32 v95, v95, v47
	v_cvt_pk_f16_f32 v92, v92, v93
	v_cvt_pk_f16_f32 v93, v94, v95
	global_store_dwordx2 v23, v[92:93], s[22:23] offset:1024
	v_mul_f32_e32 v96, v96, v186
	v_mul_f32_e32 v97, v97, v186
	v_mul_f32_e32 v98, v98, v186
	v_mul_f32_e32 v99, v99, v186
	v_mul_f32_e32 v96, v96, v48
	v_mul_f32_e32 v97, v97, v49
	v_mul_f32_e32 v98, v98, v50
	v_mul_f32_e32 v99, v99, v51
	v_cvt_pk_f16_f32 v96, v96, v97
	v_cvt_pk_f16_f32 v97, v98, v99
	global_store_dwordx2 v23, v[96:97], s[22:23] offset:2048
	v_mul_f32_e32 v100, v100, v186
	v_mul_f32_e32 v101, v101, v186
	v_mul_f32_e32 v102, v102, v186
	v_mul_f32_e32 v103, v103, v186
	v_mul_f32_e32 v100, v100, v52
	v_mul_f32_e32 v101, v101, v53
	v_mul_f32_e32 v102, v102, v54
	v_mul_f32_e32 v103, v103, v55
	v_cvt_pk_f16_f32 v100, v100, v101
	v_cvt_pk_f16_f32 v101, v102, v103
	global_store_dwordx2 v23, v[100:101], s[22:23] offset:3072
	v_add_f32_e32 v104, v104, v24
	v_add_f32_e32 v105, v105, v25
	v_add_f32_e32 v106, v106, v26
	v_add_f32_e32 v107, v107, v27
	v_add_f32_e32 v108, v108, v28
	v_add_f32_e32 v109, v109, v29
	v_add_f32_e32 v110, v110, v30
	v_add_f32_e32 v111, v111, v31
	v_add_f32_e32 v112, v112, v32
	v_add_f32_e32 v113, v113, v33
	v_add_f32_e32 v114, v114, v34
	v_add_f32_e32 v115, v115, v35
	v_add_f32_e32 v116, v116, v36
	v_add_f32_e32 v117, v117, v37
	v_add_f32_e32 v118, v118, v38
	v_add_f32_e32 v119, v119, v39
	v_mul_f32_e32 v184, v104, v104
	v_fmac_f32_e32 v184, v105, v105
	v_fmac_f32_e32 v184, v106, v106
	v_fmac_f32_e32 v184, v107, v107
	v_fmac_f32_e32 v184, v108, v108
	v_fmac_f32_e32 v184, v109, v109
	v_fmac_f32_e32 v184, v110, v110
	v_fmac_f32_e32 v184, v111, v111
	v_fmac_f32_e32 v184, v112, v112
	v_fmac_f32_e32 v184, v113, v113
	v_fmac_f32_e32 v184, v114, v114
	v_fmac_f32_e32 v184, v115, v115
	v_fmac_f32_e32 v184, v116, v116
	v_fmac_f32_e32 v184, v117, v117
	v_fmac_f32_e32 v184, v118, v118
	v_fmac_f32_e32 v184, v119, v119
	v_mov_b32_e32 v185, v184
	s_nop 1
	v_permlane16_swap_b32_e32 v184, v185
	v_add_f32_e32 v184, v184, v185
	v_mov_b32_e32 v185, v184
	s_nop 1
	v_permlane32_swap_b32_e32 v184, v185
	v_add_f32_e32 v184, v184, v185
	v_mov_b32_e32 v186, 0x358637bd
	v_fmac_f32_e32 v186, 0x3c800000, v184
	v_rsq_f32_e32 v186, v186
	s_nop 0
	v_mul_f32_e32 v186, v187, v186
	v_mul_f32_e32 v104, v104, v186
	v_mul_f32_e32 v105, v105, v186
	v_mul_f32_e32 v106, v106, v186
	v_mul_f32_e32 v107, v107, v186
	v_mul_f32_e32 v104, v104, v40
	v_mul_f32_e32 v105, v105, v41
	v_mul_f32_e32 v106, v106, v42
	v_mul_f32_e32 v107, v107, v43
	v_cvt_pk_f16_f32 v104, v104, v105
	v_cvt_pk_f16_f32 v105, v106, v107
	global_store_dwordx2 v23, v[104:105], s[22:23] offset:256
	v_mul_f32_e32 v108, v108, v186
	v_mul_f32_e32 v109, v109, v186
	v_mul_f32_e32 v110, v110, v186
	v_mul_f32_e32 v111, v111, v186
	v_mul_f32_e32 v108, v108, v44
	v_mul_f32_e32 v109, v109, v45
	v_mul_f32_e32 v110, v110, v46
	v_mul_f32_e32 v111, v111, v47
	v_cvt_pk_f16_f32 v108, v108, v109
	v_cvt_pk_f16_f32 v109, v110, v111
	global_store_dwordx2 v23, v[108:109], s[22:23] offset:1280
	v_mul_f32_e32 v112, v112, v186
	v_mul_f32_e32 v113, v113, v186
	v_mul_f32_e32 v114, v114, v186
	v_mul_f32_e32 v115, v115, v186
	v_mul_f32_e32 v112, v112, v48
	v_mul_f32_e32 v113, v113, v49
	v_mul_f32_e32 v114, v114, v50
	v_mul_f32_e32 v115, v115, v51
	v_cvt_pk_f16_f32 v112, v112, v113
	v_cvt_pk_f16_f32 v113, v114, v115
	global_store_dwordx2 v23, v[112:113], s[22:23] offset:2304
	v_mul_f32_e32 v116, v116, v186
	v_mul_f32_e32 v117, v117, v186
	v_mul_f32_e32 v118, v118, v186
	v_mul_f32_e32 v119, v119, v186
	v_mul_f32_e32 v116, v116, v52
	v_mul_f32_e32 v117, v117, v53
	v_mul_f32_e32 v118, v118, v54
	v_mul_f32_e32 v119, v119, v55
	v_cvt_pk_f16_f32 v116, v116, v117
	v_cvt_pk_f16_f32 v117, v118, v119
	global_store_dwordx2 v23, v[116:117], s[22:23] offset:3328
	s_endpgm
.Lpf_v:
	v_lshlrev_b32_e32 v5, 2, v3
	global_load_dword v24, v5, s[14:15] offset:0
	global_load_dword v25, v5, s[14:15] offset:64
	global_load_dword v26, v5, s[14:15] offset:128
	global_load_dword v27, v5, s[14:15] offset:192
	s_lshl_b32 s8, s27, 7
	s_lshr_b32 s24, s10, 4
	s_add_u32 s8, s8, s24
	s_lshl_b32 s24, s25, 2
	s_add_u32 s8, s8, s24
	s_lshl_b32 s8, s8, 11
	s_add_u32 s22, s22, s8
	s_addc_u32 s23, s23, 0
	s_add_u32 m0, s28, 0x0
	s_nop 0
	global_load_lds_dwordx4 v10, s[4:5]
	s_add_u32 m0, s28, 0x2000
	s_nop 0
	global_load_lds_dwordx4 v11, s[4:5]
	s_add_u32 m0, s28, 0x4000
	s_nop 0
	global_load_lds_dwordx4 v12, s[4:5]
	s_add_u32 m0, s28, 0x6000
	s_nop 0
	global_load_lds_dwordx4 v13, s[4:5]
	s_add_u32 s4, s4, s20
	s_addc_u32 s5, s5, 0
	s_add_u32 m0, s28, 0x8000
	s_nop 0
	global_load_lds_dwordx4 v10, s[6:7]
	s_add_u32 m0, s28, 0xa000
	s_nop 0
	global_load_lds_dwordx4 v11, s[6:7]
	s_add_u32 s6, s6, s20
	s_addc_u32 s7, s7, 0
	s_add_u32 m0, s28, 0xc000
	s_nop 0
	global_load_lds_dwordx4 v10, s[4:5]
	s_add_u32 m0, s28, 0xe000
	s_nop 0
	global_load_lds_dwordx4 v11, s[4:5]
	s_add_u32 m0, s28, 0x10000
	s_nop 0
	global_load_lds_dwordx4 v12, s[4:5]
	s_add_u32 m0, s28, 0x12000
	s_nop 0
	global_load_lds_dwordx4 v13, s[4:5]
	s_add_u32 s4, s4, s20
	s_addc_u32 s5, s5, 0
	s_add_u32 m0, s28, 0x14000
	s_nop 0
	global_load_lds_dwordx4 v10, s[6:7]
	s_add_u32 m0, s28, 0x16000
	s_nop 0
	global_load_lds_dwordx4 v11, s[6:7]
	s_add_u32 s6, s6, s20
	s_addc_u32 s7, s7, 0
	s_add_u32 m0, s28, 0x18000
	s_nop 0
	global_load_lds_dwordx4 v10, s[4:5]
	s_add_u32 m0, s28, 0x1a000
	s_nop 0
	global_load_lds_dwordx4 v11, s[4:5]
	s_add_u32 m0, s28, 0x1c000
	s_nop 0
	global_load_lds_dwordx4 v12, s[4:5]
	s_add_u32 m0, s28, 0x1e000
	s_nop 0
	global_load_lds_dwordx4 v13, s[4:5]
	s_add_u32 s4, s4, s20
	s_addc_u32 s5, s5, 0
	s_add_u32 m0, s28, 0x20000
	s_nop 0
	global_load_lds_dwordx4 v10, s[6:7]
	s_add_u32 m0, s28, 0x22000
	s_nop 0
	global_load_lds_dwordx4 v11, s[6:7]
	s_add_u32 s6, s6, s20
	s_addc_u32 s7, s7, 0
	s_waitcnt vmcnt(12)
	s_barrier
	s_waitcnt lgkmcnt(7)
	ds_read_b128 v[120:123], v14
	ds_read_b128 v[136:139], v16
	ds_read_b128 v[140:143], v16 offset:2048
	ds_read_b128 v[144:147], v16 offset:4096
	ds_read_b128 v[148:151], v16 offset:6144
	ds_read_b128 v[124:127], v14 offset:2048
	ds_read_b128 v[128:131], v14 offset:4096
	ds_read_b128 v[132:135], v14 offset:6144
	s_waitcnt lgkmcnt(7)
	ds_read_b128 v[152:155], v15
	ds_read_b128 v[168:171], v17
	ds_read_b128 v[172:175], v17 offset:2048
	ds_read_b128 v[176:179], v17 offset:4096
	ds_read_b128 v[180:183], v17 offset:6144
	ds_read_b128 v[156:159], v15 offset:2048
	ds_read_b128 v[160:163], v15 offset:4096
	ds_read_b128 v[164:167], v15 offset:6144
	s_waitcnt lgkmcnt(14)
	v_mfma_f32_16x16x32_f16 v[56:59], v[120:123], v[136:139], 0
	s_waitcnt lgkmcnt(13)
	v_mfma_f32_16x16x32_f16 v[60:63], v[120:123], v[140:143], 0
	s_waitcnt lgkmcnt(12)
	v_mfma_f32_16x16x32_f16 v[64:67], v[120:123], v[144:147], 0
	s_waitcnt lgkmcnt(11)
	v_mfma_f32_16x16x32_f16 v[68:71], v[120:123], v[148:151], 0
	s_waitcnt lgkmcnt(10)
	v_mfma_f32_16x16x32_f16 v[72:75], v[124:127], v[136:139], 0
	v_mfma_f32_16x16x32_f16 v[76:79], v[124:127], v[140:143], 0
	v_mfma_f32_16x16x32_f16 v[80:83], v[124:127], v[144:147], 0
	v_mfma_f32_16x16x32_f16 v[84:87], v[124:127], v[148:151], 0
	s_waitcnt lgkmcnt(9)
	v_mfma_f32_16x16x32_f16 v[88:91], v[128:131], v[136:139], 0
	v_mfma_f32_16x16x32_f16 v[92:95], v[128:131], v[140:143], 0
	v_mfma_f32_16x16x32_f16 v[96:99], v[128:131], v[144:147], 0
	v_mfma_f32_16x16x32_f16 v[100:103], v[128:131], v[148:151], 0
	s_waitcnt lgkmcnt(8)
	v_mfma_f32_16x16x32_f16 v[104:107], v[132:135], v[136:139], 0
	v_mfma_f32_16x16x32_f16 v[108:111], v[132:135], v[140:143], 0
	v_mfma_f32_16x16x32_f16 v[112:115], v[132:135], v[144:147], 0
	v_mfma_f32_16x16x32_f16 v[116:119], v[132:135], v[148:151], 0
	s_waitcnt vmcnt(6) lgkmcnt(0)
	s_barrier
	s_waitcnt lgkmcnt(7)
	ds_read_b128 v[120:123], v14 offset:49152
	ds_read_b128 v[136:139], v16 offset:49152
	ds_read_b128 v[140:143], v16 offset:51200
	ds_read_b128 v[144:147], v16 offset:53248
	ds_read_b128 v[148:151], v16 offset:55296
	ds_read_b128 v[124:127], v14 offset:51200
	ds_read_b128 v[128:131], v14 offset:53248
	ds_read_b128 v[132:135], v14 offset:55296
	s_waitcnt lgkmcnt(14)
	v_mfma_f32_16x16x32_f16 v[56:59], v[152:155], v[168:171], v[56:59]
	s_waitcnt lgkmcnt(13)
	v_mfma_f32_16x16x32_f16 v[60:63], v[152:155], v[172:175], v[60:63]
	s_add_u32 m0, s28, 0x0
	s_nop 0
	global_load_lds_dwordx4 v10, s[4:5]
	s_waitcnt lgkmcnt(12)
	v_mfma_f32_16x16x32_f16 v[64:67], v[152:155], v[176:179], v[64:67]
	s_waitcnt lgkmcnt(11)
	v_mfma_f32_16x16x32_f16 v[68:71], v[152:155], v[180:183], v[68:71]
	s_waitcnt lgkmcnt(10)
	v_mfma_f32_16x16x32_f16 v[72:75], v[156:159], v[168:171], v[72:75]
	v_mfma_f32_16x16x32_f16 v[76:79], v[156:159], v[172:175], v[76:79]
	v_mfma_f32_16x16x32_f16 v[80:83], v[156:159], v[176:179], v[80:83]
	s_add_u32 m0, s28, 0x2000
	s_nop 0
	global_load_lds_dwordx4 v11, s[4:5]
	v_mfma_f32_16x16x32_f16 v[84:87], v[156:159], v[180:183], v[84:87]
	s_waitcnt lgkmcnt(9)
	v_mfma_f32_16x16x32_f16 v[88:91], v[160:163], v[168:171], v[88:91]
	v_mfma_f32_16x16x32_f16 v[92:95], v[160:163], v[172:175], v[92:95]
	v_mfma_f32_16x16x32_f16 v[96:99], v[160:163], v[176:179], v[96:99]
	v_mfma_f32_16x16x32_f16 v[100:103], v[160:163], v[180:183], v[100:103]
	s_add_u32 m0, s28, 0x4000
	s_nop 0
	global_load_lds_dwordx4 v12, s[4:5]
	s_waitcnt lgkmcnt(8)
	v_mfma_f32_16x16x32_f16 v[104:107], v[164:167], v[168:171], v[104:107]
	v_mfma_f32_16x16x32_f16 v[108:111], v[164:167], v[172:175], v[108:111]
	v_mfma_f32_16x16x32_f16 v[112:115], v[164:167], v[176:179], v[112:115]
	v_mfma_f32_16x16x32_f16 v[116:119], v[164:167], v[180:183], v[116:119]
	s_waitcnt lgkmcnt(7)
	ds_read_b128 v[152:155], v15 offset:49152
	ds_read_b128 v[168:171], v17 offset:49152
	ds_read_b128 v[172:175], v17 offset:51200
	ds_read_b128 v[176:179], v17 offset:53248
	ds_read_b128 v[180:183], v17 offset:55296
	ds_read_b128 v[156:159], v15 offset:51200
	ds_read_b128 v[160:163], v15 offset:53248
	ds_read_b128 v[164:167], v15 offset:55296
	s_waitcnt lgkmcnt(14)
	v_mfma_f32_16x16x32_f16 v[56:59], v[120:123], v[136:139], v[56:59]
	s_waitcnt lgkmcnt(13)
	v_mfma_f32_16x16x32_f16 v[60:63], v[120:123], v[140:143], v[60:63]
	s_add_u32 m0, s28, 0x6000
	s_nop 0
	global_load_lds_dwordx4 v13, s[4:5]
	s_add_u32 s4, s4, s20
	s_addc_u32 s5, s5, 0
	s_waitcnt lgkmcnt(12)
	v_mfma_f32_16x16x32_f16 v[64:67], v[120:123], v[144:147], v[64:67]
	s_waitcnt lgkmcnt(11)
	v_mfma_f32_16x16x32_f16 v[68:71], v[120:123], v[148:151], v[68:71]
	s_waitcnt lgkmcnt(10)
	v_mfma_f32_16x16x32_f16 v[72:75], v[124:127], v[136:139], v[72:75]
	v_mfma_f32_16x16x32_f16 v[76:79], v[124:127], v[140:143], v[76:79]
	v_mfma_f32_16x16x32_f16 v[80:83], v[124:127], v[144:147], v[80:83]
	s_add_u32 m0, s28, 0x8000
	s_nop 0
	global_load_lds_dwordx4 v10, s[6:7]
	v_mfma_f32_16x16x32_f16 v[84:87], v[124:127], v[148:151], v[84:87]
	s_waitcnt lgkmcnt(9)
	v_mfma_f32_16x16x32_f16 v[88:91], v[128:131], v[136:139], v[88:91]
	v_mfma_f32_16x16x32_f16 v[92:95], v[128:131], v[140:143], v[92:95]
	v_mfma_f32_16x16x32_f16 v[96:99], v[128:131], v[144:147], v[96:99]
	v_mfma_f32_16x16x32_f16 v[100:103], v[128:131], v[148:151], v[100:103]
	s_add_u32 m0, s28, 0xa000
	s_nop 0
	global_load_lds_dwordx4 v11, s[6:7]
	s_add_u32 s6, s6, s20
	s_addc_u32 s7, s7, 0
	s_waitcnt lgkmcnt(8)
	v_mfma_f32_16x16x32_f16 v[104:107], v[132:135], v[136:139], v[104:107]
	v_mfma_f32_16x16x32_f16 v[108:111], v[132:135], v[140:143], v[108:111]
	v_mfma_f32_16x16x32_f16 v[112:115], v[132:135], v[144:147], v[112:115]
	v_mfma_f32_16x16x32_f16 v[116:119], v[132:135], v[148:151], v[116:119]
	s_waitcnt vmcnt(6) lgkmcnt(0)
	s_barrier
	s_waitcnt lgkmcnt(7)
	ds_read_b128 v[120:123], v18
	ds_read_b128 v[136:139], v20
	ds_read_b128 v[140:143], v20 offset:2048
	ds_read_b128 v[144:147], v20 offset:4096
	ds_read_b128 v[148:151], v20 offset:6144
	ds_read_b128 v[124:127], v18 offset:2048
	ds_read_b128 v[128:131], v18 offset:4096
	ds_read_b128 v[132:135], v18 offset:6144
	s_waitcnt lgkmcnt(14)
	v_mfma_f32_16x16x32_f16 v[56:59], v[152:155], v[168:171], v[56:59]
	s_waitcnt lgkmcnt(13)
	v_mfma_f32_16x16x32_f16 v[60:63], v[152:155], v[172:175], v[60:63]
	s_add_u32 m0, s28, 0xc000
	s_nop 0
	global_load_lds_dwordx4 v10, s[4:5]
	s_waitcnt lgkmcnt(12)
	v_mfma_f32_16x16x32_f16 v[64:67], v[152:155], v[176:179], v[64:67]
	s_waitcnt lgkmcnt(11)
	v_mfma_f32_16x16x32_f16 v[68:71], v[152:155], v[180:183], v[68:71]
	s_waitcnt lgkmcnt(10)
	v_mfma_f32_16x16x32_f16 v[72:75], v[156:159], v[168:171], v[72:75]
	v_mfma_f32_16x16x32_f16 v[76:79], v[156:159], v[172:175], v[76:79]
	v_mfma_f32_16x16x32_f16 v[80:83], v[156:159], v[176:179], v[80:83]
	s_add_u32 m0, s28, 0xe000
	s_nop 0
	global_load_lds_dwordx4 v11, s[4:5]
	v_mfma_f32_16x16x32_f16 v[84:87], v[156:159], v[180:183], v[84:87]
	s_waitcnt lgkmcnt(9)
	v_mfma_f32_16x16x32_f16 v[88:91], v[160:163], v[168:171], v[88:91]
	v_mfma_f32_16x16x32_f16 v[92:95], v[160:163], v[172:175], v[92:95]
	v_mfma_f32_16x16x32_f16 v[96:99], v[160:163], v[176:179], v[96:99]
	v_mfma_f32_16x16x32_f16 v[100:103], v[160:163], v[180:183], v[100:103]
	s_add_u32 m0, s28, 0x10000
	s_nop 0
	global_load_lds_dwordx4 v12, s[4:5]
	s_waitcnt lgkmcnt(8)
	v_mfma_f32_16x16x32_f16 v[104:107], v[164:167], v[168:171], v[104:107]
	v_mfma_f32_16x16x32_f16 v[108:111], v[164:167], v[172:175], v[108:111]
	v_mfma_f32_16x16x32_f16 v[112:115], v[164:167], v[176:179], v[112:115]
	v_mfma_f32_16x16x32_f16 v[116:119], v[164:167], v[180:183], v[116:119]
	s_waitcnt lgkmcnt(7)
	ds_read_b128 v[152:155], v19
	ds_read_b128 v[168:171], v21
	ds_read_b128 v[172:175], v21 offset:2048
	ds_read_b128 v[176:179], v21 offset:4096
	ds_read_b128 v[180:183], v21 offset:6144
	ds_read_b128 v[156:159], v19 offset:2048
	ds_read_b128 v[160:163], v19 offset:4096
	ds_read_b128 v[164:167], v19 offset:6144
	s_waitcnt lgkmcnt(14)
	v_mfma_f32_16x16x32_f16 v[56:59], v[120:123], v[136:139], v[56:59]
	s_waitcnt lgkmcnt(13)
	v_mfma_f32_16x16x32_f16 v[60:63], v[120:123], v[140:143], v[60:63]
	s_add_u32 m0, s28, 0x12000
	s_nop 0
	global_load_lds_dwordx4 v13, s[4:5]
	s_add_u32 s4, s4, s20
	s_addc_u32 s5, s5, 0
	s_waitcnt lgkmcnt(12)
	v_mfma_f32_16x16x32_f16 v[64:67], v[120:123], v[144:147], v[64:67]
	s_waitcnt lgkmcnt(11)
	v_mfma_f32_16x16x32_f16 v[68:71], v[120:123], v[148:151], v[68:71]
	s_waitcnt lgkmcnt(10)
	v_mfma_f32_16x16x32_f16 v[72:75], v[124:127], v[136:139], v[72:75]
	v_mfma_f32_16x16x32_f16 v[76:79], v[124:127], v[140:143], v[76:79]
	v_mfma_f32_16x16x32_f16 v[80:83], v[124:127], v[144:147], v[80:83]
	s_add_u32 m0, s28, 0x14000
	s_nop 0
	global_load_lds_dwordx4 v10, s[6:7]
	v_mfma_f32_16x16x32_f16 v[84:87], v[124:127], v[148:151], v[84:87]
	s_waitcnt lgkmcnt(9)
	v_mfma_f32_16x16x32_f16 v[88:91], v[128:131], v[136:139], v[88:91]
	v_mfma_f32_16x16x32_f16 v[92:95], v[128:131], v[140:143], v[92:95]
	v_mfma_f32_16x16x32_f16 v[96:99], v[128:131], v[144:147], v[96:99]
	v_mfma_f32_16x16x32_f16 v[100:103], v[128:131], v[148:151], v[100:103]
	s_add_u32 m0, s28, 0x16000
	s_nop 0
	global_load_lds_dwordx4 v11, s[6:7]
	s_add_u32 s6, s6, s20
	s_addc_u32 s7, s7, 0
	s_waitcnt lgkmcnt(8)
	v_mfma_f32_16x16x32_f16 v[104:107], v[132:135], v[136:139], v[104:107]
	v_mfma_f32_16x16x32_f16 v[108:111], v[132:135], v[140:143], v[108:111]
	v_mfma_f32_16x16x32_f16 v[112:115], v[132:135], v[144:147], v[112:115]
	v_mfma_f32_16x16x32_f16 v[116:119], v[132:135], v[148:151], v[116:119]
	s_waitcnt vmcnt(6) lgkmcnt(0)
	s_barrier
	s_waitcnt lgkmcnt(7)
	ds_read_b128 v[120:123], v14
	ds_read_b128 v[136:139], v16
	ds_read_b128 v[140:143], v16 offset:2048
	ds_read_b128 v[144:147], v16 offset:4096
	ds_read_b128 v[148:151], v16 offset:6144
	ds_read_b128 v[124:127], v14 offset:2048
	ds_read_b128 v[128:131], v14 offset:4096
	ds_read_b128 v[132:135], v14 offset:6144
	s_waitcnt lgkmcnt(14)
	v_mfma_f32_16x16x32_f16 v[56:59], v[152:155], v[168:171], v[56:59]
	s_waitcnt lgkmcnt(13)
	v_mfma_f32_16x16x32_f16 v[60:63], v[152:155], v[172:175], v[60:63]
	s_add_u32 m0, s28, 0x18000
	s_nop 0
	global_load_lds_dwordx4 v10, s[4:5]
	s_waitcnt lgkmcnt(12)
	v_mfma_f32_16x16x32_f16 v[64:67], v[152:155], v[176:179], v[64:67]
	s_waitcnt lgkmcnt(11)
	v_mfma_f32_16x16x32_f16 v[68:71], v[152:155], v[180:183], v[68:71]
	s_waitcnt lgkmcnt(10)
	v_mfma_f32_16x16x32_f16 v[72:75], v[156:159], v[168:171], v[72:75]
	v_mfma_f32_16x16x32_f16 v[76:79], v[156:159], v[172:175], v[76:79]
	v_mfma_f32_16x16x32_f16 v[80:83], v[156:159], v[176:179], v[80:83]
	s_add_u32 m0, s28, 0x1a000
	s_nop 0
	global_load_lds_dwordx4 v11, s[4:5]
	v_mfma_f32_16x16x32_f16 v[84:87], v[156:159], v[180:183], v[84:87]
	s_waitcnt lgkmcnt(9)
	v_mfma_f32_16x16x32_f16 v[88:91], v[160:163], v[168:171], v[88:91]
	v_mfma_f32_16x16x32_f16 v[92:95], v[160:163], v[172:175], v[92:95]
	v_mfma_f32_16x16x32_f16 v[96:99], v[160:163], v[176:179], v[96:99]
	v_mfma_f32_16x16x32_f16 v[100:103], v[160:163], v[180:183], v[100:103]
	s_add_u32 m0, s28, 0x1c000
	s_nop 0
	global_load_lds_dwordx4 v12, s[4:5]
	s_waitcnt lgkmcnt(8)
	v_mfma_f32_16x16x32_f16 v[104:107], v[164:167], v[168:171], v[104:107]
	v_mfma_f32_16x16x32_f16 v[108:111], v[164:167], v[172:175], v[108:111]
	v_mfma_f32_16x16x32_f16 v[112:115], v[164:167], v[176:179], v[112:115]
	v_mfma_f32_16x16x32_f16 v[116:119], v[164:167], v[180:183], v[116:119]
	s_waitcnt lgkmcnt(7)
	ds_read_b128 v[152:155], v15
	ds_read_b128 v[168:171], v17
	ds_read_b128 v[172:175], v17 offset:2048
	ds_read_b128 v[176:179], v17 offset:4096
	ds_read_b128 v[180:183], v17 offset:6144
	ds_read_b128 v[156:159], v15 offset:2048
	ds_read_b128 v[160:163], v15 offset:4096
	ds_read_b128 v[164:167], v15 offset:6144
	s_waitcnt lgkmcnt(14)
	v_mfma_f32_16x16x32_f16 v[56:59], v[120:123], v[136:139], v[56:59]
	s_waitcnt lgkmcnt(13)
	v_mfma_f32_16x16x32_f16 v[60:63], v[120:123], v[140:143], v[60:63]
	s_add_u32 m0, s28, 0x1e000
	s_nop 0
	global_load_lds_dwordx4 v13, s[4:5]
	s_add_u32 s4, s4, s20
	s_addc_u32 s5, s5, 0
	s_waitcnt lgkmcnt(12)
	v_mfma_f32_16x16x32_f16 v[64:67], v[120:123], v[144:147], v[64:67]
	s_waitcnt lgkmcnt(11)
	v_mfma_f32_16x16x32_f16 v[68:71], v[120:123], v[148:151], v[68:71]
	s_waitcnt lgkmcnt(10)
	v_mfma_f32_16x16x32_f16 v[72:75], v[124:127], v[136:139], v[72:75]
	v_mfma_f32_16x16x32_f16 v[76:79], v[124:127], v[140:143], v[76:79]
	v_mfma_f32_16x16x32_f16 v[80:83], v[124:127], v[144:147], v[80:83]
	s_add_u32 m0, s28, 0x20000
	s_nop 0
	global_load_lds_dwordx4 v10, s[6:7]
	v_mfma_f32_16x16x32_f16 v[84:87], v[124:127], v[148:151], v[84:87]
	s_waitcnt lgkmcnt(9)
	v_mfma_f32_16x16x32_f16 v[88:91], v[128:131], v[136:139], v[88:91]
	v_mfma_f32_16x16x32_f16 v[92:95], v[128:131], v[140:143], v[92:95]
	v_mfma_f32_16x16x32_f16 v[96:99], v[128:131], v[144:147], v[96:99]
	v_mfma_f32_16x16x32_f16 v[100:103], v[128:131], v[148:151], v[100:103]
	s_add_u32 m0, s28, 0x22000
	s_nop 0
	global_load_lds_dwordx4 v11, s[6:7]
	s_add_u32 s6, s6, s20
	s_addc_u32 s7, s7, 0
	s_waitcnt lgkmcnt(8)
	v_mfma_f32_16x16x32_f16 v[104:107], v[132:135], v[136:139], v[104:107]
	v_mfma_f32_16x16x32_f16 v[108:111], v[132:135], v[140:143], v[108:111]
	v_mfma_f32_16x16x32_f16 v[112:115], v[132:135], v[144:147], v[112:115]
	v_mfma_f32_16x16x32_f16 v[116:119], v[132:135], v[148:151], v[116:119]
	s_waitcnt vmcnt(6) lgkmcnt(0)
	s_barrier
	s_waitcnt lgkmcnt(7)
	ds_read_b128 v[120:123], v14 offset:49152
	ds_read_b128 v[136:139], v16 offset:49152
	ds_read_b128 v[140:143], v16 offset:51200
	ds_read_b128 v[144:147], v16 offset:53248
	ds_read_b128 v[148:151], v16 offset:55296
	ds_read_b128 v[124:127], v14 offset:51200
	ds_read_b128 v[128:131], v14 offset:53248
	ds_read_b128 v[132:135], v14 offset:55296
	s_waitcnt lgkmcnt(14)
	v_mfma_f32_16x16x32_f16 v[56:59], v[152:155], v[168:171], v[56:59]
	s_waitcnt lgkmcnt(13)
	v_mfma_f32_16x16x32_f16 v[60:63], v[152:155], v[172:175], v[60:63]
	s_add_u32 m0, s28, 0x0
	s_nop 0
	global_load_lds_dwordx4 v10, s[4:5]
	s_waitcnt lgkmcnt(12)
	v_mfma_f32_16x16x32_f16 v[64:67], v[152:155], v[176:179], v[64:67]
	s_waitcnt lgkmcnt(11)
	v_mfma_f32_16x16x32_f16 v[68:71], v[152:155], v[180:183], v[68:71]
	s_waitcnt lgkmcnt(10)
	v_mfma_f32_16x16x32_f16 v[72:75], v[156:159], v[168:171], v[72:75]
	v_mfma_f32_16x16x32_f16 v[76:79], v[156:159], v[172:175], v[76:79]
	v_mfma_f32_16x16x32_f16 v[80:83], v[156:159], v[176:179], v[80:83]
	s_add_u32 m0, s28, 0x2000
	s_nop 0
	global_load_lds_dwordx4 v11, s[4:5]
	v_mfma_f32_16x16x32_f16 v[84:87], v[156:159], v[180:183], v[84:87]
	s_waitcnt lgkmcnt(9)
	v_mfma_f32_16x16x32_f16 v[88:91], v[160:163], v[168:171], v[88:91]
	v_mfma_f32_16x16x32_f16 v[92:95], v[160:163], v[172:175], v[92:95]
	v_mfma_f32_16x16x32_f16 v[96:99], v[160:163], v[176:179], v[96:99]
	v_mfma_f32_16x16x32_f16 v[100:103], v[160:163], v[180:183], v[100:103]
	s_add_u32 m0, s28, 0x4000
	s_nop 0
	global_load_lds_dwordx4 v12, s[4:5]
	s_waitcnt lgkmcnt(8)
	v_mfma_f32_16x16x32_f16 v[104:107], v[164:167], v[168:171], v[104:107]
	v_mfma_f32_16x16x32_f16 v[108:111], v[164:167], v[172:175], v[108:111]
	v_mfma_f32_16x16x32_f16 v[112:115], v[164:167], v[176:179], v[112:115]
	v_mfma_f32_16x16x32_f16 v[116:119], v[164:167], v[180:183], v[116:119]
	s_waitcnt lgkmcnt(7)
	ds_read_b128 v[152:155], v15 offset:49152
	ds_read_b128 v[168:171], v17 offset:49152
	ds_read_b128 v[172:175], v17 offset:51200
	ds_read_b128 v[176:179], v17 offset:53248
	ds_read_b128 v[180:183], v17 offset:55296
	ds_read_b128 v[156:159], v15 offset:51200
	ds_read_b128 v[160:163], v15 offset:53248
	ds_read_b128 v[164:167], v15 offset:55296
	s_waitcnt lgkmcnt(14)
	v_mfma_f32_16x16x32_f16 v[56:59], v[120:123], v[136:139], v[56:59]
	s_waitcnt lgkmcnt(13)
	v_mfma_f32_16x16x32_f16 v[60:63], v[120:123], v[140:143], v[60:63]
	s_add_u32 m0, s28, 0x6000
	s_nop 0
	global_load_lds_dwordx4 v13, s[4:5]
	s_add_u32 s4, s4, s20
	s_addc_u32 s5, s5, 0
	s_waitcnt lgkmcnt(12)
	v_mfma_f32_16x16x32_f16 v[64:67], v[120:123], v[144:147], v[64:67]
	s_waitcnt lgkmcnt(11)
	v_mfma_f32_16x16x32_f16 v[68:71], v[120:123], v[148:151], v[68:71]
	s_waitcnt lgkmcnt(10)
	v_mfma_f32_16x16x32_f16 v[72:75], v[124:127], v[136:139], v[72:75]
	v_mfma_f32_16x16x32_f16 v[76:79], v[124:127], v[140:143], v[76:79]
	v_mfma_f32_16x16x32_f16 v[80:83], v[124:127], v[144:147], v[80:83]
	s_add_u32 m0, s28, 0x8000
	s_nop 0
	global_load_lds_dwordx4 v10, s[6:7]
	v_mfma_f32_16x16x32_f16 v[84:87], v[124:127], v[148:151], v[84:87]
	s_waitcnt lgkmcnt(9)
	v_mfma_f32_16x16x32_f16 v[88:91], v[128:131], v[136:139], v[88:91]
	v_mfma_f32_16x16x32_f16 v[92:95], v[128:131], v[140:143], v[92:95]
	v_mfma_f32_16x16x32_f16 v[96:99], v[128:131], v[144:147], v[96:99]
	v_mfma_f32_16x16x32_f16 v[100:103], v[128:131], v[148:151], v[100:103]
	s_add_u32 m0, s28, 0xa000
	s_nop 0
	global_load_lds_dwordx4 v11, s[6:7]
	s_add_u32 s6, s6, s20
	s_addc_u32 s7, s7, 0
	s_waitcnt lgkmcnt(8)
	v_mfma_f32_16x16x32_f16 v[104:107], v[132:135], v[136:139], v[104:107]
	v_mfma_f32_16x16x32_f16 v[108:111], v[132:135], v[140:143], v[108:111]
	v_mfma_f32_16x16x32_f16 v[112:115], v[132:135], v[144:147], v[112:115]
	v_mfma_f32_16x16x32_f16 v[116:119], v[132:135], v[148:151], v[116:119]
	s_waitcnt vmcnt(6) lgkmcnt(0)
	s_barrier
	s_waitcnt lgkmcnt(7)
	ds_read_b128 v[120:123], v18
	ds_read_b128 v[136:139], v20
	ds_read_b128 v[140:143], v20 offset:2048
	ds_read_b128 v[144:147], v20 offset:4096
	ds_read_b128 v[148:151], v20 offset:6144
	ds_read_b128 v[124:127], v18 offset:2048
	ds_read_b128 v[128:131], v18 offset:4096
	ds_read_b128 v[132:135], v18 offset:6144
	s_waitcnt lgkmcnt(14)
	v_mfma_f32_16x16x32_f16 v[56:59], v[152:155], v[168:171], v[56:59]
	s_waitcnt lgkmcnt(13)
	v_mfma_f32_16x16x32_f16 v[60:63], v[152:155], v[172:175], v[60:63]
	s_add_u32 m0, s28, 0xc000
	s_nop 0
	global_load_lds_dwordx4 v10, s[4:5]
	s_waitcnt lgkmcnt(12)
	v_mfma_f32_16x16x32_f16 v[64:67], v[152:155], v[176:179], v[64:67]
	s_waitcnt lgkmcnt(11)
	v_mfma_f32_16x16x32_f16 v[68:71], v[152:155], v[180:183], v[68:71]
	s_waitcnt lgkmcnt(10)
	v_mfma_f32_16x16x32_f16 v[72:75], v[156:159], v[168:171], v[72:75]
	v_mfma_f32_16x16x32_f16 v[76:79], v[156:159], v[172:175], v[76:79]
	v_mfma_f32_16x16x32_f16 v[80:83], v[156:159], v[176:179], v[80:83]
	s_add_u32 m0, s28, 0xe000
	s_nop 0
	global_load_lds_dwordx4 v11, s[4:5]
	v_mfma_f32_16x16x32_f16 v[84:87], v[156:159], v[180:183], v[84:87]
	s_waitcnt lgkmcnt(9)
	v_mfma_f32_16x16x32_f16 v[88:91], v[160:163], v[168:171], v[88:91]
	v_mfma_f32_16x16x32_f16 v[92:95], v[160:163], v[172:175], v[92:95]
	v_mfma_f32_16x16x32_f16 v[96:99], v[160:163], v[176:179], v[96:99]
	v_mfma_f32_16x16x32_f16 v[100:103], v[160:163], v[180:183], v[100:103]
	s_add_u32 m0, s28, 0x10000
	s_nop 0
	global_load_lds_dwordx4 v12, s[4:5]
	s_waitcnt lgkmcnt(8)
	v_mfma_f32_16x16x32_f16 v[104:107], v[164:167], v[168:171], v[104:107]
	v_mfma_f32_16x16x32_f16 v[108:111], v[164:167], v[172:175], v[108:111]
	v_mfma_f32_16x16x32_f16 v[112:115], v[164:167], v[176:179], v[112:115]
	v_mfma_f32_16x16x32_f16 v[116:119], v[164:167], v[180:183], v[116:119]
	s_waitcnt lgkmcnt(7)
	ds_read_b128 v[152:155], v19
	ds_read_b128 v[168:171], v21
	ds_read_b128 v[172:175], v21 offset:2048
	ds_read_b128 v[176:179], v21 offset:4096
	ds_read_b128 v[180:183], v21 offset:6144
	ds_read_b128 v[156:159], v19 offset:2048
	ds_read_b128 v[160:163], v19 offset:4096
	ds_read_b128 v[164:167], v19 offset:6144
	s_waitcnt lgkmcnt(14)
	v_mfma_f32_16x16x32_f16 v[56:59], v[120:123], v[136:139], v[56:59]
	s_waitcnt lgkmcnt(13)
	v_mfma_f32_16x16x32_f16 v[60:63], v[120:123], v[140:143], v[60:63]
	s_add_u32 m0, s28, 0x12000
	s_nop 0
	global_load_lds_dwordx4 v13, s[4:5]
	s_add_u32 s4, s4, s20
	s_addc_u32 s5, s5, 0
	s_waitcnt lgkmcnt(12)
	v_mfma_f32_16x16x32_f16 v[64:67], v[120:123], v[144:147], v[64:67]
	s_waitcnt lgkmcnt(11)
	v_mfma_f32_16x16x32_f16 v[68:71], v[120:123], v[148:151], v[68:71]
	s_waitcnt lgkmcnt(10)
	v_mfma_f32_16x16x32_f16 v[72:75], v[124:127], v[136:139], v[72:75]
	v_mfma_f32_16x16x32_f16 v[76:79], v[124:127], v[140:143], v[76:79]
	v_mfma_f32_16x16x32_f16 v[80:83], v[124:127], v[144:147], v[80:83]
	s_add_u32 m0, s28, 0x14000
	s_nop 0
	global_load_lds_dwordx4 v10, s[6:7]
	v_mfma_f32_16x16x32_f16 v[84:87], v[124:127], v[148:151], v[84:87]
	s_waitcnt lgkmcnt(9)
	v_mfma_f32_16x16x32_f16 v[88:91], v[128:131], v[136:139], v[88:91]
	v_mfma_f32_16x16x32_f16 v[92:95], v[128:131], v[140:143], v[92:95]
	v_mfma_f32_16x16x32_f16 v[96:99], v[128:131], v[144:147], v[96:99]
	v_mfma_f32_16x16x32_f16 v[100:103], v[128:131], v[148:151], v[100:103]
	s_add_u32 m0, s28, 0x16000
	s_nop 0
	global_load_lds_dwordx4 v11, s[6:7]
	s_add_u32 s6, s6, s20
	s_addc_u32 s7, s7, 0
	s_waitcnt lgkmcnt(8)
	v_mfma_f32_16x16x32_f16 v[104:107], v[132:135], v[136:139], v[104:107]
	v_mfma_f32_16x16x32_f16 v[108:111], v[132:135], v[140:143], v[108:111]
	v_mfma_f32_16x16x32_f16 v[112:115], v[132:135], v[144:147], v[112:115]
	v_mfma_f32_16x16x32_f16 v[116:119], v[132:135], v[148:151], v[116:119]
	s_waitcnt vmcnt(6) lgkmcnt(0)
	s_barrier
	s_waitcnt lgkmcnt(7)
	ds_read_b128 v[120:123], v14
	ds_read_b128 v[136:139], v16
	ds_read_b128 v[140:143], v16 offset:2048
	ds_read_b128 v[144:147], v16 offset:4096
	ds_read_b128 v[148:151], v16 offset:6144
	ds_read_b128 v[124:127], v14 offset:2048
	ds_read_b128 v[128:131], v14 offset:4096
	ds_read_b128 v[132:135], v14 offset:6144
	s_waitcnt lgkmcnt(14)
	v_mfma_f32_16x16x32_f16 v[56:59], v[152:155], v[168:171], v[56:59]
	s_waitcnt lgkmcnt(13)
	v_mfma_f32_16x16x32_f16 v[60:63], v[152:155], v[172:175], v[60:63]
	s_add_u32 m0, s28, 0x18000
	s_nop 0
	global_load_lds_dwordx4 v10, s[4:5]
	s_waitcnt lgkmcnt(12)
	v_mfma_f32_16x16x32_f16 v[64:67], v[152:155], v[176:179], v[64:67]
	s_waitcnt lgkmcnt(11)
	v_mfma_f32_16x16x32_f16 v[68:71], v[152:155], v[180:183], v[68:71]
	s_waitcnt lgkmcnt(10)
	v_mfma_f32_16x16x32_f16 v[72:75], v[156:159], v[168:171], v[72:75]
	v_mfma_f32_16x16x32_f16 v[76:79], v[156:159], v[172:175], v[76:79]
	v_mfma_f32_16x16x32_f16 v[80:83], v[156:159], v[176:179], v[80:83]
	s_add_u32 m0, s28, 0x1a000
	s_nop 0
	global_load_lds_dwordx4 v11, s[4:5]
	v_mfma_f32_16x16x32_f16 v[84:87], v[156:159], v[180:183], v[84:87]
	s_waitcnt lgkmcnt(9)
	v_mfma_f32_16x16x32_f16 v[88:91], v[160:163], v[168:171], v[88:91]
	v_mfma_f32_16x16x32_f16 v[92:95], v[160:163], v[172:175], v[92:95]
	v_mfma_f32_16x16x32_f16 v[96:99], v[160:163], v[176:179], v[96:99]
	v_mfma_f32_16x16x32_f16 v[100:103], v[160:163], v[180:183], v[100:103]
	s_add_u32 m0, s28, 0x1c000
	s_nop 0
	global_load_lds_dwordx4 v12, s[4:5]
	s_waitcnt lgkmcnt(8)
	v_mfma_f32_16x16x32_f16 v[104:107], v[164:167], v[168:171], v[104:107]
	v_mfma_f32_16x16x32_f16 v[108:111], v[164:167], v[172:175], v[108:111]
	v_mfma_f32_16x16x32_f16 v[112:115], v[164:167], v[176:179], v[112:115]
	v_mfma_f32_16x16x32_f16 v[116:119], v[164:167], v[180:183], v[116:119]
	s_waitcnt lgkmcnt(7)
	ds_read_b128 v[152:155], v15
	ds_read_b128 v[168:171], v17
	ds_read_b128 v[172:175], v17 offset:2048
	ds_read_b128 v[176:179], v17 offset:4096
	ds_read_b128 v[180:183], v17 offset:6144
	ds_read_b128 v[156:159], v15 offset:2048
	ds_read_b128 v[160:163], v15 offset:4096
	ds_read_b128 v[164:167], v15 offset:6144
	s_waitcnt lgkmcnt(14)
	v_mfma_f32_16x16x32_f16 v[56:59], v[120:123], v[136:139], v[56:59]
	s_waitcnt lgkmcnt(13)
	v_mfma_f32_16x16x32_f16 v[60:63], v[120:123], v[140:143], v[60:63]
	s_add_u32 m0, s28, 0x1e000
	s_nop 0
	global_load_lds_dwordx4 v13, s[4:5]
	s_add_u32 s4, s4, s20
	s_addc_u32 s5, s5, 0
	s_waitcnt lgkmcnt(12)
	v_mfma_f32_16x16x32_f16 v[64:67], v[120:123], v[144:147], v[64:67]
	s_waitcnt lgkmcnt(11)
	v_mfma_f32_16x16x32_f16 v[68:71], v[120:123], v[148:151], v[68:71]
	s_waitcnt lgkmcnt(10)
	v_mfma_f32_16x16x32_f16 v[72:75], v[124:127], v[136:139], v[72:75]
	v_mfma_f32_16x16x32_f16 v[76:79], v[124:127], v[140:143], v[76:79]
	v_mfma_f32_16x16x32_f16 v[80:83], v[124:127], v[144:147], v[80:83]
	s_add_u32 m0, s28, 0x20000
	s_nop 0
	global_load_lds_dwordx4 v10, s[6:7]
	v_mfma_f32_16x16x32_f16 v[84:87], v[124:127], v[148:151], v[84:87]
	s_waitcnt lgkmcnt(9)
	v_mfma_f32_16x16x32_f16 v[88:91], v[128:131], v[136:139], v[88:91]
	v_mfma_f32_16x16x32_f16 v[92:95], v[128:131], v[140:143], v[92:95]
	v_mfma_f32_16x16x32_f16 v[96:99], v[128:131], v[144:147], v[96:99]
	v_mfma_f32_16x16x32_f16 v[100:103], v[128:131], v[148:151], v[100:103]
	s_add_u32 m0, s28, 0x22000
	s_nop 0
	global_load_lds_dwordx4 v11, s[6:7]
	s_add_u32 s6, s6, s20
	s_addc_u32 s7, s7, 0
	s_waitcnt lgkmcnt(8)
	v_mfma_f32_16x16x32_f16 v[104:107], v[132:135], v[136:139], v[104:107]
	v_mfma_f32_16x16x32_f16 v[108:111], v[132:135], v[140:143], v[108:111]
	v_mfma_f32_16x16x32_f16 v[112:115], v[132:135], v[144:147], v[112:115]
	v_mfma_f32_16x16x32_f16 v[116:119], v[132:135], v[148:151], v[116:119]
	s_waitcnt vmcnt(6) lgkmcnt(0)
	s_barrier
	s_waitcnt lgkmcnt(7)
	ds_read_b128 v[120:123], v14 offset:49152
	ds_read_b128 v[136:139], v16 offset:49152
	ds_read_b128 v[140:143], v16 offset:51200
	ds_read_b128 v[144:147], v16 offset:53248
	ds_read_b128 v[148:151], v16 offset:55296
	ds_read_b128 v[124:127], v14 offset:51200
	ds_read_b128 v[128:131], v14 offset:53248
	ds_read_b128 v[132:135], v14 offset:55296
	s_waitcnt lgkmcnt(14)
	v_mfma_f32_16x16x32_f16 v[56:59], v[152:155], v[168:171], v[56:59]
	s_waitcnt lgkmcnt(13)
	v_mfma_f32_16x16x32_f16 v[60:63], v[152:155], v[172:175], v[60:63]
	s_add_u32 m0, s28, 0x0
	s_nop 0
	global_load_lds_dwordx4 v10, s[4:5]
	s_waitcnt lgkmcnt(12)
	v_mfma_f32_16x16x32_f16 v[64:67], v[152:155], v[176:179], v[64:67]
	s_waitcnt lgkmcnt(11)
	v_mfma_f32_16x16x32_f16 v[68:71], v[152:155], v[180:183], v[68:71]
	s_waitcnt lgkmcnt(10)
	v_mfma_f32_16x16x32_f16 v[72:75], v[156:159], v[168:171], v[72:75]
	v_mfma_f32_16x16x32_f16 v[76:79], v[156:159], v[172:175], v[76:79]
	v_mfma_f32_16x16x32_f16 v[80:83], v[156:159], v[176:179], v[80:83]
	s_add_u32 m0, s28, 0x2000
	s_nop 0
	global_load_lds_dwordx4 v11, s[4:5]
	v_mfma_f32_16x16x32_f16 v[84:87], v[156:159], v[180:183], v[84:87]
	s_waitcnt lgkmcnt(9)
	v_mfma_f32_16x16x32_f16 v[88:91], v[160:163], v[168:171], v[88:91]
	v_mfma_f32_16x16x32_f16 v[92:95], v[160:163], v[172:175], v[92:95]
	v_mfma_f32_16x16x32_f16 v[96:99], v[160:163], v[176:179], v[96:99]
	v_mfma_f32_16x16x32_f16 v[100:103], v[160:163], v[180:183], v[100:103]
	s_add_u32 m0, s28, 0x4000
	s_nop 0
	global_load_lds_dwordx4 v12, s[4:5]
	s_waitcnt lgkmcnt(8)
	v_mfma_f32_16x16x32_f16 v[104:107], v[164:167], v[168:171], v[104:107]
	v_mfma_f32_16x16x32_f16 v[108:111], v[164:167], v[172:175], v[108:111]
	v_mfma_f32_16x16x32_f16 v[112:115], v[164:167], v[176:179], v[112:115]
	v_mfma_f32_16x16x32_f16 v[116:119], v[164:167], v[180:183], v[116:119]
	s_waitcnt lgkmcnt(7)
	ds_read_b128 v[152:155], v15 offset:49152
	ds_read_b128 v[168:171], v17 offset:49152
	ds_read_b128 v[172:175], v17 offset:51200
	ds_read_b128 v[176:179], v17 offset:53248
	ds_read_b128 v[180:183], v17 offset:55296
	ds_read_b128 v[156:159], v15 offset:51200
	ds_read_b128 v[160:163], v15 offset:53248
	ds_read_b128 v[164:167], v15 offset:55296
	s_waitcnt lgkmcnt(14)
	v_mfma_f32_16x16x32_f16 v[56:59], v[120:123], v[136:139], v[56:59]
	s_waitcnt lgkmcnt(13)
	v_mfma_f32_16x16x32_f16 v[60:63], v[120:123], v[140:143], v[60:63]
	s_add_u32 m0, s28, 0x6000
	s_nop 0
	global_load_lds_dwordx4 v13, s[4:5]
	s_add_u32 s4, s4, s20
	s_addc_u32 s5, s5, 0
	s_waitcnt lgkmcnt(12)
	v_mfma_f32_16x16x32_f16 v[64:67], v[120:123], v[144:147], v[64:67]
	s_waitcnt lgkmcnt(11)
	v_mfma_f32_16x16x32_f16 v[68:71], v[120:123], v[148:151], v[68:71]
	s_waitcnt lgkmcnt(10)
	v_mfma_f32_16x16x32_f16 v[72:75], v[124:127], v[136:139], v[72:75]
	v_mfma_f32_16x16x32_f16 v[76:79], v[124:127], v[140:143], v[76:79]
	v_mfma_f32_16x16x32_f16 v[80:83], v[124:127], v[144:147], v[80:83]
	s_add_u32 m0, s28, 0x8000
	s_nop 0
	global_load_lds_dwordx4 v10, s[6:7]
	v_mfma_f32_16x16x32_f16 v[84:87], v[124:127], v[148:151], v[84:87]
	s_waitcnt lgkmcnt(9)
	v_mfma_f32_16x16x32_f16 v[88:91], v[128:131], v[136:139], v[88:91]
	v_mfma_f32_16x16x32_f16 v[92:95], v[128:131], v[140:143], v[92:95]
	v_mfma_f32_16x16x32_f16 v[96:99], v[128:131], v[144:147], v[96:99]
	v_mfma_f32_16x16x32_f16 v[100:103], v[128:131], v[148:151], v[100:103]
	s_add_u32 m0, s28, 0xa000
	s_nop 0
	global_load_lds_dwordx4 v11, s[6:7]
	s_add_u32 s6, s6, s20
	s_addc_u32 s7, s7, 0
	s_waitcnt lgkmcnt(8)
	v_mfma_f32_16x16x32_f16 v[104:107], v[132:135], v[136:139], v[104:107]
	v_mfma_f32_16x16x32_f16 v[108:111], v[132:135], v[140:143], v[108:111]
	v_mfma_f32_16x16x32_f16 v[112:115], v[132:135], v[144:147], v[112:115]
	v_mfma_f32_16x16x32_f16 v[116:119], v[132:135], v[148:151], v[116:119]
	s_waitcnt vmcnt(6) lgkmcnt(0)
	s_barrier
	s_waitcnt lgkmcnt(7)
	ds_read_b128 v[120:123], v18
	ds_read_b128 v[136:139], v20
	ds_read_b128 v[140:143], v20 offset:2048
	ds_read_b128 v[144:147], v20 offset:4096
	ds_read_b128 v[148:151], v20 offset:6144
	ds_read_b128 v[124:127], v18 offset:2048
	ds_read_b128 v[128:131], v18 offset:4096
	ds_read_b128 v[132:135], v18 offset:6144
	s_waitcnt lgkmcnt(14)
	v_mfma_f32_16x16x32_f16 v[56:59], v[152:155], v[168:171], v[56:59]
	s_waitcnt lgkmcnt(13)
	v_mfma_f32_16x16x32_f16 v[60:63], v[152:155], v[172:175], v[60:63]
	s_add_u32 m0, s28, 0xc000
	s_nop 0
	global_load_lds_dwordx4 v10, s[4:5]
	s_waitcnt lgkmcnt(12)
	v_mfma_f32_16x16x32_f16 v[64:67], v[152:155], v[176:179], v[64:67]
	s_waitcnt lgkmcnt(11)
	v_mfma_f32_16x16x32_f16 v[68:71], v[152:155], v[180:183], v[68:71]
	s_waitcnt lgkmcnt(10)
	v_mfma_f32_16x16x32_f16 v[72:75], v[156:159], v[168:171], v[72:75]
	v_mfma_f32_16x16x32_f16 v[76:79], v[156:159], v[172:175], v[76:79]
	v_mfma_f32_16x16x32_f16 v[80:83], v[156:159], v[176:179], v[80:83]
	s_add_u32 m0, s28, 0xe000
	s_nop 0
	global_load_lds_dwordx4 v11, s[4:5]
	v_mfma_f32_16x16x32_f16 v[84:87], v[156:159], v[180:183], v[84:87]
	s_waitcnt lgkmcnt(9)
	v_mfma_f32_16x16x32_f16 v[88:91], v[160:163], v[168:171], v[88:91]
	v_mfma_f32_16x16x32_f16 v[92:95], v[160:163], v[172:175], v[92:95]
	v_mfma_f32_16x16x32_f16 v[96:99], v[160:163], v[176:179], v[96:99]
	v_mfma_f32_16x16x32_f16 v[100:103], v[160:163], v[180:183], v[100:103]
	s_add_u32 m0, s28, 0x10000
	s_nop 0
	global_load_lds_dwordx4 v12, s[4:5]
	s_waitcnt lgkmcnt(8)
	v_mfma_f32_16x16x32_f16 v[104:107], v[164:167], v[168:171], v[104:107]
	v_mfma_f32_16x16x32_f16 v[108:111], v[164:167], v[172:175], v[108:111]
	v_mfma_f32_16x16x32_f16 v[112:115], v[164:167], v[176:179], v[112:115]
	v_mfma_f32_16x16x32_f16 v[116:119], v[164:167], v[180:183], v[116:119]
	s_waitcnt lgkmcnt(7)
	ds_read_b128 v[152:155], v19
	ds_read_b128 v[168:171], v21
	ds_read_b128 v[172:175], v21 offset:2048
	ds_read_b128 v[176:179], v21 offset:4096
	ds_read_b128 v[180:183], v21 offset:6144
	ds_read_b128 v[156:159], v19 offset:2048
	ds_read_b128 v[160:163], v19 offset:4096
	ds_read_b128 v[164:167], v19 offset:6144
	s_waitcnt lgkmcnt(14)
	v_mfma_f32_16x16x32_f16 v[56:59], v[120:123], v[136:139], v[56:59]
	s_waitcnt lgkmcnt(13)
	v_mfma_f32_16x16x32_f16 v[60:63], v[120:123], v[140:143], v[60:63]
	s_add_u32 m0, s28, 0x12000
	s_nop 0
	global_load_lds_dwordx4 v13, s[4:5]
	s_add_u32 s4, s4, s20
	s_addc_u32 s5, s5, 0
	s_waitcnt lgkmcnt(12)
	v_mfma_f32_16x16x32_f16 v[64:67], v[120:123], v[144:147], v[64:67]
	s_waitcnt lgkmcnt(11)
	v_mfma_f32_16x16x32_f16 v[68:71], v[120:123], v[148:151], v[68:71]
	s_waitcnt lgkmcnt(10)
	v_mfma_f32_16x16x32_f16 v[72:75], v[124:127], v[136:139], v[72:75]
	v_mfma_f32_16x16x32_f16 v[76:79], v[124:127], v[140:143], v[76:79]
	v_mfma_f32_16x16x32_f16 v[80:83], v[124:127], v[144:147], v[80:83]
	s_add_u32 m0, s28, 0x14000
	s_nop 0
	global_load_lds_dwordx4 v10, s[6:7]
	v_mfma_f32_16x16x32_f16 v[84:87], v[124:127], v[148:151], v[84:87]
	s_waitcnt lgkmcnt(9)
	v_mfma_f32_16x16x32_f16 v[88:91], v[128:131], v[136:139], v[88:91]
	v_mfma_f32_16x16x32_f16 v[92:95], v[128:131], v[140:143], v[92:95]
	v_mfma_f32_16x16x32_f16 v[96:99], v[128:131], v[144:147], v[96:99]
	v_mfma_f32_16x16x32_f16 v[100:103], v[128:131], v[148:151], v[100:103]
	s_add_u32 m0, s28, 0x16000
	s_nop 0
	global_load_lds_dwordx4 v11, s[6:7]
	s_add_u32 s6, s6, s20
	s_addc_u32 s7, s7, 0
	s_waitcnt lgkmcnt(8)
	v_mfma_f32_16x16x32_f16 v[104:107], v[132:135], v[136:139], v[104:107]
	v_mfma_f32_16x16x32_f16 v[108:111], v[132:135], v[140:143], v[108:111]
	v_mfma_f32_16x16x32_f16 v[112:115], v[132:135], v[144:147], v[112:115]
	v_mfma_f32_16x16x32_f16 v[116:119], v[132:135], v[148:151], v[116:119]
	s_waitcnt vmcnt(6) lgkmcnt(0)
	s_barrier
	s_waitcnt lgkmcnt(7)
	ds_read_b128 v[120:123], v14
	ds_read_b128 v[136:139], v16
	ds_read_b128 v[140:143], v16 offset:2048
	ds_read_b128 v[144:147], v16 offset:4096
	ds_read_b128 v[148:151], v16 offset:6144
	ds_read_b128 v[124:127], v14 offset:2048
	ds_read_b128 v[128:131], v14 offset:4096
	ds_read_b128 v[132:135], v14 offset:6144
	s_waitcnt lgkmcnt(14)
	v_mfma_f32_16x16x32_f16 v[56:59], v[152:155], v[168:171], v[56:59]
	s_waitcnt lgkmcnt(13)
	v_mfma_f32_16x16x32_f16 v[60:63], v[152:155], v[172:175], v[60:63]
	s_add_u32 m0, s28, 0x18000
	s_nop 0
	global_load_lds_dwordx4 v10, s[4:5]
	s_waitcnt lgkmcnt(12)
	v_mfma_f32_16x16x32_f16 v[64:67], v[152:155], v[176:179], v[64:67]
	s_waitcnt lgkmcnt(11)
	v_mfma_f32_16x16x32_f16 v[68:71], v[152:155], v[180:183], v[68:71]
	s_waitcnt lgkmcnt(10)
	v_mfma_f32_16x16x32_f16 v[72:75], v[156:159], v[168:171], v[72:75]
	v_mfma_f32_16x16x32_f16 v[76:79], v[156:159], v[172:175], v[76:79]
	v_mfma_f32_16x16x32_f16 v[80:83], v[156:159], v[176:179], v[80:83]
	s_add_u32 m0, s28, 0x1a000
	s_nop 0
	global_load_lds_dwordx4 v11, s[4:5]
	v_mfma_f32_16x16x32_f16 v[84:87], v[156:159], v[180:183], v[84:87]
	s_waitcnt lgkmcnt(9)
	v_mfma_f32_16x16x32_f16 v[88:91], v[160:163], v[168:171], v[88:91]
	v_mfma_f32_16x16x32_f16 v[92:95], v[160:163], v[172:175], v[92:95]
	v_mfma_f32_16x16x32_f16 v[96:99], v[160:163], v[176:179], v[96:99]
	v_mfma_f32_16x16x32_f16 v[100:103], v[160:163], v[180:183], v[100:103]
	s_add_u32 m0, s28, 0x1c000
	s_nop 0
	global_load_lds_dwordx4 v12, s[4:5]
	s_waitcnt lgkmcnt(8)
	v_mfma_f32_16x16x32_f16 v[104:107], v[164:167], v[168:171], v[104:107]
	v_mfma_f32_16x16x32_f16 v[108:111], v[164:167], v[172:175], v[108:111]
	v_mfma_f32_16x16x32_f16 v[112:115], v[164:167], v[176:179], v[112:115]
	v_mfma_f32_16x16x32_f16 v[116:119], v[164:167], v[180:183], v[116:119]
	s_waitcnt lgkmcnt(7)
	ds_read_b128 v[152:155], v15
	ds_read_b128 v[168:171], v17
	ds_read_b128 v[172:175], v17 offset:2048
	ds_read_b128 v[176:179], v17 offset:4096
	ds_read_b128 v[180:183], v17 offset:6144
	ds_read_b128 v[156:159], v15 offset:2048
	ds_read_b128 v[160:163], v15 offset:4096
	ds_read_b128 v[164:167], v15 offset:6144
	s_waitcnt lgkmcnt(14)
	v_mfma_f32_16x16x32_f16 v[56:59], v[120:123], v[136:139], v[56:59]
	s_waitcnt lgkmcnt(13)
	v_mfma_f32_16x16x32_f16 v[60:63], v[120:123], v[140:143], v[60:63]
	s_add_u32 m0, s28, 0x1e000
	s_nop 0
	global_load_lds_dwordx4 v13, s[4:5]
	s_add_u32 s4, s4, s20
	s_addc_u32 s5, s5, 0
	s_waitcnt lgkmcnt(12)
	v_mfma_f32_16x16x32_f16 v[64:67], v[120:123], v[144:147], v[64:67]
	s_waitcnt lgkmcnt(11)
	v_mfma_f32_16x16x32_f16 v[68:71], v[120:123], v[148:151], v[68:71]
	s_waitcnt lgkmcnt(10)
	v_mfma_f32_16x16x32_f16 v[72:75], v[124:127], v[136:139], v[72:75]
	v_mfma_f32_16x16x32_f16 v[76:79], v[124:127], v[140:143], v[76:79]
	v_mfma_f32_16x16x32_f16 v[80:83], v[124:127], v[144:147], v[80:83]
	s_add_u32 m0, s28, 0x20000
	s_nop 0
	global_load_lds_dwordx4 v10, s[6:7]
	v_mfma_f32_16x16x32_f16 v[84:87], v[124:127], v[148:151], v[84:87]
	s_waitcnt lgkmcnt(9)
	v_mfma_f32_16x16x32_f16 v[88:91], v[128:131], v[136:139], v[88:91]
	v_mfma_f32_16x16x32_f16 v[92:95], v[128:131], v[140:143], v[92:95]
	v_mfma_f32_16x16x32_f16 v[96:99], v[128:131], v[144:147], v[96:99]
	v_mfma_f32_16x16x32_f16 v[100:103], v[128:131], v[148:151], v[100:103]
	s_add_u32 m0, s28, 0x22000
	s_nop 0
	global_load_lds_dwordx4 v11, s[6:7]
	s_add_u32 s6, s6, s20
	s_addc_u32 s7, s7, 0
	s_waitcnt lgkmcnt(8)
	v_mfma_f32_16x16x32_f16 v[104:107], v[132:135], v[136:139], v[104:107]
	v_mfma_f32_16x16x32_f16 v[108:111], v[132:135], v[140:143], v[108:111]
	v_mfma_f32_16x16x32_f16 v[112:115], v[132:135], v[144:147], v[112:115]
	v_mfma_f32_16x16x32_f16 v[116:119], v[132:135], v[148:151], v[116:119]
	s_waitcnt vmcnt(6) lgkmcnt(0)
	s_barrier
	s_waitcnt lgkmcnt(7)
	ds_read_b128 v[120:123], v14 offset:49152
	ds_read_b128 v[136:139], v16 offset:49152
	ds_read_b128 v[140:143], v16 offset:51200
	ds_read_b128 v[144:147], v16 offset:53248
	ds_read_b128 v[148:151], v16 offset:55296
	ds_read_b128 v[124:127], v14 offset:51200
	ds_read_b128 v[128:131], v14 offset:53248
	ds_read_b128 v[132:135], v14 offset:55296
	s_waitcnt lgkmcnt(14)
	v_mfma_f32_16x16x32_f16 v[56:59], v[152:155], v[168:171], v[56:59]
	s_waitcnt lgkmcnt(13)
	v_mfma_f32_16x16x32_f16 v[60:63], v[152:155], v[172:175], v[60:63]
	s_add_u32 m0, s28, 0x0
	s_nop 0
	global_load_lds_dwordx4 v10, s[4:5]
	s_waitcnt lgkmcnt(12)
	v_mfma_f32_16x16x32_f16 v[64:67], v[152:155], v[176:179], v[64:67]
	s_waitcnt lgkmcnt(11)
	v_mfma_f32_16x16x32_f16 v[68:71], v[152:155], v[180:183], v[68:71]
	s_waitcnt lgkmcnt(10)
	v_mfma_f32_16x16x32_f16 v[72:75], v[156:159], v[168:171], v[72:75]
	v_mfma_f32_16x16x32_f16 v[76:79], v[156:159], v[172:175], v[76:79]
	v_mfma_f32_16x16x32_f16 v[80:83], v[156:159], v[176:179], v[80:83]
	s_add_u32 m0, s28, 0x2000
	s_nop 0
	global_load_lds_dwordx4 v11, s[4:5]
	v_mfma_f32_16x16x32_f16 v[84:87], v[156:159], v[180:183], v[84:87]
	s_waitcnt lgkmcnt(9)
	v_mfma_f32_16x16x32_f16 v[88:91], v[160:163], v[168:171], v[88:91]
	v_mfma_f32_16x16x32_f16 v[92:95], v[160:163], v[172:175], v[92:95]
	v_mfma_f32_16x16x32_f16 v[96:99], v[160:163], v[176:179], v[96:99]
	v_mfma_f32_16x16x32_f16 v[100:103], v[160:163], v[180:183], v[100:103]
	s_add_u32 m0, s28, 0x4000
	s_nop 0
	global_load_lds_dwordx4 v12, s[4:5]
	s_waitcnt lgkmcnt(8)
	v_mfma_f32_16x16x32_f16 v[104:107], v[164:167], v[168:171], v[104:107]
	v_mfma_f32_16x16x32_f16 v[108:111], v[164:167], v[172:175], v[108:111]
	v_mfma_f32_16x16x32_f16 v[112:115], v[164:167], v[176:179], v[112:115]
	v_mfma_f32_16x16x32_f16 v[116:119], v[164:167], v[180:183], v[116:119]
	s_waitcnt lgkmcnt(7)
	ds_read_b128 v[152:155], v15 offset:49152
	ds_read_b128 v[168:171], v17 offset:49152
	ds_read_b128 v[172:175], v17 offset:51200
	ds_read_b128 v[176:179], v17 offset:53248
	ds_read_b128 v[180:183], v17 offset:55296
	ds_read_b128 v[156:159], v15 offset:51200
	ds_read_b128 v[160:163], v15 offset:53248
	ds_read_b128 v[164:167], v15 offset:55296
	s_waitcnt lgkmcnt(14)
	v_mfma_f32_16x16x32_f16 v[56:59], v[120:123], v[136:139], v[56:59]
	s_waitcnt lgkmcnt(13)
	v_mfma_f32_16x16x32_f16 v[60:63], v[120:123], v[140:143], v[60:63]
	s_add_u32 m0, s28, 0x6000
	s_nop 0
	global_load_lds_dwordx4 v13, s[4:5]
	s_add_u32 s4, s4, s20
	s_addc_u32 s5, s5, 0
	s_waitcnt lgkmcnt(12)
	v_mfma_f32_16x16x32_f16 v[64:67], v[120:123], v[144:147], v[64:67]
	s_waitcnt lgkmcnt(11)
	v_mfma_f32_16x16x32_f16 v[68:71], v[120:123], v[148:151], v[68:71]
	s_waitcnt lgkmcnt(10)
	v_mfma_f32_16x16x32_f16 v[72:75], v[124:127], v[136:139], v[72:75]
	v_mfma_f32_16x16x32_f16 v[76:79], v[124:127], v[140:143], v[76:79]
	v_mfma_f32_16x16x32_f16 v[80:83], v[124:127], v[144:147], v[80:83]
	s_add_u32 m0, s28, 0x8000
	s_nop 0
	global_load_lds_dwordx4 v10, s[6:7]
	v_mfma_f32_16x16x32_f16 v[84:87], v[124:127], v[148:151], v[84:87]
	s_waitcnt lgkmcnt(9)
	v_mfma_f32_16x16x32_f16 v[88:91], v[128:131], v[136:139], v[88:91]
	v_mfma_f32_16x16x32_f16 v[92:95], v[128:131], v[140:143], v[92:95]
	v_mfma_f32_16x16x32_f16 v[96:99], v[128:131], v[144:147], v[96:99]
	v_mfma_f32_16x16x32_f16 v[100:103], v[128:131], v[148:151], v[100:103]
	s_add_u32 m0, s28, 0xa000
	s_nop 0
	global_load_lds_dwordx4 v11, s[6:7]
	s_add_u32 s6, s6, s20
	s_addc_u32 s7, s7, 0
	s_waitcnt lgkmcnt(8)
	v_mfma_f32_16x16x32_f16 v[104:107], v[132:135], v[136:139], v[104:107]
	v_mfma_f32_16x16x32_f16 v[108:111], v[132:135], v[140:143], v[108:111]
	v_mfma_f32_16x16x32_f16 v[112:115], v[132:135], v[144:147], v[112:115]
	v_mfma_f32_16x16x32_f16 v[116:119], v[132:135], v[148:151], v[116:119]
	s_waitcnt vmcnt(6) lgkmcnt(0)
	s_barrier
	s_waitcnt lgkmcnt(7)
	ds_read_b128 v[120:123], v18
	ds_read_b128 v[136:139], v20
	ds_read_b128 v[140:143], v20 offset:2048
	ds_read_b128 v[144:147], v20 offset:4096
	ds_read_b128 v[148:151], v20 offset:6144
	ds_read_b128 v[124:127], v18 offset:2048
	ds_read_b128 v[128:131], v18 offset:4096
	ds_read_b128 v[132:135], v18 offset:6144
	s_waitcnt lgkmcnt(14)
	v_mfma_f32_16x16x32_f16 v[56:59], v[152:155], v[168:171], v[56:59]
	s_waitcnt lgkmcnt(13)
	v_mfma_f32_16x16x32_f16 v[60:63], v[152:155], v[172:175], v[60:63]
	s_add_u32 m0, s28, 0xc000
	s_nop 0
	global_load_lds_dwordx4 v10, s[4:5]
	s_waitcnt lgkmcnt(12)
	v_mfma_f32_16x16x32_f16 v[64:67], v[152:155], v[176:179], v[64:67]
	s_waitcnt lgkmcnt(11)
	v_mfma_f32_16x16x32_f16 v[68:71], v[152:155], v[180:183], v[68:71]
	s_waitcnt lgkmcnt(10)
	v_mfma_f32_16x16x32_f16 v[72:75], v[156:159], v[168:171], v[72:75]
	v_mfma_f32_16x16x32_f16 v[76:79], v[156:159], v[172:175], v[76:79]
	v_mfma_f32_16x16x32_f16 v[80:83], v[156:159], v[176:179], v[80:83]
	s_add_u32 m0, s28, 0xe000
	s_nop 0
	global_load_lds_dwordx4 v11, s[4:5]
	v_mfma_f32_16x16x32_f16 v[84:87], v[156:159], v[180:183], v[84:87]
	s_waitcnt lgkmcnt(9)
	v_mfma_f32_16x16x32_f16 v[88:91], v[160:163], v[168:171], v[88:91]
	v_mfma_f32_16x16x32_f16 v[92:95], v[160:163], v[172:175], v[92:95]
	v_mfma_f32_16x16x32_f16 v[96:99], v[160:163], v[176:179], v[96:99]
	v_mfma_f32_16x16x32_f16 v[100:103], v[160:163], v[180:183], v[100:103]
	s_add_u32 m0, s28, 0x10000
	s_nop 0
	global_load_lds_dwordx4 v12, s[4:5]
	s_waitcnt lgkmcnt(8)
	v_mfma_f32_16x16x32_f16 v[104:107], v[164:167], v[168:171], v[104:107]
	v_mfma_f32_16x16x32_f16 v[108:111], v[164:167], v[172:175], v[108:111]
	v_mfma_f32_16x16x32_f16 v[112:115], v[164:167], v[176:179], v[112:115]
	v_mfma_f32_16x16x32_f16 v[116:119], v[164:167], v[180:183], v[116:119]
	s_waitcnt lgkmcnt(7)
	ds_read_b128 v[152:155], v19
	ds_read_b128 v[168:171], v21
	ds_read_b128 v[172:175], v21 offset:2048
	ds_read_b128 v[176:179], v21 offset:4096
	ds_read_b128 v[180:183], v21 offset:6144
	ds_read_b128 v[156:159], v19 offset:2048
	ds_read_b128 v[160:163], v19 offset:4096
	ds_read_b128 v[164:167], v19 offset:6144
	s_waitcnt lgkmcnt(14)
	v_mfma_f32_16x16x32_f16 v[56:59], v[120:123], v[136:139], v[56:59]
	s_waitcnt lgkmcnt(13)
	v_mfma_f32_16x16x32_f16 v[60:63], v[120:123], v[140:143], v[60:63]
	s_add_u32 m0, s28, 0x12000
	s_nop 0
	global_load_lds_dwordx4 v13, s[4:5]
	s_add_u32 s4, s4, s20
	s_addc_u32 s5, s5, 0
	s_waitcnt lgkmcnt(12)
	v_mfma_f32_16x16x32_f16 v[64:67], v[120:123], v[144:147], v[64:67]
	s_waitcnt lgkmcnt(11)
	v_mfma_f32_16x16x32_f16 v[68:71], v[120:123], v[148:151], v[68:71]
	s_waitcnt lgkmcnt(10)
	v_mfma_f32_16x16x32_f16 v[72:75], v[124:127], v[136:139], v[72:75]
	v_mfma_f32_16x16x32_f16 v[76:79], v[124:127], v[140:143], v[76:79]
	v_mfma_f32_16x16x32_f16 v[80:83], v[124:127], v[144:147], v[80:83]
	s_add_u32 m0, s28, 0x14000
	s_nop 0
	global_load_lds_dwordx4 v10, s[6:7]
	v_mfma_f32_16x16x32_f16 v[84:87], v[124:127], v[148:151], v[84:87]
	s_waitcnt lgkmcnt(9)
	v_mfma_f32_16x16x32_f16 v[88:91], v[128:131], v[136:139], v[88:91]
	v_mfma_f32_16x16x32_f16 v[92:95], v[128:131], v[140:143], v[92:95]
	v_mfma_f32_16x16x32_f16 v[96:99], v[128:131], v[144:147], v[96:99]
	v_mfma_f32_16x16x32_f16 v[100:103], v[128:131], v[148:151], v[100:103]
	s_add_u32 m0, s28, 0x16000
	s_nop 0
	global_load_lds_dwordx4 v11, s[6:7]
	s_add_u32 s6, s6, s20
	s_addc_u32 s7, s7, 0
	s_waitcnt lgkmcnt(8)
	v_mfma_f32_16x16x32_f16 v[104:107], v[132:135], v[136:139], v[104:107]
	v_mfma_f32_16x16x32_f16 v[108:111], v[132:135], v[140:143], v[108:111]
	v_mfma_f32_16x16x32_f16 v[112:115], v[132:135], v[144:147], v[112:115]
	v_mfma_f32_16x16x32_f16 v[116:119], v[132:135], v[148:151], v[116:119]
	s_waitcnt vmcnt(6) lgkmcnt(0)
	s_barrier
	s_waitcnt lgkmcnt(7)
	ds_read_b128 v[120:123], v14
	ds_read_b128 v[136:139], v16
	ds_read_b128 v[140:143], v16 offset:2048
	ds_read_b128 v[144:147], v16 offset:4096
	ds_read_b128 v[148:151], v16 offset:6144
	ds_read_b128 v[124:127], v14 offset:2048
	ds_read_b128 v[128:131], v14 offset:4096
	ds_read_b128 v[132:135], v14 offset:6144
	s_waitcnt lgkmcnt(14)
	v_mfma_f32_16x16x32_f16 v[56:59], v[152:155], v[168:171], v[56:59]
	s_waitcnt lgkmcnt(13)
	v_mfma_f32_16x16x32_f16 v[60:63], v[152:155], v[172:175], v[60:63]
	s_add_u32 m0, s28, 0x18000
	s_nop 0
	global_load_lds_dwordx4 v10, s[4:5]
	s_waitcnt lgkmcnt(12)
	v_mfma_f32_16x16x32_f16 v[64:67], v[152:155], v[176:179], v[64:67]
	s_waitcnt lgkmcnt(11)
	v_mfma_f32_16x16x32_f16 v[68:71], v[152:155], v[180:183], v[68:71]
	s_waitcnt lgkmcnt(10)
	v_mfma_f32_16x16x32_f16 v[72:75], v[156:159], v[168:171], v[72:75]
	v_mfma_f32_16x16x32_f16 v[76:79], v[156:159], v[172:175], v[76:79]
	v_mfma_f32_16x16x32_f16 v[80:83], v[156:159], v[176:179], v[80:83]
	s_add_u32 m0, s28, 0x1a000
	s_nop 0
	global_load_lds_dwordx4 v11, s[4:5]
	v_mfma_f32_16x16x32_f16 v[84:87], v[156:159], v[180:183], v[84:87]
	s_waitcnt lgkmcnt(9)
	v_mfma_f32_16x16x32_f16 v[88:91], v[160:163], v[168:171], v[88:91]
	v_mfma_f32_16x16x32_f16 v[92:95], v[160:163], v[172:175], v[92:95]
	v_mfma_f32_16x16x32_f16 v[96:99], v[160:163], v[176:179], v[96:99]
	v_mfma_f32_16x16x32_f16 v[100:103], v[160:163], v[180:183], v[100:103]
	s_add_u32 m0, s28, 0x1c000
	s_nop 0
	global_load_lds_dwordx4 v12, s[4:5]
	s_waitcnt lgkmcnt(8)
	v_mfma_f32_16x16x32_f16 v[104:107], v[164:167], v[168:171], v[104:107]
	v_mfma_f32_16x16x32_f16 v[108:111], v[164:167], v[172:175], v[108:111]
	v_mfma_f32_16x16x32_f16 v[112:115], v[164:167], v[176:179], v[112:115]
	v_mfma_f32_16x16x32_f16 v[116:119], v[164:167], v[180:183], v[116:119]
	s_waitcnt lgkmcnt(7)
	ds_read_b128 v[152:155], v15
	ds_read_b128 v[168:171], v17
	ds_read_b128 v[172:175], v17 offset:2048
	ds_read_b128 v[176:179], v17 offset:4096
	ds_read_b128 v[180:183], v17 offset:6144
	ds_read_b128 v[156:159], v15 offset:2048
	ds_read_b128 v[160:163], v15 offset:4096
	ds_read_b128 v[164:167], v15 offset:6144
	s_waitcnt lgkmcnt(14)
	v_mfma_f32_16x16x32_f16 v[56:59], v[120:123], v[136:139], v[56:59]
	s_waitcnt lgkmcnt(13)
	v_mfma_f32_16x16x32_f16 v[60:63], v[120:123], v[140:143], v[60:63]
	s_add_u32 m0, s28, 0x1e000
	s_nop 0
	global_load_lds_dwordx4 v13, s[4:5]
	s_add_u32 s4, s4, s20
	s_addc_u32 s5, s5, 0
	s_waitcnt lgkmcnt(12)
	v_mfma_f32_16x16x32_f16 v[64:67], v[120:123], v[144:147], v[64:67]
	s_waitcnt lgkmcnt(11)
	v_mfma_f32_16x16x32_f16 v[68:71], v[120:123], v[148:151], v[68:71]
	s_waitcnt lgkmcnt(10)
	v_mfma_f32_16x16x32_f16 v[72:75], v[124:127], v[136:139], v[72:75]
	v_mfma_f32_16x16x32_f16 v[76:79], v[124:127], v[140:143], v[76:79]
	v_mfma_f32_16x16x32_f16 v[80:83], v[124:127], v[144:147], v[80:83]
	s_add_u32 m0, s28, 0x20000
	s_nop 0
	global_load_lds_dwordx4 v10, s[6:7]
	v_mfma_f32_16x16x32_f16 v[84:87], v[124:127], v[148:151], v[84:87]
	s_waitcnt lgkmcnt(9)
	v_mfma_f32_16x16x32_f16 v[88:91], v[128:131], v[136:139], v[88:91]
	v_mfma_f32_16x16x32_f16 v[92:95], v[128:131], v[140:143], v[92:95]
	v_mfma_f32_16x16x32_f16 v[96:99], v[128:131], v[144:147], v[96:99]
	v_mfma_f32_16x16x32_f16 v[100:103], v[128:131], v[148:151], v[100:103]
	s_add_u32 m0, s28, 0x22000
	s_nop 0
	global_load_lds_dwordx4 v11, s[6:7]
	s_add_u32 s6, s6, s20
	s_addc_u32 s7, s7, 0
	s_waitcnt lgkmcnt(8)
	v_mfma_f32_16x16x32_f16 v[104:107], v[132:135], v[136:139], v[104:107]
	v_mfma_f32_16x16x32_f16 v[108:111], v[132:135], v[140:143], v[108:111]
	v_mfma_f32_16x16x32_f16 v[112:115], v[132:135], v[144:147], v[112:115]
	v_mfma_f32_16x16x32_f16 v[116:119], v[132:135], v[148:151], v[116:119]
	s_waitcnt vmcnt(6) lgkmcnt(0)
	s_barrier
	s_waitcnt lgkmcnt(7)
	ds_read_b128 v[120:123], v14 offset:49152
	ds_read_b128 v[136:139], v16 offset:49152
	ds_read_b128 v[140:143], v16 offset:51200
	ds_read_b128 v[144:147], v16 offset:53248
	ds_read_b128 v[148:151], v16 offset:55296
	ds_read_b128 v[124:127], v14 offset:51200
	ds_read_b128 v[128:131], v14 offset:53248
	ds_read_b128 v[132:135], v14 offset:55296
	s_waitcnt lgkmcnt(14)
	v_mfma_f32_16x16x32_f16 v[56:59], v[152:155], v[168:171], v[56:59]
	s_waitcnt lgkmcnt(13)
	v_mfma_f32_16x16x32_f16 v[60:63], v[152:155], v[172:175], v[60:63]
	s_add_u32 m0, s28, 0x0
	s_nop 0
	global_load_lds_dwordx4 v10, s[4:5]
	s_waitcnt lgkmcnt(12)
	v_mfma_f32_16x16x32_f16 v[64:67], v[152:155], v[176:179], v[64:67]
	s_waitcnt lgkmcnt(11)
	v_mfma_f32_16x16x32_f16 v[68:71], v[152:155], v[180:183], v[68:71]
	s_waitcnt lgkmcnt(10)
	v_mfma_f32_16x16x32_f16 v[72:75], v[156:159], v[168:171], v[72:75]
	v_mfma_f32_16x16x32_f16 v[76:79], v[156:159], v[172:175], v[76:79]
	v_mfma_f32_16x16x32_f16 v[80:83], v[156:159], v[176:179], v[80:83]
	s_add_u32 m0, s28, 0x2000
	s_nop 0
	global_load_lds_dwordx4 v11, s[4:5]
	v_mfma_f32_16x16x32_f16 v[84:87], v[156:159], v[180:183], v[84:87]
	s_waitcnt lgkmcnt(9)
	v_mfma_f32_16x16x32_f16 v[88:91], v[160:163], v[168:171], v[88:91]
	v_mfma_f32_16x16x32_f16 v[92:95], v[160:163], v[172:175], v[92:95]
	v_mfma_f32_16x16x32_f16 v[96:99], v[160:163], v[176:179], v[96:99]
	v_mfma_f32_16x16x32_f16 v[100:103], v[160:163], v[180:183], v[100:103]
	s_add_u32 m0, s28, 0x4000
	s_nop 0
	global_load_lds_dwordx4 v12, s[4:5]
	s_waitcnt lgkmcnt(8)
	v_mfma_f32_16x16x32_f16 v[104:107], v[164:167], v[168:171], v[104:107]
	v_mfma_f32_16x16x32_f16 v[108:111], v[164:167], v[172:175], v[108:111]
	v_mfma_f32_16x16x32_f16 v[112:115], v[164:167], v[176:179], v[112:115]
	v_mfma_f32_16x16x32_f16 v[116:119], v[164:167], v[180:183], v[116:119]
	s_waitcnt lgkmcnt(7)
	ds_read_b128 v[152:155], v15 offset:49152
	ds_read_b128 v[168:171], v17 offset:49152
	ds_read_b128 v[172:175], v17 offset:51200
	ds_read_b128 v[176:179], v17 offset:53248
	ds_read_b128 v[180:183], v17 offset:55296
	ds_read_b128 v[156:159], v15 offset:51200
	ds_read_b128 v[160:163], v15 offset:53248
	ds_read_b128 v[164:167], v15 offset:55296
	s_waitcnt lgkmcnt(14)
	v_mfma_f32_16x16x32_f16 v[56:59], v[120:123], v[136:139], v[56:59]
	s_waitcnt lgkmcnt(13)
	v_mfma_f32_16x16x32_f16 v[60:63], v[120:123], v[140:143], v[60:63]
	s_add_u32 m0, s28, 0x6000
	s_nop 0
	global_load_lds_dwordx4 v13, s[4:5]
	s_add_u32 s4, s4, s20
	s_addc_u32 s5, s5, 0
	s_waitcnt lgkmcnt(12)
	v_mfma_f32_16x16x32_f16 v[64:67], v[120:123], v[144:147], v[64:67]
	s_waitcnt lgkmcnt(11)
	v_mfma_f32_16x16x32_f16 v[68:71], v[120:123], v[148:151], v[68:71]
	s_waitcnt lgkmcnt(10)
	v_mfma_f32_16x16x32_f16 v[72:75], v[124:127], v[136:139], v[72:75]
	v_mfma_f32_16x16x32_f16 v[76:79], v[124:127], v[140:143], v[76:79]
	v_mfma_f32_16x16x32_f16 v[80:83], v[124:127], v[144:147], v[80:83]
	s_add_u32 m0, s28, 0x8000
	s_nop 0
	global_load_lds_dwordx4 v10, s[6:7]
	v_mfma_f32_16x16x32_f16 v[84:87], v[124:127], v[148:151], v[84:87]
	s_waitcnt lgkmcnt(9)
	v_mfma_f32_16x16x32_f16 v[88:91], v[128:131], v[136:139], v[88:91]
	v_mfma_f32_16x16x32_f16 v[92:95], v[128:131], v[140:143], v[92:95]
	v_mfma_f32_16x16x32_f16 v[96:99], v[128:131], v[144:147], v[96:99]
	v_mfma_f32_16x16x32_f16 v[100:103], v[128:131], v[148:151], v[100:103]
	s_add_u32 m0, s28, 0xa000
	s_nop 0
	global_load_lds_dwordx4 v11, s[6:7]
	s_add_u32 s6, s6, s20
	s_addc_u32 s7, s7, 0
	s_waitcnt lgkmcnt(8)
	v_mfma_f32_16x16x32_f16 v[104:107], v[132:135], v[136:139], v[104:107]
	v_mfma_f32_16x16x32_f16 v[108:111], v[132:135], v[140:143], v[108:111]
	v_mfma_f32_16x16x32_f16 v[112:115], v[132:135], v[144:147], v[112:115]
	v_mfma_f32_16x16x32_f16 v[116:119], v[132:135], v[148:151], v[116:119]
	s_waitcnt vmcnt(6) lgkmcnt(0)
	s_barrier
	s_waitcnt lgkmcnt(7)
	ds_read_b128 v[120:123], v18
	ds_read_b128 v[136:139], v20
	ds_read_b128 v[140:143], v20 offset:2048
	ds_read_b128 v[144:147], v20 offset:4096
	ds_read_b128 v[148:151], v20 offset:6144
	ds_read_b128 v[124:127], v18 offset:2048
	ds_read_b128 v[128:131], v18 offset:4096
	ds_read_b128 v[132:135], v18 offset:6144
	s_waitcnt lgkmcnt(14)
	v_mfma_f32_16x16x32_f16 v[56:59], v[152:155], v[168:171], v[56:59]
	s_waitcnt lgkmcnt(13)
	v_mfma_f32_16x16x32_f16 v[60:63], v[152:155], v[172:175], v[60:63]
	s_waitcnt lgkmcnt(12)
	v_mfma_f32_16x16x32_f16 v[64:67], v[152:155], v[176:179], v[64:67]
	s_waitcnt lgkmcnt(11)
	v_mfma_f32_16x16x32_f16 v[68:71], v[152:155], v[180:183], v[68:71]
	s_waitcnt lgkmcnt(10)
	v_mfma_f32_16x16x32_f16 v[72:75], v[156:159], v[168:171], v[72:75]
	v_mfma_f32_16x16x32_f16 v[76:79], v[156:159], v[172:175], v[76:79]
	v_mfma_f32_16x16x32_f16 v[80:83], v[156:159], v[176:179], v[80:83]
	v_mfma_f32_16x16x32_f16 v[84:87], v[156:159], v[180:183], v[84:87]
	s_waitcnt lgkmcnt(9)
	v_mfma_f32_16x16x32_f16 v[88:91], v[160:163], v[168:171], v[88:91]
	v_mfma_f32_16x16x32_f16 v[92:95], v[160:163], v[172:175], v[92:95]
	v_mfma_f32_16x16x32_f16 v[96:99], v[160:163], v[176:179], v[96:99]
	v_mfma_f32_16x16x32_f16 v[100:103], v[160:163], v[180:183], v[100:103]
	s_waitcnt lgkmcnt(8)
	v_mfma_f32_16x16x32_f16 v[104:107], v[164:167], v[168:171], v[104:107]
	v_mfma_f32_16x16x32_f16 v[108:111], v[164:167], v[172:175], v[108:111]
	v_mfma_f32_16x16x32_f16 v[112:115], v[164:167], v[176:179], v[112:115]
	v_mfma_f32_16x16x32_f16 v[116:119], v[164:167], v[180:183], v[116:119]
	s_waitcnt lgkmcnt(7)
	ds_read_b128 v[152:155], v19
	ds_read_b128 v[168:171], v21
	ds_read_b128 v[172:175], v21 offset:2048
	ds_read_b128 v[176:179], v21 offset:4096
	ds_read_b128 v[180:183], v21 offset:6144
	ds_read_b128 v[156:159], v19 offset:2048
	ds_read_b128 v[160:163], v19 offset:4096
	ds_read_b128 v[164:167], v19 offset:6144
	s_waitcnt lgkmcnt(14)
	v_mfma_f32_16x16x32_f16 v[56:59], v[120:123], v[136:139], v[56:59]
	s_waitcnt lgkmcnt(13)
	v_mfma_f32_16x16x32_f16 v[60:63], v[120:123], v[140:143], v[60:63]
	s_waitcnt lgkmcnt(12)
	v_mfma_f32_16x16x32_f16 v[64:67], v[120:123], v[144:147], v[64:67]
	s_waitcnt lgkmcnt(11)
	v_mfma_f32_16x16x32_f16 v[68:71], v[120:123], v[148:151], v[68:71]
	s_waitcnt lgkmcnt(10)
	v_mfma_f32_16x16x32_f16 v[72:75], v[124:127], v[136:139], v[72:75]
	v_mfma_f32_16x16x32_f16 v[76:79], v[124:127], v[140:143], v[76:79]
	v_mfma_f32_16x16x32_f16 v[80:83], v[124:127], v[144:147], v[80:83]
	v_mfma_f32_16x16x32_f16 v[84:87], v[124:127], v[148:151], v[84:87]
	s_waitcnt lgkmcnt(9)
	v_mfma_f32_16x16x32_f16 v[88:91], v[128:131], v[136:139], v[88:91]
	v_mfma_f32_16x16x32_f16 v[92:95], v[128:131], v[140:143], v[92:95]
	v_mfma_f32_16x16x32_f16 v[96:99], v[128:131], v[144:147], v[96:99]
	v_mfma_f32_16x16x32_f16 v[100:103], v[128:131], v[148:151], v[100:103]
	s_waitcnt lgkmcnt(8)
	v_mfma_f32_16x16x32_f16 v[104:107], v[132:135], v[136:139], v[104:107]
	v_mfma_f32_16x16x32_f16 v[108:111], v[132:135], v[140:143], v[108:111]
	v_mfma_f32_16x16x32_f16 v[112:115], v[132:135], v[144:147], v[112:115]
	v_mfma_f32_16x16x32_f16 v[116:119], v[132:135], v[148:151], v[116:119]
	s_waitcnt vmcnt(0) lgkmcnt(0)
	s_barrier
	s_waitcnt lgkmcnt(7)
	ds_read_b128 v[120:123], v14
	ds_read_b128 v[136:139], v16
	ds_read_b128 v[140:143], v16 offset:2048
	ds_read_b128 v[144:147], v16 offset:4096
	ds_read_b128 v[148:151], v16 offset:6144
	ds_read_b128 v[124:127], v14 offset:2048
	ds_read_b128 v[128:131], v14 offset:4096
	ds_read_b128 v[132:135], v14 offset:6144
	s_waitcnt lgkmcnt(14)
	v_mfma_f32_16x16x32_f16 v[56:59], v[152:155], v[168:171], v[56:59]
	s_waitcnt lgkmcnt(13)
	v_mfma_f32_16x16x32_f16 v[60:63], v[152:155], v[172:175], v[60:63]
	s_waitcnt lgkmcnt(12)
	v_mfma_f32_16x16x32_f16 v[64:67], v[152:155], v[176:179], v[64:67]
	s_waitcnt lgkmcnt(11)
	v_mfma_f32_16x16x32_f16 v[68:71], v[152:155], v[180:183], v[68:71]
	s_waitcnt lgkmcnt(10)
	v_mfma_f32_16x16x32_f16 v[72:75], v[156:159], v[168:171], v[72:75]
	v_mfma_f32_16x16x32_f16 v[76:79], v[156:159], v[172:175], v[76:79]
	v_mfma_f32_16x16x32_f16 v[80:83], v[156:159], v[176:179], v[80:83]
	v_mfma_f32_16x16x32_f16 v[84:87], v[156:159], v[180:183], v[84:87]
	s_waitcnt lgkmcnt(9)
	v_mfma_f32_16x16x32_f16 v[88:91], v[160:163], v[168:171], v[88:91]
	v_mfma_f32_16x16x32_f16 v[92:95], v[160:163], v[172:175], v[92:95]
	v_mfma_f32_16x16x32_f16 v[96:99], v[160:163], v[176:179], v[96:99]
	v_mfma_f32_16x16x32_f16 v[100:103], v[160:163], v[180:183], v[100:103]
	s_waitcnt lgkmcnt(8)
	v_mfma_f32_16x16x32_f16 v[104:107], v[164:167], v[168:171], v[104:107]
	v_mfma_f32_16x16x32_f16 v[108:111], v[164:167], v[172:175], v[108:111]
	v_mfma_f32_16x16x32_f16 v[112:115], v[164:167], v[176:179], v[112:115]
	v_mfma_f32_16x16x32_f16 v[116:119], v[164:167], v[180:183], v[116:119]
	s_waitcnt lgkmcnt(7)
	ds_read_b128 v[152:155], v15
	ds_read_b128 v[168:171], v17
	ds_read_b128 v[172:175], v17 offset:2048
	ds_read_b128 v[176:179], v17 offset:4096
	ds_read_b128 v[180:183], v17 offset:6144
	ds_read_b128 v[156:159], v15 offset:2048
	ds_read_b128 v[160:163], v15 offset:4096
	ds_read_b128 v[164:167], v15 offset:6144
	s_waitcnt lgkmcnt(14)
	v_mfma_f32_16x16x32_f16 v[56:59], v[120:123], v[136:139], v[56:59]
	s_waitcnt lgkmcnt(13)
	v_mfma_f32_16x16x32_f16 v[60:63], v[120:123], v[140:143], v[60:63]
	s_waitcnt lgkmcnt(12)
	v_mfma_f32_16x16x32_f16 v[64:67], v[120:123], v[144:147], v[64:67]
	s_waitcnt lgkmcnt(11)
	v_mfma_f32_16x16x32_f16 v[68:71], v[120:123], v[148:151], v[68:71]
	s_waitcnt lgkmcnt(10)
	v_mfma_f32_16x16x32_f16 v[72:75], v[124:127], v[136:139], v[72:75]
	v_mfma_f32_16x16x32_f16 v[76:79], v[124:127], v[140:143], v[76:79]
	v_mfma_f32_16x16x32_f16 v[80:83], v[124:127], v[144:147], v[80:83]
	v_mfma_f32_16x16x32_f16 v[84:87], v[124:127], v[148:151], v[84:87]
	s_waitcnt lgkmcnt(9)
	v_mfma_f32_16x16x32_f16 v[88:91], v[128:131], v[136:139], v[88:91]
	v_mfma_f32_16x16x32_f16 v[92:95], v[128:131], v[140:143], v[92:95]
	v_mfma_f32_16x16x32_f16 v[96:99], v[128:131], v[144:147], v[96:99]
	v_mfma_f32_16x16x32_f16 v[100:103], v[128:131], v[148:151], v[100:103]
	s_waitcnt lgkmcnt(8)
	v_mfma_f32_16x16x32_f16 v[104:107], v[132:135], v[136:139], v[104:107]
	v_mfma_f32_16x16x32_f16 v[108:111], v[132:135], v[140:143], v[108:111]
	v_mfma_f32_16x16x32_f16 v[112:115], v[132:135], v[144:147], v[112:115]
	v_mfma_f32_16x16x32_f16 v[116:119], v[132:135], v[148:151], v[116:119]
	s_waitcnt lgkmcnt(6)
	v_mfma_f32_16x16x32_f16 v[56:59], v[152:155], v[168:171], v[56:59]
	s_waitcnt lgkmcnt(5)
	v_mfma_f32_16x16x32_f16 v[60:63], v[152:155], v[172:175], v[60:63]
	s_waitcnt lgkmcnt(4)
	v_mfma_f32_16x16x32_f16 v[64:67], v[152:155], v[176:179], v[64:67]
	s_waitcnt lgkmcnt(3)
	v_mfma_f32_16x16x32_f16 v[68:71], v[152:155], v[180:183], v[68:71]
	s_waitcnt lgkmcnt(2)
	v_mfma_f32_16x16x32_f16 v[72:75], v[156:159], v[168:171], v[72:75]
	v_mfma_f32_16x16x32_f16 v[76:79], v[156:159], v[172:175], v[76:79]
	v_mfma_f32_16x16x32_f16 v[80:83], v[156:159], v[176:179], v[80:83]
	v_mfma_f32_16x16x32_f16 v[84:87], v[156:159], v[180:183], v[84:87]
	s_waitcnt lgkmcnt(1)
	v_mfma_f32_16x16x32_f16 v[88:91], v[160:163], v[168:171], v[88:91]
	v_mfma_f32_16x16x32_f16 v[92:95], v[160:163], v[172:175], v[92:95]
	v_mfma_f32_16x16x32_f16 v[96:99], v[160:163], v[176:179], v[96:99]
	v_mfma_f32_16x16x32_f16 v[100:103], v[160:163], v[180:183], v[100:103]
	s_waitcnt lgkmcnt(0)
	v_mfma_f32_16x16x32_f16 v[104:107], v[164:167], v[168:171], v[104:107]
	v_mfma_f32_16x16x32_f16 v[108:111], v[164:167], v[172:175], v[108:111]
	v_mfma_f32_16x16x32_f16 v[112:115], v[164:167], v[176:179], v[112:115]
	v_mfma_f32_16x16x32_f16 v[116:119], v[164:167], v[180:183], v[116:119]
	s_nop 7
	s_nop 1
	v_add_f32_e32 v56, v56, v24
	v_add_f32_e32 v57, v57, v24
	v_add_f32_e32 v58, v58, v24
	v_add_f32_e32 v59, v59, v24
	v_cvt_pk_f16_f32 v56, v56, v57
	v_cvt_pk_f16_f32 v57, v58, v59
	global_store_dwordx2 v22, v[56:57], s[22:23] offset:0
	v_add_f32_e32 v60, v60, v25
	v_add_f32_e32 v61, v61, v25
	v_add_f32_e32 v62, v62, v25
	v_add_f32_e32 v63, v63, v25
	v_cvt_pk_f16_f32 v60, v60, v61
	v_cvt_pk_f16_f32 v61, v62, v63
	global_store_dwordx2 v22, v[60:61], s[22:23] offset:256
	v_add_f32_e32 v64, v64, v26
	v_add_f32_e32 v65, v65, v26
	v_add_f32_e32 v66, v66, v26
	v_add_f32_e32 v67, v67, v26
	v_cvt_pk_f16_f32 v64, v64, v65
	v_cvt_pk_f16_f32 v65, v66, v67
	global_store_dwordx2 v22, v[64:65], s[22:23] offset:1024
	v_add_f32_e32 v68, v68, v27
	v_add_f32_e32 v69, v69, v27
	v_add_f32_e32 v70, v70, v27
	v_add_f32_e32 v71, v71, v27
	v_cvt_pk_f16_f32 v68, v68, v69
	v_cvt_pk_f16_f32 v69, v70, v71
	global_store_dwordx2 v22, v[68:69], s[22:23] offset:1280
	v_add_f32_e32 v72, v72, v24
	v_add_f32_e32 v73, v73, v24
	v_add_f32_e32 v74, v74, v24
	v_add_f32_e32 v75, v75, v24
	v_cvt_pk_f16_f32 v72, v72, v73
	v_cvt_pk_f16_f32 v73, v74, v75
	global_store_dwordx2 v22, v[72:73], s[22:23] offset:2048
	v_add_f32_e32 v76, v76, v25
	v_add_f32_e32 v77, v77, v25
	v_add_f32_e32 v78, v78, v25
	v_add_f32_e32 v79, v79, v25
	v_cvt_pk_f16_f32 v76, v76, v77
	v_cvt_pk_f16_f32 v77, v78, v79
	global_store_dwordx2 v22, v[76:77], s[22:23] offset:2304
	v_add_f32_e32 v80, v80, v26
	v_add_f32_e32 v81, v81, v26
	v_add_f32_e32 v82, v82, v26
	v_add_f32_e32 v83, v83, v26
	v_cvt_pk_f16_f32 v80, v80, v81
	v_cvt_pk_f16_f32 v81, v82, v83
	global_store_dwordx2 v22, v[80:81], s[22:23] offset:3072
	v_add_f32_e32 v84, v84, v27
	v_add_f32_e32 v85, v85, v27
	v_add_f32_e32 v86, v86, v27
	v_add_f32_e32 v87, v87, v27
	v_cvt_pk_f16_f32 v84, v84, v85
	v_cvt_pk_f16_f32 v85, v86, v87
	global_store_dwordx2 v22, v[84:85], s[22:23] offset:3328
	v_add_f32_e32 v88, v88, v24
	v_add_f32_e32 v89, v89, v24
	v_add_f32_e32 v90, v90, v24
	v_add_f32_e32 v91, v91, v24
	v_cvt_pk_f16_f32 v88, v88, v89
	v_cvt_pk_f16_f32 v89, v90, v91
	global_store_dwordx2 v23, v[88:89], s[22:23] offset:0
	v_add_f32_e32 v92, v92, v25
	v_add_f32_e32 v93, v93, v25
	v_add_f32_e32 v94, v94, v25
	v_add_f32_e32 v95, v95, v25
	v_cvt_pk_f16_f32 v92, v92, v93
	v_cvt_pk_f16_f32 v93, v94, v95
	global_store_dwordx2 v23, v[92:93], s[22:23] offset:256
	v_add_f32_e32 v96, v96, v26
	v_add_f32_e32 v97, v97, v26
	v_add_f32_e32 v98, v98, v26
	v_add_f32_e32 v99, v99, v26
	v_cvt_pk_f16_f32 v96, v96, v97
	v_cvt_pk_f16_f32 v97, v98, v99
	global_store_dwordx2 v23, v[96:97], s[22:23] offset:1024
	v_add_f32_e32 v100, v100, v27
	v_add_f32_e32 v101, v101, v27
	v_add_f32_e32 v102, v102, v27
	v_add_f32_e32 v103, v103, v27
	v_cvt_pk_f16_f32 v100, v100, v101
	v_cvt_pk_f16_f32 v101, v102, v103
	global_store_dwordx2 v23, v[100:101], s[22:23] offset:1280
	v_add_f32_e32 v104, v104, v24
	v_add_f32_e32 v105, v105, v24
	v_add_f32_e32 v106, v106, v24
	v_add_f32_e32 v107, v107, v24
	v_cvt_pk_f16_f32 v104, v104, v105
	v_cvt_pk_f16_f32 v105, v106, v107
	global_store_dwordx2 v23, v[104:105], s[22:23] offset:2048
	v_add_f32_e32 v108, v108, v25
	v_add_f32_e32 v109, v109, v25
	v_add_f32_e32 v110, v110, v25
	v_add_f32_e32 v111, v111, v25
	v_cvt_pk_f16_f32 v108, v108, v109
	v_cvt_pk_f16_f32 v109, v110, v111
	global_store_dwordx2 v23, v[108:109], s[22:23] offset:2304
	v_add_f32_e32 v112, v112, v26
	v_add_f32_e32 v113, v113, v26
	v_add_f32_e32 v114, v114, v26
	v_add_f32_e32 v115, v115, v26
	v_cvt_pk_f16_f32 v112, v112, v113
	v_cvt_pk_f16_f32 v113, v114, v115
	global_store_dwordx2 v23, v[112:113], s[22:23] offset:3072
	v_add_f32_e32 v116, v116, v27
	v_add_f32_e32 v117, v117, v27
	v_add_f32_e32 v118, v118, v27
	v_add_f32_e32 v119, v119, v27
	v_cvt_pk_f16_f32 v116, v116, v117
	v_cvt_pk_f16_f32 v117, v118, v119
	global_store_dwordx2 v23, v[116:117], s[22:23] offset:3328
	s_endpgm
